# GEMM K-loops: s_setprio 1 issued before the segment barrier instead of after it, on top of v144
# baseline (speedup 1.0000x reference)
.LBB0_143:
	ds_read_b128 v[148:151], v142
	ds_read_b128 v[152:155], v142 offset:1024
	ds_read_b128 v[156:159], v142 offset:2048
	ds_read_b128 v[160:163], v142 offset:3072
	ds_read_b128 v[164:167], v143
	ds_read_b128 v[174:177], v143 offset:1024
	ds_read_b128 v[178:181], v143 offset:2048
	ds_read_b128 v[182:185], v143 offset:3072
	s_add_u32 s40, s22, 0x100
	s_addc_u32 s41, s23, 0
	s_cmp_eq_u32 s82, 12
	s_cselect_b32 s58, s33, s40
	s_cselect_b32 s59, s13, s41
	s_cselect_b32 s56, s79, s80
	s_cselect_b32 s57, s15, s81
	s_add_u32 s54, s58, 0x80
	s_addc_u32 s55, s59, 0
	ds_read_b128 v[186:189], v144
	ds_read_b128 v[190:193], v144 offset:1024
	ds_read_b128 v[194:197], v144 offset:2048
	ds_read_b128 v[198:201], v144 offset:3072
	ds_read_b128 v[202:205], v144 offset:4096
	ds_read_b128 v[206:209], v144 offset:5120
	ds_read_b128 v[210:213], v144 offset:6144
	ds_read_b128 v[214:217], v144 offset:7168
	s_add_u32 s22, s22, 0x40080
	s_addc_u32 s23, s23, 0
	s_mov_b32 s83, m0
	s_mov_b32 m0, s67
	s_nop 2
	global_load_lds_dwordx4 v136, s[22:23]
	s_mov_b32 m0, s83
	s_nop 0
	s_mov_b32 s83, m0
	s_mov_b32 m0, s76
	s_nop 2
	global_load_lds_dwordx4 v138, s[22:23]
	s_mov_b32 m0, s83
	s_waitcnt vmcnt(8)
	s_waitcnt lgkmcnt(0)
	s_setprio 1
	s_barrier
	v_mfma_f32_16x16x32_bf16 v[126:129], v[148:151], v[186:189], v[126:129]
	v_mfma_f32_16x16x32_bf16 v[122:125], v[156:159], v[186:189], v[122:125]
	v_mfma_f32_16x16x32_bf16 v[110:113], v[148:151], v[194:197], v[110:113]
	v_mfma_f32_16x16x32_bf16 v[106:109], v[156:159], v[194:197], v[106:109]
	v_mfma_f32_16x16x32_bf16 v[94:97], v[148:151], v[202:205], v[94:97]
	v_mfma_f32_16x16x32_bf16 v[90:93], v[156:159], v[202:205], v[90:93]
	v_mfma_f32_16x16x32_bf16 v[78:81], v[148:151], v[210:213], v[78:81]
	v_mfma_f32_16x16x32_bf16 v[74:77], v[156:159], v[210:213], v[74:77]
	v_mfma_f32_16x16x32_bf16 v[126:129], v[152:155], v[190:193], v[126:129]
	v_mfma_f32_16x16x32_bf16 v[122:125], v[160:163], v[190:193], v[122:125]
	v_mfma_f32_16x16x32_bf16 v[110:113], v[152:155], v[198:201], v[110:113]
	v_mfma_f32_16x16x32_bf16 v[106:109], v[160:163], v[198:201], v[106:109]
	v_mfma_f32_16x16x32_bf16 v[94:97], v[152:155], v[206:209], v[94:97]
	v_mfma_f32_16x16x32_bf16 v[90:93], v[160:163], v[206:209], v[90:93]
	v_mfma_f32_16x16x32_bf16 v[78:81], v[152:155], v[214:217], v[78:81]
	v_mfma_f32_16x16x32_bf16 v[74:77], v[160:163], v[214:217], v[74:77]
	v_mfma_f32_16x16x32_bf16 v[118:121], v[164:167], v[186:189], v[118:121]
	v_mfma_f32_16x16x32_bf16 v[114:117], v[178:181], v[186:189], v[114:117]
	v_mfma_f32_16x16x32_bf16 v[102:105], v[164:167], v[194:197], v[102:105]
	v_mfma_f32_16x16x32_bf16 v[98:101], v[178:181], v[194:197], v[98:101]
	v_mfma_f32_16x16x32_bf16 v[86:89], v[164:167], v[202:205], v[86:89]
	v_mfma_f32_16x16x32_bf16 v[82:85], v[178:181], v[202:205], v[82:85]
	v_mfma_f32_16x16x32_bf16 v[70:73], v[164:167], v[210:213], v[70:73]
	v_mfma_f32_16x16x32_bf16 v[66:69], v[178:181], v[210:213], v[66:69]
	v_mfma_f32_16x16x32_bf16 v[118:121], v[174:177], v[190:193], v[118:121]
	v_mfma_f32_16x16x32_bf16 v[114:117], v[182:185], v[190:193], v[114:117]
	v_mfma_f32_16x16x32_bf16 v[102:105], v[174:177], v[198:201], v[102:105]
	v_mfma_f32_16x16x32_bf16 v[98:101], v[182:185], v[198:201], v[98:101]
	v_mfma_f32_16x16x32_bf16 v[86:89], v[174:177], v[206:209], v[86:89]
	v_mfma_f32_16x16x32_bf16 v[82:85], v[182:185], v[206:209], v[82:85]
	v_mfma_f32_16x16x32_bf16 v[70:73], v[174:177], v[214:217], v[70:73]
	v_mfma_f32_16x16x32_bf16 v[66:69], v[182:185], v[214:217], v[66:69]
	s_setprio 0
	s_barrier
	ds_read_b128 v[186:189], v144 offset:16384
	ds_read_b128 v[190:193], v144 offset:17408
	ds_read_b128 v[194:197], v144 offset:18432
	ds_read_b128 v[198:201], v144 offset:19456
	ds_read_b128 v[202:205], v144 offset:20480
	ds_read_b128 v[206:209], v144 offset:21504
	ds_read_b128 v[210:213], v144 offset:22528
	ds_read_b128 v[214:217], v144 offset:23552
	s_mov_b32 s22, m0
	s_mov_b32 m0, s30
	s_nop 2
	global_load_lds_dwordx4 v137, s[56:57]
	s_mov_b32 m0, s22
	s_nop 0
	s_mov_b32 s22, m0
	s_mov_b32 m0, s31
	s_nop 2
	global_load_lds_dwordx4 v139, s[56:57]
	s_mov_b32 m0, s22
	s_add_u32 s22, s56, 0x40000
	s_addc_u32 s23, s57, 0
	s_mov_b32 s83, m0
	s_mov_b32 m0, s34
	s_nop 2
	global_load_lds_dwordx4 v137, s[22:23]
	s_mov_b32 m0, s83
	s_nop 0
	s_mov_b32 s83, m0
	s_mov_b32 m0, s35
	s_nop 2
	global_load_lds_dwordx4 v139, s[22:23]
	s_mov_b32 m0, s83
	s_mov_b32 s22, m0
	s_mov_b32 m0, s21
	s_nop 2
	global_load_lds_dwordx4 v136, s[58:59]
	s_mov_b32 m0, s22
	s_nop 0
	s_mov_b32 s22, m0
	s_mov_b32 m0, s36
	s_nop 2
	global_load_lds_dwordx4 v138, s[58:59]
	s_mov_b32 m0, s22
	s_waitcnt vmcnt(8)
	s_waitcnt lgkmcnt(0)
	s_setprio 1
	s_barrier
	v_mfma_f32_16x16x32_bf16 v[62:65], v[148:151], v[186:189], v[62:65]
	v_mfma_f32_16x16x32_bf16 v[58:61], v[156:159], v[186:189], v[58:61]
	v_mfma_f32_16x16x32_bf16 v[46:49], v[148:151], v[194:197], v[46:49]
	v_mfma_f32_16x16x32_bf16 v[42:45], v[156:159], v[194:197], v[42:45]
	v_mfma_f32_16x16x32_bf16 v[30:33], v[148:151], v[202:205], v[30:33]
	v_mfma_f32_16x16x32_bf16 v[26:29], v[156:159], v[202:205], v[26:29]
	v_mfma_f32_16x16x32_bf16 v[14:17], v[148:151], v[210:213], v[14:17]
	v_mfma_f32_16x16x32_bf16 v[10:13], v[156:159], v[210:213], v[10:13]
	v_mfma_f32_16x16x32_bf16 v[62:65], v[152:155], v[190:193], v[62:65]
	v_mfma_f32_16x16x32_bf16 v[58:61], v[160:163], v[190:193], v[58:61]
	v_mfma_f32_16x16x32_bf16 v[46:49], v[152:155], v[198:201], v[46:49]
	v_mfma_f32_16x16x32_bf16 v[42:45], v[160:163], v[198:201], v[42:45]
	v_mfma_f32_16x16x32_bf16 v[30:33], v[152:155], v[206:209], v[30:33]
	v_mfma_f32_16x16x32_bf16 v[26:29], v[160:163], v[206:209], v[26:29]
	v_mfma_f32_16x16x32_bf16 v[14:17], v[152:155], v[214:217], v[14:17]
	v_mfma_f32_16x16x32_bf16 v[10:13], v[160:163], v[214:217], v[10:13]
	v_mfma_f32_16x16x32_bf16 v[54:57], v[164:167], v[186:189], v[54:57]
	v_mfma_f32_16x16x32_bf16 v[50:53], v[178:181], v[186:189], v[50:53]
	v_mfma_f32_16x16x32_bf16 v[38:41], v[164:167], v[194:197], v[38:41]
	v_mfma_f32_16x16x32_bf16 v[34:37], v[178:181], v[194:197], v[34:37]
	v_mfma_f32_16x16x32_bf16 v[22:25], v[164:167], v[202:205], v[22:25]
	v_mfma_f32_16x16x32_bf16 v[18:21], v[178:181], v[202:205], v[18:21]
	v_mfma_f32_16x16x32_bf16 v[6:9], v[164:167], v[210:213], v[6:9]
	v_mfma_f32_16x16x32_bf16 v[2:5], v[178:181], v[210:213], v[2:5]
	v_mfma_f32_16x16x32_bf16 v[54:57], v[174:177], v[190:193], v[54:57]
	v_mfma_f32_16x16x32_bf16 v[50:53], v[182:185], v[190:193], v[50:53]
	v_mfma_f32_16x16x32_bf16 v[38:41], v[174:177], v[198:201], v[38:41]
	v_mfma_f32_16x16x32_bf16 v[34:37], v[182:185], v[198:201], v[34:37]
	v_mfma_f32_16x16x32_bf16 v[22:25], v[174:177], v[206:209], v[22:25]
	v_mfma_f32_16x16x32_bf16 v[18:21], v[182:185], v[206:209], v[18:21]
	v_mfma_f32_16x16x32_bf16 v[6:9], v[174:177], v[214:217], v[6:9]
	v_mfma_f32_16x16x32_bf16 v[2:5], v[182:185], v[214:217], v[2:5]
	s_setprio 0
	s_barrier
	ds_read_b128 v[148:151], v145
	ds_read_b128 v[152:155], v145 offset:1024
	ds_read_b128 v[156:159], v145 offset:2048
	ds_read_b128 v[160:163], v145 offset:3072
	ds_read_b128 v[164:167], v146
	ds_read_b128 v[174:177], v146 offset:1024
	ds_read_b128 v[178:181], v146 offset:2048
	ds_read_b128 v[182:185], v146 offset:3072
	ds_read_b128 v[186:189], v144 offset:32768
	ds_read_b128 v[190:193], v144 offset:33792
	ds_read_b128 v[194:197], v144 offset:34816
	ds_read_b128 v[198:201], v144 offset:35840
	ds_read_b128 v[202:205], v144 offset:36864
	ds_read_b128 v[206:209], v144 offset:37888
	ds_read_b128 v[210:213], v144 offset:38912
	ds_read_b128 v[214:217], v144 offset:39936
	s_add_u32 s22, s58, 0x40000
	s_addc_u32 s23, s59, 0
	s_mov_b32 s58, m0
	s_mov_b32 m0, s37
	s_nop 2
	global_load_lds_dwordx4 v136, s[22:23]
	s_mov_b32 m0, s58
	s_nop 0
	s_mov_b32 s58, m0
	s_mov_b32 m0, s52
	s_nop 2
	global_load_lds_dwordx4 v138, s[22:23]
	s_mov_b32 m0, s58
	s_waitcnt vmcnt(8)
	s_waitcnt lgkmcnt(0)
	s_setprio 1
	s_barrier
	v_mfma_f32_16x16x32_bf16 v[126:129], v[148:151], v[186:189], v[126:129]
	v_mfma_f32_16x16x32_bf16 v[122:125], v[156:159], v[186:189], v[122:125]
	v_mfma_f32_16x16x32_bf16 v[110:113], v[148:151], v[194:197], v[110:113]
	v_mfma_f32_16x16x32_bf16 v[106:109], v[156:159], v[194:197], v[106:109]
	v_mfma_f32_16x16x32_bf16 v[94:97], v[148:151], v[202:205], v[94:97]
	v_mfma_f32_16x16x32_bf16 v[90:93], v[156:159], v[202:205], v[90:93]
	v_mfma_f32_16x16x32_bf16 v[78:81], v[148:151], v[210:213], v[78:81]
	v_mfma_f32_16x16x32_bf16 v[74:77], v[156:159], v[210:213], v[74:77]
	v_mfma_f32_16x16x32_bf16 v[126:129], v[152:155], v[190:193], v[126:129]
	v_mfma_f32_16x16x32_bf16 v[122:125], v[160:163], v[190:193], v[122:125]
	v_mfma_f32_16x16x32_bf16 v[110:113], v[152:155], v[198:201], v[110:113]
	v_mfma_f32_16x16x32_bf16 v[106:109], v[160:163], v[198:201], v[106:109]
	v_mfma_f32_16x16x32_bf16 v[94:97], v[152:155], v[206:209], v[94:97]
	v_mfma_f32_16x16x32_bf16 v[90:93], v[160:163], v[206:209], v[90:93]
	v_mfma_f32_16x16x32_bf16 v[78:81], v[152:155], v[214:217], v[78:81]
	v_mfma_f32_16x16x32_bf16 v[74:77], v[160:163], v[214:217], v[74:77]
	v_mfma_f32_16x16x32_bf16 v[118:121], v[164:167], v[186:189], v[118:121]
	v_mfma_f32_16x16x32_bf16 v[114:117], v[178:181], v[186:189], v[114:117]
	v_mfma_f32_16x16x32_bf16 v[102:105], v[164:167], v[194:197], v[102:105]
	v_mfma_f32_16x16x32_bf16 v[98:101], v[178:181], v[194:197], v[98:101]
	v_mfma_f32_16x16x32_bf16 v[86:89], v[164:167], v[202:205], v[86:89]
	v_mfma_f32_16x16x32_bf16 v[82:85], v[178:181], v[202:205], v[82:85]
	v_mfma_f32_16x16x32_bf16 v[70:73], v[164:167], v[210:213], v[70:73]
	v_mfma_f32_16x16x32_bf16 v[66:69], v[178:181], v[210:213], v[66:69]
	v_mfma_f32_16x16x32_bf16 v[118:121], v[174:177], v[190:193], v[118:121]
	v_mfma_f32_16x16x32_bf16 v[114:117], v[182:185], v[190:193], v[114:117]
	v_mfma_f32_16x16x32_bf16 v[102:105], v[174:177], v[198:201], v[102:105]
	v_mfma_f32_16x16x32_bf16 v[98:101], v[182:185], v[198:201], v[98:101]
	v_mfma_f32_16x16x32_bf16 v[86:89], v[174:177], v[206:209], v[86:89]
	v_mfma_f32_16x16x32_bf16 v[82:85], v[182:185], v[206:209], v[82:85]
	v_mfma_f32_16x16x32_bf16 v[70:73], v[174:177], v[214:217], v[70:73]
	v_mfma_f32_16x16x32_bf16 v[66:69], v[182:185], v[214:217], v[66:69]
	s_setprio 0
	s_barrier
	ds_read_b128 v[186:189], v144 offset:49152
	ds_read_b128 v[190:193], v144 offset:50176
	ds_read_b128 v[194:197], v144 offset:51200
	ds_read_b128 v[198:201], v144 offset:52224
	ds_read_b128 v[202:205], v144 offset:53248
	ds_read_b128 v[206:209], v144 offset:54272
	ds_read_b128 v[210:213], v144 offset:55296
	ds_read_b128 v[214:217], v144 offset:56320
	s_add_u32 s22, s56, 0x80
	s_addc_u32 s23, s57, 0
	s_mov_b32 s58, m0
	s_mov_b32 m0, s61
	s_nop 2
	global_load_lds_dwordx4 v137, s[22:23]
	s_mov_b32 m0, s58
	s_nop 0
	s_mov_b32 s58, m0
	s_mov_b32 m0, s62
	s_nop 2
	global_load_lds_dwordx4 v139, s[22:23]
	s_mov_b32 m0, s58
	s_add_u32 s22, s56, 0x40080
	s_addc_u32 s23, s57, 0
	s_mov_b32 s56, m0
	s_mov_b32 m0, s65
	s_nop 2
	global_load_lds_dwordx4 v137, s[22:23]
	s_mov_b32 m0, s56
	s_nop 0
	s_mov_b32 s56, m0
	s_mov_b32 m0, s66
	s_nop 2
	global_load_lds_dwordx4 v139, s[22:23]
	s_mov_b32 m0, s56
	s_mov_b32 s22, m0
	s_mov_b32 m0, s63
	s_nop 2
	global_load_lds_dwordx4 v136, s[54:55]
	s_mov_b32 m0, s22
	s_nop 0
	s_mov_b32 s22, m0
	s_mov_b32 m0, s64
	s_nop 2
	global_load_lds_dwordx4 v138, s[54:55]
	s_mov_b32 m0, s22
	s_waitcnt vmcnt(8)
	s_waitcnt lgkmcnt(0)
	s_setprio 1
	s_barrier
	v_mfma_f32_16x16x32_bf16 v[62:65], v[148:151], v[186:189], v[62:65]
	v_mfma_f32_16x16x32_bf16 v[58:61], v[156:159], v[186:189], v[58:61]
	v_mfma_f32_16x16x32_bf16 v[46:49], v[148:151], v[194:197], v[46:49]
	v_mfma_f32_16x16x32_bf16 v[42:45], v[156:159], v[194:197], v[42:45]
	v_mfma_f32_16x16x32_bf16 v[30:33], v[148:151], v[202:205], v[30:33]
	v_mfma_f32_16x16x32_bf16 v[26:29], v[156:159], v[202:205], v[26:29]
	v_mfma_f32_16x16x32_bf16 v[14:17], v[148:151], v[210:213], v[14:17]
	v_mfma_f32_16x16x32_bf16 v[10:13], v[156:159], v[210:213], v[10:13]
	v_mfma_f32_16x16x32_bf16 v[62:65], v[152:155], v[190:193], v[62:65]
	v_mfma_f32_16x16x32_bf16 v[58:61], v[160:163], v[190:193], v[58:61]
	v_mfma_f32_16x16x32_bf16 v[46:49], v[152:155], v[198:201], v[46:49]
	v_mfma_f32_16x16x32_bf16 v[42:45], v[160:163], v[198:201], v[42:45]
	v_mfma_f32_16x16x32_bf16 v[30:33], v[152:155], v[206:209], v[30:33]
	v_mfma_f32_16x16x32_bf16 v[26:29], v[160:163], v[206:209], v[26:29]
	v_mfma_f32_16x16x32_bf16 v[14:17], v[152:155], v[214:217], v[14:17]
	v_mfma_f32_16x16x32_bf16 v[10:13], v[160:163], v[214:217], v[10:13]
	v_mfma_f32_16x16x32_bf16 v[54:57], v[164:167], v[186:189], v[54:57]
	v_mfma_f32_16x16x32_bf16 v[50:53], v[178:181], v[186:189], v[50:53]
	v_mfma_f32_16x16x32_bf16 v[38:41], v[164:167], v[194:197], v[38:41]
	v_mfma_f32_16x16x32_bf16 v[34:37], v[178:181], v[194:197], v[34:37]
	v_mfma_f32_16x16x32_bf16 v[22:25], v[164:167], v[202:205], v[22:25]
	v_mfma_f32_16x16x32_bf16 v[18:21], v[178:181], v[202:205], v[18:21]
	v_mfma_f32_16x16x32_bf16 v[6:9], v[164:167], v[210:213], v[6:9]
	v_mfma_f32_16x16x32_bf16 v[2:5], v[178:181], v[210:213], v[2:5]
	v_mfma_f32_16x16x32_bf16 v[54:57], v[174:177], v[190:193], v[54:57]
	v_mfma_f32_16x16x32_bf16 v[50:53], v[182:185], v[190:193], v[50:53]
	v_mfma_f32_16x16x32_bf16 v[38:41], v[174:177], v[198:201], v[38:41]
	v_mfma_f32_16x16x32_bf16 v[34:37], v[182:185], v[198:201], v[34:37]
	v_mfma_f32_16x16x32_bf16 v[22:25], v[174:177], v[206:209], v[22:25]
	v_mfma_f32_16x16x32_bf16 v[18:21], v[182:185], v[206:209], v[18:21]
	v_mfma_f32_16x16x32_bf16 v[6:9], v[174:177], v[214:217], v[6:9]
	v_mfma_f32_16x16x32_bf16 v[2:5], v[182:185], v[214:217], v[2:5]
	s_setprio 0
	s_barrier
	s_add_i32 s82, s82, 2
	s_add_u32 s80, s80, 0x100
	s_addc_u32 s81, s81, 0
	s_cmp_gt_u32 s82, 13
	s_mov_b64 s[22:23], s[40:41]
	s_cbranch_scc0 .LBB0_143
	s_and_b64 vcc, exec, s[10:11]
	s_cbranch_vccz .LBB0_146
	s_barrier

.Lpeel170:
	ds_read_b128 v[142:145], v136
	ds_read_b128 v[146:149], v136 offset:1024
	ds_read_b128 v[150:153], v136 offset:2048
	ds_read_b128 v[154:157], v136 offset:3072
	ds_read_b128 v[158:161], v137
	ds_read_b128 v[162:165], v137 offset:1024
	ds_read_b128 v[166:169], v137 offset:2048
	ds_read_b128 v[174:177], v137 offset:3072
	s_add_u32 s14, s12, 0x100
	s_addc_u32 s15, s13, 0
	s_cmp_eq_u32 s56, 12
	s_cselect_b32 s20, s10, s14
	s_cselect_b32 s21, s11, s15
	s_cselect_b32 s18, s8, s54
	s_cselect_b32 s19, s9, s55
	s_add_u32 s16, s20, 0x80
	s_addc_u32 s17, s21, 0
	ds_read_b128 v[178:181], v138
	ds_read_b128 v[182:185], v138 offset:1024
	ds_read_b128 v[186:189], v138 offset:2048
	ds_read_b128 v[190:193], v138 offset:3072
	ds_read_b128 v[194:197], v138 offset:4096
	ds_read_b128 v[198:201], v138 offset:5120
	ds_read_b128 v[202:205], v138 offset:6144
	ds_read_b128 v[206:209], v138 offset:7168
	s_add_u32 s12, s12, 0x40080
	s_addc_u32 s13, s13, 0
	s_mov_b32 s57, m0
	s_mov_b32 m0, s52
	s_nop 2
	global_load_lds_dwordx4 v132, s[12:13]
	s_mov_b32 m0, s57
	s_nop 0
	s_mov_b32 s57, m0
	s_mov_b32 m0, s53
	s_nop 2
	global_load_lds_dwordx4 v134, s[12:13]
	s_mov_b32 m0, s57
	s_waitcnt vmcnt(8)
	s_waitcnt lgkmcnt(0)
	s_setprio 1
	s_barrier
	v_mfma_f32_16x16x32_bf16 v[126:129], v[142:145], v[178:181], 0
	v_mfma_f32_16x16x32_bf16 v[122:125], v[150:153], v[178:181], 0
	v_mfma_f32_16x16x32_bf16 v[110:113], v[142:145], v[186:189], 0
	v_mfma_f32_16x16x32_bf16 v[106:109], v[150:153], v[186:189], 0
	v_mfma_f32_16x16x32_bf16 v[94:97], v[142:145], v[194:197], 0
	v_mfma_f32_16x16x32_bf16 v[90:93], v[150:153], v[194:197], 0
	v_mfma_f32_16x16x32_bf16 v[78:81], v[142:145], v[202:205], 0
	v_mfma_f32_16x16x32_bf16 v[74:77], v[150:153], v[202:205], 0
	v_mfma_f32_16x16x32_bf16 v[126:129], v[146:149], v[182:185], v[126:129]
	v_mfma_f32_16x16x32_bf16 v[122:125], v[154:157], v[182:185], v[122:125]
	v_mfma_f32_16x16x32_bf16 v[110:113], v[146:149], v[190:193], v[110:113]
	v_mfma_f32_16x16x32_bf16 v[106:109], v[154:157], v[190:193], v[106:109]
	v_mfma_f32_16x16x32_bf16 v[94:97], v[146:149], v[198:201], v[94:97]
	v_mfma_f32_16x16x32_bf16 v[90:93], v[154:157], v[198:201], v[90:93]
	v_mfma_f32_16x16x32_bf16 v[78:81], v[146:149], v[206:209], v[78:81]
	v_mfma_f32_16x16x32_bf16 v[74:77], v[154:157], v[206:209], v[74:77]
	v_mfma_f32_16x16x32_bf16 v[118:121], v[158:161], v[178:181], 0
	v_mfma_f32_16x16x32_bf16 v[114:117], v[166:169], v[178:181], 0
	v_mfma_f32_16x16x32_bf16 v[102:105], v[158:161], v[186:189], 0
	v_mfma_f32_16x16x32_bf16 v[98:101], v[166:169], v[186:189], 0
	v_mfma_f32_16x16x32_bf16 v[86:89], v[158:161], v[194:197], 0
	v_mfma_f32_16x16x32_bf16 v[82:85], v[166:169], v[194:197], 0
	v_mfma_f32_16x16x32_bf16 v[70:73], v[158:161], v[202:205], 0
	v_mfma_f32_16x16x32_bf16 v[66:69], v[166:169], v[202:205], 0
	v_mfma_f32_16x16x32_bf16 v[118:121], v[162:165], v[182:185], v[118:121]
	v_mfma_f32_16x16x32_bf16 v[114:117], v[174:177], v[182:185], v[114:117]
	v_mfma_f32_16x16x32_bf16 v[102:105], v[162:165], v[190:193], v[102:105]
	v_mfma_f32_16x16x32_bf16 v[98:101], v[174:177], v[190:193], v[98:101]
	v_mfma_f32_16x16x32_bf16 v[86:89], v[162:165], v[198:201], v[86:89]
	v_mfma_f32_16x16x32_bf16 v[82:85], v[174:177], v[198:201], v[82:85]
	v_mfma_f32_16x16x32_bf16 v[70:73], v[162:165], v[206:209], v[70:73]
	v_mfma_f32_16x16x32_bf16 v[66:69], v[174:177], v[206:209], v[66:69]
	s_setprio 0
	s_barrier
	ds_read_b128 v[178:181], v138 offset:16384
	ds_read_b128 v[182:185], v138 offset:17408
	ds_read_b128 v[186:189], v138 offset:18432
	ds_read_b128 v[190:193], v138 offset:19456
	ds_read_b128 v[194:197], v138 offset:20480
	ds_read_b128 v[198:201], v138 offset:21504
	ds_read_b128 v[202:205], v138 offset:22528
	ds_read_b128 v[206:209], v138 offset:23552
	s_mov_b32 s12, m0
	s_mov_b32 m0, s24
	s_nop 2
	global_load_lds_dwordx4 v133, s[18:19]
	s_mov_b32 m0, s12
	s_nop 0
	s_mov_b32 s12, m0
	s_mov_b32 m0, s25
	s_nop 2
	global_load_lds_dwordx4 v135, s[18:19]
	s_mov_b32 m0, s12
	s_add_u32 s12, s18, 0x40000
	s_addc_u32 s13, s19, 0
	s_mov_b32 s57, m0
	s_mov_b32 m0, s28
	s_nop 2
	global_load_lds_dwordx4 v133, s[12:13]
	s_mov_b32 m0, s57
	s_nop 0
	s_mov_b32 s57, m0
	s_mov_b32 m0, s29
	s_nop 2
	global_load_lds_dwordx4 v135, s[12:13]
	s_mov_b32 m0, s57
	s_mov_b32 s12, m0
	s_mov_b32 m0, s5
	s_nop 2
	global_load_lds_dwordx4 v132, s[20:21]
	s_mov_b32 m0, s12
	s_nop 0
	s_mov_b32 s12, m0
	s_mov_b32 m0, s30
	s_nop 2
	global_load_lds_dwordx4 v134, s[20:21]
	s_mov_b32 m0, s12
	s_waitcnt vmcnt(8)
	s_waitcnt lgkmcnt(0)
	s_setprio 1
	s_barrier
	v_mfma_f32_16x16x32_bf16 v[62:65], v[142:145], v[178:181], 0
	v_mfma_f32_16x16x32_bf16 v[58:61], v[150:153], v[178:181], 0
	v_mfma_f32_16x16x32_bf16 v[46:49], v[142:145], v[186:189], 0
	v_mfma_f32_16x16x32_bf16 v[42:45], v[150:153], v[186:189], 0
	v_mfma_f32_16x16x32_bf16 v[30:33], v[142:145], v[194:197], 0
	v_mfma_f32_16x16x32_bf16 v[26:29], v[150:153], v[194:197], 0
	v_mfma_f32_16x16x32_bf16 v[14:17], v[142:145], v[202:205], 0
	v_mfma_f32_16x16x32_bf16 v[10:13], v[150:153], v[202:205], 0
	v_mfma_f32_16x16x32_bf16 v[62:65], v[146:149], v[182:185], v[62:65]
	v_mfma_f32_16x16x32_bf16 v[58:61], v[154:157], v[182:185], v[58:61]
	v_mfma_f32_16x16x32_bf16 v[46:49], v[146:149], v[190:193], v[46:49]
	v_mfma_f32_16x16x32_bf16 v[42:45], v[154:157], v[190:193], v[42:45]
	v_mfma_f32_16x16x32_bf16 v[30:33], v[146:149], v[198:201], v[30:33]
	v_mfma_f32_16x16x32_bf16 v[26:29], v[154:157], v[198:201], v[26:29]
	v_mfma_f32_16x16x32_bf16 v[14:17], v[146:149], v[206:209], v[14:17]
	v_mfma_f32_16x16x32_bf16 v[10:13], v[154:157], v[206:209], v[10:13]
	v_mfma_f32_16x16x32_bf16 v[54:57], v[158:161], v[178:181], 0
	v_mfma_f32_16x16x32_bf16 v[50:53], v[166:169], v[178:181], 0
	v_mfma_f32_16x16x32_bf16 v[38:41], v[158:161], v[186:189], 0
	v_mfma_f32_16x16x32_bf16 v[34:37], v[166:169], v[186:189], 0
	v_mfma_f32_16x16x32_bf16 v[22:25], v[158:161], v[194:197], 0
	v_mfma_f32_16x16x32_bf16 v[18:21], v[166:169], v[194:197], 0
	v_mfma_f32_16x16x32_bf16 v[6:9], v[158:161], v[202:205], 0
	v_mfma_f32_16x16x32_bf16 v[2:5], v[166:169], v[202:205], 0
	v_mfma_f32_16x16x32_bf16 v[54:57], v[162:165], v[182:185], v[54:57]
	v_mfma_f32_16x16x32_bf16 v[50:53], v[174:177], v[182:185], v[50:53]
	v_mfma_f32_16x16x32_bf16 v[38:41], v[162:165], v[190:193], v[38:41]
	v_mfma_f32_16x16x32_bf16 v[34:37], v[174:177], v[190:193], v[34:37]
	v_mfma_f32_16x16x32_bf16 v[22:25], v[162:165], v[198:201], v[22:25]
	v_mfma_f32_16x16x32_bf16 v[18:21], v[174:177], v[198:201], v[18:21]
	v_mfma_f32_16x16x32_bf16 v[6:9], v[162:165], v[206:209], v[6:9]
	v_mfma_f32_16x16x32_bf16 v[2:5], v[174:177], v[206:209], v[2:5]
	s_setprio 0
	s_barrier
	s_branch .Lmid170
.LBB0_170:
	ds_read_b128 v[142:145], v136
	ds_read_b128 v[146:149], v136 offset:1024
	ds_read_b128 v[150:153], v136 offset:2048
	ds_read_b128 v[154:157], v136 offset:3072
	ds_read_b128 v[158:161], v137
	ds_read_b128 v[162:165], v137 offset:1024
	ds_read_b128 v[166:169], v137 offset:2048
	ds_read_b128 v[174:177], v137 offset:3072
	s_add_u32 s14, s12, 0x100
	s_addc_u32 s15, s13, 0
	s_cmp_eq_u32 s56, 12
	s_cselect_b32 s20, s10, s14
	s_cselect_b32 s21, s11, s15
	s_cselect_b32 s18, s8, s54
	s_cselect_b32 s19, s9, s55
	s_add_u32 s16, s20, 0x80
	s_addc_u32 s17, s21, 0
	ds_read_b128 v[178:181], v138
	ds_read_b128 v[182:185], v138 offset:1024
	ds_read_b128 v[186:189], v138 offset:2048
	ds_read_b128 v[190:193], v138 offset:3072
	ds_read_b128 v[194:197], v138 offset:4096
	ds_read_b128 v[198:201], v138 offset:5120
	ds_read_b128 v[202:205], v138 offset:6144
	ds_read_b128 v[206:209], v138 offset:7168
	s_add_u32 s12, s12, 0x40080
	s_addc_u32 s13, s13, 0
	s_mov_b32 s57, m0
	s_mov_b32 m0, s52
	s_nop 2
	global_load_lds_dwordx4 v132, s[12:13]
	s_mov_b32 m0, s57
	s_nop 0
	s_mov_b32 s57, m0
	s_mov_b32 m0, s53
	s_nop 2
	global_load_lds_dwordx4 v134, s[12:13]
	s_mov_b32 m0, s57
	s_waitcnt vmcnt(8)
	s_waitcnt lgkmcnt(0)
	s_setprio 1
	s_barrier
	v_mfma_f32_16x16x32_bf16 v[126:129], v[142:145], v[178:181], v[126:129]
	v_mfma_f32_16x16x32_bf16 v[122:125], v[150:153], v[178:181], v[122:125]
	v_mfma_f32_16x16x32_bf16 v[110:113], v[142:145], v[186:189], v[110:113]
	v_mfma_f32_16x16x32_bf16 v[106:109], v[150:153], v[186:189], v[106:109]
	v_mfma_f32_16x16x32_bf16 v[94:97], v[142:145], v[194:197], v[94:97]
	v_mfma_f32_16x16x32_bf16 v[90:93], v[150:153], v[194:197], v[90:93]
	v_mfma_f32_16x16x32_bf16 v[78:81], v[142:145], v[202:205], v[78:81]
	v_mfma_f32_16x16x32_bf16 v[74:77], v[150:153], v[202:205], v[74:77]
	v_mfma_f32_16x16x32_bf16 v[126:129], v[146:149], v[182:185], v[126:129]
	v_mfma_f32_16x16x32_bf16 v[122:125], v[154:157], v[182:185], v[122:125]
	v_mfma_f32_16x16x32_bf16 v[110:113], v[146:149], v[190:193], v[110:113]
	v_mfma_f32_16x16x32_bf16 v[106:109], v[154:157], v[190:193], v[106:109]
	v_mfma_f32_16x16x32_bf16 v[94:97], v[146:149], v[198:201], v[94:97]
	v_mfma_f32_16x16x32_bf16 v[90:93], v[154:157], v[198:201], v[90:93]
	v_mfma_f32_16x16x32_bf16 v[78:81], v[146:149], v[206:209], v[78:81]
	v_mfma_f32_16x16x32_bf16 v[74:77], v[154:157], v[206:209], v[74:77]
	v_mfma_f32_16x16x32_bf16 v[118:121], v[158:161], v[178:181], v[118:121]
	v_mfma_f32_16x16x32_bf16 v[114:117], v[166:169], v[178:181], v[114:117]
	v_mfma_f32_16x16x32_bf16 v[102:105], v[158:161], v[186:189], v[102:105]
	v_mfma_f32_16x16x32_bf16 v[98:101], v[166:169], v[186:189], v[98:101]
	v_mfma_f32_16x16x32_bf16 v[86:89], v[158:161], v[194:197], v[86:89]
	v_mfma_f32_16x16x32_bf16 v[82:85], v[166:169], v[194:197], v[82:85]
	v_mfma_f32_16x16x32_bf16 v[70:73], v[158:161], v[202:205], v[70:73]
	v_mfma_f32_16x16x32_bf16 v[66:69], v[166:169], v[202:205], v[66:69]
	v_mfma_f32_16x16x32_bf16 v[118:121], v[162:165], v[182:185], v[118:121]
	v_mfma_f32_16x16x32_bf16 v[114:117], v[174:177], v[182:185], v[114:117]
	v_mfma_f32_16x16x32_bf16 v[102:105], v[162:165], v[190:193], v[102:105]
	v_mfma_f32_16x16x32_bf16 v[98:101], v[174:177], v[190:193], v[98:101]
	v_mfma_f32_16x16x32_bf16 v[86:89], v[162:165], v[198:201], v[86:89]
	v_mfma_f32_16x16x32_bf16 v[82:85], v[174:177], v[198:201], v[82:85]
	v_mfma_f32_16x16x32_bf16 v[70:73], v[162:165], v[206:209], v[70:73]
	v_mfma_f32_16x16x32_bf16 v[66:69], v[174:177], v[206:209], v[66:69]
	s_setprio 0
	s_barrier
	ds_read_b128 v[178:181], v138 offset:16384
	ds_read_b128 v[182:185], v138 offset:17408
	ds_read_b128 v[186:189], v138 offset:18432
	ds_read_b128 v[190:193], v138 offset:19456
	ds_read_b128 v[194:197], v138 offset:20480
	ds_read_b128 v[198:201], v138 offset:21504
	ds_read_b128 v[202:205], v138 offset:22528
	ds_read_b128 v[206:209], v138 offset:23552
	s_mov_b32 s12, m0
	s_mov_b32 m0, s24
	s_nop 2
	global_load_lds_dwordx4 v133, s[18:19]
	s_mov_b32 m0, s12
	s_nop 0
	s_mov_b32 s12, m0
	s_mov_b32 m0, s25
	s_nop 2
	global_load_lds_dwordx4 v135, s[18:19]
	s_mov_b32 m0, s12
	s_add_u32 s12, s18, 0x40000
	s_addc_u32 s13, s19, 0
	s_mov_b32 s57, m0
	s_mov_b32 m0, s28
	s_nop 2
	global_load_lds_dwordx4 v133, s[12:13]
	s_mov_b32 m0, s57
	s_nop 0
	s_mov_b32 s57, m0
	s_mov_b32 m0, s29
	s_nop 2
	global_load_lds_dwordx4 v135, s[12:13]
	s_mov_b32 m0, s57
	s_mov_b32 s12, m0
	s_mov_b32 m0, s5
	s_nop 2
	global_load_lds_dwordx4 v132, s[20:21]
	s_mov_b32 m0, s12
	s_nop 0
	s_mov_b32 s12, m0
	s_mov_b32 m0, s30
	s_nop 2
	global_load_lds_dwordx4 v134, s[20:21]
	s_mov_b32 m0, s12
	s_waitcnt vmcnt(8)
	s_waitcnt lgkmcnt(0)
	s_setprio 1
	s_barrier
	v_mfma_f32_16x16x32_bf16 v[62:65], v[142:145], v[178:181], v[62:65]
	v_mfma_f32_16x16x32_bf16 v[58:61], v[150:153], v[178:181], v[58:61]
	v_mfma_f32_16x16x32_bf16 v[46:49], v[142:145], v[186:189], v[46:49]
	v_mfma_f32_16x16x32_bf16 v[42:45], v[150:153], v[186:189], v[42:45]
	v_mfma_f32_16x16x32_bf16 v[30:33], v[142:145], v[194:197], v[30:33]
	v_mfma_f32_16x16x32_bf16 v[26:29], v[150:153], v[194:197], v[26:29]
	v_mfma_f32_16x16x32_bf16 v[14:17], v[142:145], v[202:205], v[14:17]
	v_mfma_f32_16x16x32_bf16 v[10:13], v[150:153], v[202:205], v[10:13]
	v_mfma_f32_16x16x32_bf16 v[62:65], v[146:149], v[182:185], v[62:65]
	v_mfma_f32_16x16x32_bf16 v[58:61], v[154:157], v[182:185], v[58:61]
	v_mfma_f32_16x16x32_bf16 v[46:49], v[146:149], v[190:193], v[46:49]
	v_mfma_f32_16x16x32_bf16 v[42:45], v[154:157], v[190:193], v[42:45]
	v_mfma_f32_16x16x32_bf16 v[30:33], v[146:149], v[198:201], v[30:33]
	v_mfma_f32_16x16x32_bf16 v[26:29], v[154:157], v[198:201], v[26:29]
	v_mfma_f32_16x16x32_bf16 v[14:17], v[146:149], v[206:209], v[14:17]
	v_mfma_f32_16x16x32_bf16 v[10:13], v[154:157], v[206:209], v[10:13]
	v_mfma_f32_16x16x32_bf16 v[54:57], v[158:161], v[178:181], v[54:57]
	v_mfma_f32_16x16x32_bf16 v[50:53], v[166:169], v[178:181], v[50:53]
	v_mfma_f32_16x16x32_bf16 v[38:41], v[158:161], v[186:189], v[38:41]
	v_mfma_f32_16x16x32_bf16 v[34:37], v[166:169], v[186:189], v[34:37]
	v_mfma_f32_16x16x32_bf16 v[22:25], v[158:161], v[194:197], v[22:25]
	v_mfma_f32_16x16x32_bf16 v[18:21], v[166:169], v[194:197], v[18:21]
	v_mfma_f32_16x16x32_bf16 v[6:9], v[158:161], v[202:205], v[6:9]
	v_mfma_f32_16x16x32_bf16 v[2:5], v[166:169], v[202:205], v[2:5]
	v_mfma_f32_16x16x32_bf16 v[54:57], v[162:165], v[182:185], v[54:57]
	v_mfma_f32_16x16x32_bf16 v[50:53], v[174:177], v[182:185], v[50:53]
	v_mfma_f32_16x16x32_bf16 v[38:41], v[162:165], v[190:193], v[38:41]
	v_mfma_f32_16x16x32_bf16 v[34:37], v[174:177], v[190:193], v[34:37]
	v_mfma_f32_16x16x32_bf16 v[22:25], v[162:165], v[198:201], v[22:25]
	v_mfma_f32_16x16x32_bf16 v[18:21], v[174:177], v[198:201], v[18:21]
	v_mfma_f32_16x16x32_bf16 v[6:9], v[162:165], v[206:209], v[6:9]
	v_mfma_f32_16x16x32_bf16 v[2:5], v[174:177], v[206:209], v[2:5]
	s_setprio 0
	s_barrier
.Lmid170:
	ds_read_b128 v[142:145], v139
	ds_read_b128 v[146:149], v139 offset:1024
	ds_read_b128 v[150:153], v139 offset:2048
	ds_read_b128 v[154:157], v139 offset:3072
	ds_read_b128 v[158:161], v140
	ds_read_b128 v[162:165], v140 offset:1024
	ds_read_b128 v[166:169], v140 offset:2048
	ds_read_b128 v[174:177], v140 offset:3072
	ds_read_b128 v[178:181], v138 offset:32768
	ds_read_b128 v[182:185], v138 offset:33792
	ds_read_b128 v[186:189], v138 offset:34816
	ds_read_b128 v[190:193], v138 offset:35840
	ds_read_b128 v[194:197], v138 offset:36864
	ds_read_b128 v[198:201], v138 offset:37888
	ds_read_b128 v[202:205], v138 offset:38912
	ds_read_b128 v[206:209], v138 offset:39936
	s_add_u32 s12, s20, 0x40000
	s_addc_u32 s13, s21, 0
	s_mov_b32 s20, m0
	s_mov_b32 m0, s31
	s_nop 2
	global_load_lds_dwordx4 v132, s[12:13]
	s_mov_b32 m0, s20
	s_nop 0
	s_mov_b32 s20, m0
	s_mov_b32 m0, s33
	s_nop 2
	global_load_lds_dwordx4 v134, s[12:13]
	s_mov_b32 m0, s20
	s_waitcnt vmcnt(8)
	s_waitcnt lgkmcnt(0)
	s_setprio 1
	s_barrier
	v_mfma_f32_16x16x32_bf16 v[126:129], v[142:145], v[178:181], v[126:129]
	v_mfma_f32_16x16x32_bf16 v[122:125], v[150:153], v[178:181], v[122:125]
	v_mfma_f32_16x16x32_bf16 v[110:113], v[142:145], v[186:189], v[110:113]
	v_mfma_f32_16x16x32_bf16 v[106:109], v[150:153], v[186:189], v[106:109]
	v_mfma_f32_16x16x32_bf16 v[94:97], v[142:145], v[194:197], v[94:97]
	v_mfma_f32_16x16x32_bf16 v[90:93], v[150:153], v[194:197], v[90:93]
	v_mfma_f32_16x16x32_bf16 v[78:81], v[142:145], v[202:205], v[78:81]
	v_mfma_f32_16x16x32_bf16 v[74:77], v[150:153], v[202:205], v[74:77]
	v_mfma_f32_16x16x32_bf16 v[126:129], v[146:149], v[182:185], v[126:129]
	v_mfma_f32_16x16x32_bf16 v[122:125], v[154:157], v[182:185], v[122:125]
	v_mfma_f32_16x16x32_bf16 v[110:113], v[146:149], v[190:193], v[110:113]
	v_mfma_f32_16x16x32_bf16 v[106:109], v[154:157], v[190:193], v[106:109]
	v_mfma_f32_16x16x32_bf16 v[94:97], v[146:149], v[198:201], v[94:97]
	v_mfma_f32_16x16x32_bf16 v[90:93], v[154:157], v[198:201], v[90:93]
	v_mfma_f32_16x16x32_bf16 v[78:81], v[146:149], v[206:209], v[78:81]
	v_mfma_f32_16x16x32_bf16 v[74:77], v[154:157], v[206:209], v[74:77]
	v_mfma_f32_16x16x32_bf16 v[118:121], v[158:161], v[178:181], v[118:121]
	v_mfma_f32_16x16x32_bf16 v[114:117], v[166:169], v[178:181], v[114:117]
	v_mfma_f32_16x16x32_bf16 v[102:105], v[158:161], v[186:189], v[102:105]
	v_mfma_f32_16x16x32_bf16 v[98:101], v[166:169], v[186:189], v[98:101]
	v_mfma_f32_16x16x32_bf16 v[86:89], v[158:161], v[194:197], v[86:89]
	v_mfma_f32_16x16x32_bf16 v[82:85], v[166:169], v[194:197], v[82:85]
	v_mfma_f32_16x16x32_bf16 v[70:73], v[158:161], v[202:205], v[70:73]
	v_mfma_f32_16x16x32_bf16 v[66:69], v[166:169], v[202:205], v[66:69]
	v_mfma_f32_16x16x32_bf16 v[118:121], v[162:165], v[182:185], v[118:121]
	v_mfma_f32_16x16x32_bf16 v[114:117], v[174:177], v[182:185], v[114:117]
	v_mfma_f32_16x16x32_bf16 v[102:105], v[162:165], v[190:193], v[102:105]
	v_mfma_f32_16x16x32_bf16 v[98:101], v[174:177], v[190:193], v[98:101]
	v_mfma_f32_16x16x32_bf16 v[86:89], v[162:165], v[198:201], v[86:89]
	v_mfma_f32_16x16x32_bf16 v[82:85], v[174:177], v[198:201], v[82:85]
	v_mfma_f32_16x16x32_bf16 v[70:73], v[162:165], v[206:209], v[70:73]
	v_mfma_f32_16x16x32_bf16 v[66:69], v[174:177], v[206:209], v[66:69]
	s_setprio 0
	s_barrier
	ds_read_b128 v[178:181], v138 offset:49152
	ds_read_b128 v[182:185], v138 offset:50176
	ds_read_b128 v[186:189], v138 offset:51200
	ds_read_b128 v[190:193], v138 offset:52224
	ds_read_b128 v[194:197], v138 offset:53248
	ds_read_b128 v[198:201], v138 offset:54272
	ds_read_b128 v[202:205], v138 offset:55296
	ds_read_b128 v[206:209], v138 offset:56320
	s_add_u32 s12, s18, 0x80
	s_addc_u32 s13, s19, 0
	s_mov_b32 s20, m0
	s_mov_b32 m0, s34
	s_nop 2
	global_load_lds_dwordx4 v133, s[12:13]
	s_mov_b32 m0, s20
	s_nop 0
	s_mov_b32 s20, m0
	s_mov_b32 m0, s35
	s_nop 2
	global_load_lds_dwordx4 v135, s[12:13]
	s_mov_b32 m0, s20
	s_add_u32 s12, s18, 0x40080
	s_addc_u32 s13, s19, 0
	s_mov_b32 s18, m0
	s_mov_b32 m0, s40
	s_nop 2
	global_load_lds_dwordx4 v133, s[12:13]
	s_mov_b32 m0, s18
	s_nop 0
	s_mov_b32 s18, m0
	s_mov_b32 m0, s41
	s_nop 2
	global_load_lds_dwordx4 v135, s[12:13]
	s_mov_b32 m0, s18
	s_mov_b32 s12, m0
	s_mov_b32 m0, s36
	s_nop 2
	global_load_lds_dwordx4 v132, s[16:17]
	s_mov_b32 m0, s12
	s_nop 0
	s_mov_b32 s12, m0
	s_mov_b32 m0, s37
	s_nop 2
	global_load_lds_dwordx4 v134, s[16:17]
	s_mov_b32 m0, s12
	s_waitcnt vmcnt(8)
	s_waitcnt lgkmcnt(0)
	s_setprio 1
	s_barrier
	v_mfma_f32_16x16x32_bf16 v[62:65], v[142:145], v[178:181], v[62:65]
	v_mfma_f32_16x16x32_bf16 v[58:61], v[150:153], v[178:181], v[58:61]
	v_mfma_f32_16x16x32_bf16 v[46:49], v[142:145], v[186:189], v[46:49]
	v_mfma_f32_16x16x32_bf16 v[42:45], v[150:153], v[186:189], v[42:45]
	v_mfma_f32_16x16x32_bf16 v[30:33], v[142:145], v[194:197], v[30:33]
	v_mfma_f32_16x16x32_bf16 v[26:29], v[150:153], v[194:197], v[26:29]
	v_mfma_f32_16x16x32_bf16 v[14:17], v[142:145], v[202:205], v[14:17]
	v_mfma_f32_16x16x32_bf16 v[10:13], v[150:153], v[202:205], v[10:13]
	v_mfma_f32_16x16x32_bf16 v[62:65], v[146:149], v[182:185], v[62:65]
	v_mfma_f32_16x16x32_bf16 v[58:61], v[154:157], v[182:185], v[58:61]
	v_mfma_f32_16x16x32_bf16 v[46:49], v[146:149], v[190:193], v[46:49]
	v_mfma_f32_16x16x32_bf16 v[42:45], v[154:157], v[190:193], v[42:45]
	v_mfma_f32_16x16x32_bf16 v[30:33], v[146:149], v[198:201], v[30:33]
	v_mfma_f32_16x16x32_bf16 v[26:29], v[154:157], v[198:201], v[26:29]
	v_mfma_f32_16x16x32_bf16 v[14:17], v[146:149], v[206:209], v[14:17]
	v_mfma_f32_16x16x32_bf16 v[10:13], v[154:157], v[206:209], v[10:13]
	v_mfma_f32_16x16x32_bf16 v[54:57], v[158:161], v[178:181], v[54:57]
	v_mfma_f32_16x16x32_bf16 v[50:53], v[166:169], v[178:181], v[50:53]
	v_mfma_f32_16x16x32_bf16 v[38:41], v[158:161], v[186:189], v[38:41]
	v_mfma_f32_16x16x32_bf16 v[34:37], v[166:169], v[186:189], v[34:37]
	v_mfma_f32_16x16x32_bf16 v[22:25], v[158:161], v[194:197], v[22:25]
	v_mfma_f32_16x16x32_bf16 v[18:21], v[166:169], v[194:197], v[18:21]
	v_mfma_f32_16x16x32_bf16 v[6:9], v[158:161], v[202:205], v[6:9]
	v_mfma_f32_16x16x32_bf16 v[2:5], v[166:169], v[202:205], v[2:5]
	v_mfma_f32_16x16x32_bf16 v[54:57], v[162:165], v[182:185], v[54:57]
	v_mfma_f32_16x16x32_bf16 v[50:53], v[174:177], v[182:185], v[50:53]
	v_mfma_f32_16x16x32_bf16 v[38:41], v[162:165], v[190:193], v[38:41]
	v_mfma_f32_16x16x32_bf16 v[34:37], v[174:177], v[190:193], v[34:37]
	v_mfma_f32_16x16x32_bf16 v[22:25], v[162:165], v[198:201], v[22:25]
	v_mfma_f32_16x16x32_bf16 v[18:21], v[174:177], v[198:201], v[18:21]
	v_mfma_f32_16x16x32_bf16 v[6:9], v[162:165], v[206:209], v[6:9]
	v_mfma_f32_16x16x32_bf16 v[2:5], v[174:177], v[206:209], v[2:5]
	s_setprio 0
	s_barrier
	s_add_i32 s56, s56, 2
	s_add_u32 s54, s54, 0x100
	s_addc_u32 s55, s55, 0
	s_cmp_gt_u32 s56, 13
	s_mov_b64 s[12:13], s[14:15]
	s_cbranch_scc0 .LBB0_170
	s_cmpk_lt_u32 s23, 0x100
	s_cbranch_scc0 .LBB0_173
	s_barrier

.LBB0_190:
	ds_read_b128 v[18:21], v174
	ds_read_b128 v[22:25], v174 offset:1024
	ds_read_b128 v[26:29], v174 offset:2048
	ds_read_b128 v[30:33], v174 offset:3072
	ds_read_b128 v[2:5], v175
	ds_read_b128 v[6:9], v175 offset:1024
	ds_read_b128 v[10:13], v175 offset:2048
	ds_read_b128 v[14:17], v175 offset:3072
	s_add_u32 s76, s78, 0x100
	s_addc_u32 s77, s79, 0
	s_cmp_eq_u32 s33, 4
	s_cselect_b32 s84, s59, s76
	s_cselect_b32 s85, s7, s77
	s_cselect_b32 s82, s67, vcc_lo
	s_cselect_b32 s83, s57, vcc_hi
	s_add_u32 s80, s84, 0x80
	s_addc_u32 s81, s85, 0
	ds_read_b128 v[180:183], v176
	ds_read_b128 v[184:187], v176 offset:1024
	ds_read_b128 v[188:191], v176 offset:2048
	ds_read_b128 v[192:195], v176 offset:3072
	ds_read_b128 v[196:199], v176 offset:4096
	ds_read_b128 v[200:203], v176 offset:5120
	ds_read_b128 v[204:207], v176 offset:6144
	ds_read_b128 v[208:211], v176 offset:7168
	s_add_u32 s78, s78, 0x20080
	s_addc_u32 s79, s79, 0
	s_mov_b32 s88, m0
	s_mov_b32 m0, s96
	s_nop 2
	global_load_lds_dwordx4 v166, s[78:79]
	s_mov_b32 m0, s88
	s_nop 0
	s_mov_b32 s88, m0
	s_mov_b32 m0, s92
	s_nop 2
	global_load_lds_dwordx4 v168, s[78:79]
	s_mov_b32 m0, s88
	s_waitcnt vmcnt(8)
	s_waitcnt lgkmcnt(0)
	s_setprio 1
	s_barrier
	v_mfma_f32_16x16x128_f8f6f4 v[158:161], v[18:25], v[180:187], v[158:161]
	v_mfma_f32_16x16x128_f8f6f4 v[154:157], v[26:33], v[180:187], v[154:157]
	v_mfma_f32_16x16x128_f8f6f4 v[146:149], v[18:25], v[188:195], v[146:149]
	v_mfma_f32_16x16x128_f8f6f4 v[138:141], v[26:33], v[188:195], v[138:141]
	v_mfma_f32_16x16x128_f8f6f4 v[130:133], v[18:25], v[196:203], v[130:133]
	v_mfma_f32_16x16x128_f8f6f4 v[122:125], v[26:33], v[196:203], v[122:125]
	v_mfma_f32_16x16x128_f8f6f4 v[114:117], v[18:25], v[204:211], v[114:117]
	v_mfma_f32_16x16x128_f8f6f4 v[106:109], v[26:33], v[204:211], v[106:109]
	v_mfma_f32_16x16x128_f8f6f4 v[150:153], v[2:9], v[180:187], v[150:153]
	v_mfma_f32_16x16x128_f8f6f4 v[142:145], v[10:17], v[180:187], v[142:145]
	v_mfma_f32_16x16x128_f8f6f4 v[134:137], v[2:9], v[188:195], v[134:137]
	v_mfma_f32_16x16x128_f8f6f4 v[126:129], v[10:17], v[188:195], v[126:129]
	v_mfma_f32_16x16x128_f8f6f4 v[118:121], v[2:9], v[196:203], v[118:121]
	v_mfma_f32_16x16x128_f8f6f4 v[110:113], v[10:17], v[196:203], v[110:113]
	v_mfma_f32_16x16x128_f8f6f4 v[102:105], v[2:9], v[204:211], v[102:105]
	v_mfma_f32_16x16x128_f8f6f4 v[98:101], v[10:17], v[204:211], v[98:101]
	s_setprio 0
	s_barrier
	ds_read_b128 v[180:183], v176 offset:16384
	ds_read_b128 v[184:187], v176 offset:17408
	ds_read_b128 v[188:191], v176 offset:18432
	ds_read_b128 v[192:195], v176 offset:19456
	ds_read_b128 v[196:199], v176 offset:20480
	ds_read_b128 v[200:203], v176 offset:21504
	ds_read_b128 v[204:207], v176 offset:22528
	ds_read_b128 v[208:211], v176 offset:23552
	s_mov_b32 s78, m0
	s_mov_b32 m0, s36
	s_nop 2
	global_load_lds_dwordx4 v167, s[82:83]
	s_mov_b32 m0, s78
	s_nop 0
	s_mov_b32 s78, m0
	s_mov_b32 m0, s37
	s_nop 2
	global_load_lds_dwordx4 v169, s[82:83]
	s_mov_b32 m0, s78
	s_add_u32 s78, s82, 0x20000
	s_addc_u32 s79, s83, 0
	s_mov_b32 s88, m0
	s_mov_b32 m0, s55
	s_nop 2
	global_load_lds_dwordx4 v167, s[78:79]
	s_mov_b32 m0, s88
	s_nop 0
	s_mov_b32 s88, m0
	s_mov_b32 m0, s86
	s_nop 2
	global_load_lds_dwordx4 v169, s[78:79]
	s_mov_b32 m0, s88
	s_mov_b32 s78, m0
	s_mov_b32 m0, s35
	s_nop 2
	global_load_lds_dwordx4 v166, s[84:85]
	s_mov_b32 m0, s78
	s_nop 0
	s_mov_b32 s78, m0
	s_mov_b32 m0, s87
	s_nop 2
	global_load_lds_dwordx4 v168, s[84:85]
	s_mov_b32 m0, s78
	s_waitcnt vmcnt(8)
	s_waitcnt lgkmcnt(0)
	s_setprio 1
	s_barrier
	v_mfma_f32_16x16x128_f8f6f4 v[94:97], v[18:25], v[180:187], v[94:97]
	v_mfma_f32_16x16x128_f8f6f4 v[90:93], v[26:33], v[180:187], v[90:93]
	v_mfma_f32_16x16x128_f8f6f4 v[82:85], v[18:25], v[188:195], v[82:85]
	v_mfma_f32_16x16x128_f8f6f4 v[74:77], v[26:33], v[188:195], v[74:77]
	v_mfma_f32_16x16x128_f8f6f4 v[66:69], v[18:25], v[196:203], v[66:69]
	v_mfma_f32_16x16x128_f8f6f4 v[58:61], v[26:33], v[196:203], v[58:61]
	v_mfma_f32_16x16x128_f8f6f4 v[50:53], v[18:25], v[204:211], v[50:53]
	v_mfma_f32_16x16x128_f8f6f4 v[42:45], v[26:33], v[204:211], v[42:45]
	v_mfma_f32_16x16x128_f8f6f4 v[86:89], v[2:9], v[180:187], v[86:89]
	v_mfma_f32_16x16x128_f8f6f4 v[78:81], v[10:17], v[180:187], v[78:81]
	v_mfma_f32_16x16x128_f8f6f4 v[70:73], v[2:9], v[188:195], v[70:73]
	v_mfma_f32_16x16x128_f8f6f4 v[62:65], v[10:17], v[188:195], v[62:65]
	v_mfma_f32_16x16x128_f8f6f4 v[54:57], v[2:9], v[196:203], v[54:57]
	v_mfma_f32_16x16x128_f8f6f4 v[46:49], v[10:17], v[196:203], v[46:49]
	v_mfma_f32_16x16x128_f8f6f4 v[38:41], v[2:9], v[204:211], v[38:41]
	v_mfma_f32_16x16x128_f8f6f4 v[34:37], v[10:17], v[204:211], v[34:37]
	s_setprio 0
	s_barrier
	ds_read_b128 v[2:5], v177
	ds_read_b128 v[6:9], v177 offset:1024
	ds_read_b128 v[10:13], v177 offset:2048
	ds_read_b128 v[14:17], v177 offset:3072
	ds_read_b128 v[18:21], v178
	ds_read_b128 v[22:25], v178 offset:1024
	ds_read_b128 v[26:29], v178 offset:2048
	ds_read_b128 v[30:33], v178 offset:3072
	ds_read_b128 v[180:183], v176 offset:32768
	ds_read_b128 v[184:187], v176 offset:33792
	ds_read_b128 v[188:191], v176 offset:34816
	ds_read_b128 v[192:195], v176 offset:35840
	ds_read_b128 v[196:199], v176 offset:36864
	ds_read_b128 v[200:203], v176 offset:37888
	ds_read_b128 v[204:207], v176 offset:38912
	ds_read_b128 v[208:211], v176 offset:39936
	s_add_u32 s78, s84, 0x20000
	s_addc_u32 s79, s85, 0
	s_mov_b32 s84, m0
	s_mov_b32 m0, s89
	s_nop 2
	global_load_lds_dwordx4 v166, s[78:79]
	s_mov_b32 m0, s84
	s_nop 0
	s_mov_b32 s84, m0
	s_mov_b32 m0, s3
	s_nop 2
	global_load_lds_dwordx4 v168, s[78:79]
	s_mov_b32 m0, s84
	s_waitcnt vmcnt(8)
	s_waitcnt lgkmcnt(0)
	s_setprio 1
	s_barrier
	v_mfma_f32_16x16x128_f8f6f4 v[158:161], v[2:9], v[180:187], v[158:161]
	v_mfma_f32_16x16x128_f8f6f4 v[154:157], v[10:17], v[180:187], v[154:157]
	v_mfma_f32_16x16x128_f8f6f4 v[146:149], v[2:9], v[188:195], v[146:149]
	v_mfma_f32_16x16x128_f8f6f4 v[138:141], v[10:17], v[188:195], v[138:141]
	v_mfma_f32_16x16x128_f8f6f4 v[130:133], v[2:9], v[196:203], v[130:133]
	v_mfma_f32_16x16x128_f8f6f4 v[122:125], v[10:17], v[196:203], v[122:125]
	v_mfma_f32_16x16x128_f8f6f4 v[114:117], v[2:9], v[204:211], v[114:117]
	v_mfma_f32_16x16x128_f8f6f4 v[106:109], v[10:17], v[204:211], v[106:109]
	v_mfma_f32_16x16x128_f8f6f4 v[150:153], v[18:25], v[180:187], v[150:153]
	v_mfma_f32_16x16x128_f8f6f4 v[142:145], v[26:33], v[180:187], v[142:145]
	v_mfma_f32_16x16x128_f8f6f4 v[134:137], v[18:25], v[188:195], v[134:137]
	v_mfma_f32_16x16x128_f8f6f4 v[126:129], v[26:33], v[188:195], v[126:129]
	v_mfma_f32_16x16x128_f8f6f4 v[118:121], v[18:25], v[196:203], v[118:121]
	v_mfma_f32_16x16x128_f8f6f4 v[110:113], v[26:33], v[196:203], v[110:113]
	v_mfma_f32_16x16x128_f8f6f4 v[102:105], v[18:25], v[204:211], v[102:105]
	v_mfma_f32_16x16x128_f8f6f4 v[98:101], v[26:33], v[204:211], v[98:101]
	s_setprio 0
	s_barrier
	ds_read_b128 v[180:183], v176 offset:49152
	ds_read_b128 v[184:187], v176 offset:50176
	ds_read_b128 v[188:191], v176 offset:51200
	ds_read_b128 v[192:195], v176 offset:52224
	ds_read_b128 v[196:199], v176 offset:53248
	ds_read_b128 v[200:203], v176 offset:54272
	ds_read_b128 v[204:207], v176 offset:55296
	ds_read_b128 v[208:211], v176 offset:56320
	s_add_u32 s78, s82, 0x80
	s_addc_u32 s79, s83, 0
	s_mov_b32 s84, m0
	s_mov_b32 m0, s90
	s_nop 2
	global_load_lds_dwordx4 v167, s[78:79]
	s_mov_b32 m0, s84
	s_nop 0
	s_mov_b32 s84, m0
	s_mov_b32 m0, s28
	s_nop 2
	global_load_lds_dwordx4 v169, s[78:79]
	s_mov_b32 m0, s84
	s_add_u32 s78, s82, 0x20080
	s_addc_u32 s79, s83, 0
	s_mov_b32 s82, m0
	s_mov_b32 m0, s94
	s_nop 2
	global_load_lds_dwordx4 v167, s[78:79]
	s_mov_b32 m0, s82
	s_nop 0
	s_mov_b32 s82, m0
	s_mov_b32 m0, s95
	s_nop 2
	global_load_lds_dwordx4 v169, s[78:79]
	s_mov_b32 m0, s82
	s_mov_b32 s78, m0
	s_mov_b32 m0, s93
	s_nop 2
	global_load_lds_dwordx4 v166, s[80:81]
	s_mov_b32 m0, s78
	s_nop 0
	s_mov_b32 s78, m0
	s_mov_b32 m0, s2
	s_nop 2
	global_load_lds_dwordx4 v168, s[80:81]
	s_mov_b32 m0, s78
	s_waitcnt vmcnt(8)
	s_waitcnt lgkmcnt(0)
	s_setprio 1
	s_barrier
	v_mfma_f32_16x16x128_f8f6f4 v[94:97], v[2:9], v[180:187], v[94:97]
	v_mfma_f32_16x16x128_f8f6f4 v[90:93], v[10:17], v[180:187], v[90:93]
	v_mfma_f32_16x16x128_f8f6f4 v[82:85], v[2:9], v[188:195], v[82:85]
	v_mfma_f32_16x16x128_f8f6f4 v[74:77], v[10:17], v[188:195], v[74:77]
	v_mfma_f32_16x16x128_f8f6f4 v[66:69], v[2:9], v[196:203], v[66:69]
	v_mfma_f32_16x16x128_f8f6f4 v[58:61], v[10:17], v[196:203], v[58:61]
	v_mfma_f32_16x16x128_f8f6f4 v[50:53], v[2:9], v[204:211], v[50:53]
	v_mfma_f32_16x16x128_f8f6f4 v[42:45], v[10:17], v[204:211], v[42:45]
	v_mfma_f32_16x16x128_f8f6f4 v[86:89], v[18:25], v[180:187], v[86:89]
	v_mfma_f32_16x16x128_f8f6f4 v[78:81], v[26:33], v[180:187], v[78:81]
	v_mfma_f32_16x16x128_f8f6f4 v[70:73], v[18:25], v[188:195], v[70:73]
	v_mfma_f32_16x16x128_f8f6f4 v[62:65], v[26:33], v[188:195], v[62:65]
	v_mfma_f32_16x16x128_f8f6f4 v[54:57], v[18:25], v[196:203], v[54:57]
	v_mfma_f32_16x16x128_f8f6f4 v[46:49], v[26:33], v[196:203], v[46:49]
	v_mfma_f32_16x16x128_f8f6f4 v[38:41], v[18:25], v[204:211], v[38:41]
	v_mfma_f32_16x16x128_f8f6f4 v[34:37], v[26:33], v[204:211], v[34:37]
	s_setprio 0
	s_barrier
	s_add_i32 s33, s33, 2
	s_add_u32 vcc_lo, vcc_lo, 0x100
	s_addc_u32 vcc_hi, vcc_hi, 0
	s_cmp_gt_u32 s33, 5
	s_mov_b64 s[78:79], s[76:77]
	s_cbranch_scc0 .LBB0_190
	s_and_b64 vcc, exec, s[10:11]
	s_cbranch_vccz .LBB0_193
	s_barrier

.LBB0_217:
	s_cmp_lt_i32 s33, 0
	s_cbranch_scc1 .Lpeel1
	ds_read_b128 v[18:21], v168
	ds_read_b128 v[22:25], v168 offset:1024
	ds_read_b128 v[26:29], v168 offset:2048
	ds_read_b128 v[30:33], v168 offset:3072
	ds_read_b128 v[2:5], v169
	ds_read_b128 v[6:9], v169 offset:1024
	ds_read_b128 v[10:13], v169 offset:2048
	ds_read_b128 v[14:17], v169 offset:3072
	s_add_u32 s78, s80, 0x100
	s_addc_u32 s79, s81, 0
	s_cmp_eq_u32 s33, 4
	s_cselect_b32 s86, s57, s78
	s_cselect_b32 s87, s7, s79
	s_cselect_b32 s84, vcc_lo, vcc_hi
	s_cselect_b32 s85, s59, s89
	s_add_u32 s82, s86, 0x80
	s_addc_u32 s83, s87, 0
	ds_read_b128 v[176:179], v170
	ds_read_b128 v[180:183], v170 offset:1024
	ds_read_b128 v[184:187], v170 offset:2048
	ds_read_b128 v[188:191], v170 offset:3072
	ds_read_b128 v[192:195], v170 offset:4096
	ds_read_b128 v[196:199], v170 offset:5120
	ds_read_b128 v[200:203], v170 offset:6144
	ds_read_b128 v[204:207], v170 offset:7168
	s_add_u32 s80, s80, 0x20080
	s_addc_u32 s81, s81, 0
	s_mov_b32 s29, m0
	s_mov_b32 m0, s91
	s_nop 2
	global_load_lds_dwordx4 v162, s[80:81]
	s_mov_b32 m0, s29
	s_nop 0
	s_mov_b32 s29, m0
	s_mov_b32 m0, s92
	s_nop 2
	global_load_lds_dwordx4 v164, s[80:81]
	s_mov_b32 m0, s29
	s_waitcnt vmcnt(8)
	s_waitcnt lgkmcnt(0)
	s_setprio 1
	s_barrier
	v_mfma_f32_16x16x128_f8f6f4 v[158:161], v[18:25], v[176:183], v[158:161]
	v_mfma_f32_16x16x128_f8f6f4 v[154:157], v[26:33], v[176:183], v[154:157]
	v_mfma_f32_16x16x128_f8f6f4 v[146:149], v[18:25], v[184:191], v[146:149]
	v_mfma_f32_16x16x128_f8f6f4 v[138:141], v[26:33], v[184:191], v[138:141]
	v_mfma_f32_16x16x128_f8f6f4 v[130:133], v[18:25], v[192:199], v[130:133]
	v_mfma_f32_16x16x128_f8f6f4 v[122:125], v[26:33], v[192:199], v[122:125]
	v_mfma_f32_16x16x128_f8f6f4 v[114:117], v[18:25], v[200:207], v[114:117]
	v_mfma_f32_16x16x128_f8f6f4 v[106:109], v[26:33], v[200:207], v[106:109]
	v_mfma_f32_16x16x128_f8f6f4 v[150:153], v[2:9], v[176:183], v[150:153]
	v_mfma_f32_16x16x128_f8f6f4 v[142:145], v[10:17], v[176:183], v[142:145]
	v_mfma_f32_16x16x128_f8f6f4 v[134:137], v[2:9], v[184:191], v[134:137]
	v_mfma_f32_16x16x128_f8f6f4 v[126:129], v[10:17], v[184:191], v[126:129]
	v_mfma_f32_16x16x128_f8f6f4 v[118:121], v[2:9], v[192:199], v[118:121]
	v_mfma_f32_16x16x128_f8f6f4 v[110:113], v[10:17], v[192:199], v[110:113]
	v_mfma_f32_16x16x128_f8f6f4 v[102:105], v[2:9], v[200:207], v[102:105]
	v_mfma_f32_16x16x128_f8f6f4 v[98:101], v[10:17], v[200:207], v[98:101]
	s_setprio 0
	s_barrier
	ds_read_b128 v[176:179], v170 offset:16384
	ds_read_b128 v[180:183], v170 offset:17408
	ds_read_b128 v[184:187], v170 offset:18432
	ds_read_b128 v[188:191], v170 offset:19456
	ds_read_b128 v[192:195], v170 offset:20480
	ds_read_b128 v[196:199], v170 offset:21504
	ds_read_b128 v[200:203], v170 offset:22528
	ds_read_b128 v[204:207], v170 offset:23552
	s_mov_b32 s29, m0
	s_mov_b32 m0, s36
	s_nop 2
	global_load_lds_dwordx4 v163, s[84:85]
	s_mov_b32 m0, s29
	s_add_u32 s80, s84, 0x20000
	s_mov_b32 s29, m0
	s_mov_b32 m0, s37
	s_nop 2
	global_load_lds_dwordx4 v165, s[84:85]
	s_mov_b32 m0, s29
	s_addc_u32 s81, s85, 0
	s_mov_b32 s29, m0
	s_mov_b32 m0, s55
	s_nop 2
	global_load_lds_dwordx4 v163, s[80:81]
	s_mov_b32 m0, s29
	s_nop 0
	s_mov_b32 s29, m0
	s_mov_b32 m0, s77
	s_nop 2
	global_load_lds_dwordx4 v165, s[80:81]
	s_mov_b32 m0, s29
	s_nop 0
	s_mov_b32 s29, m0
	s_mov_b32 m0, s35
	s_nop 2
	global_load_lds_dwordx4 v162, s[86:87]
	s_mov_b32 m0, s29
	s_nop 0
	s_mov_b32 s29, m0
	s_mov_b32 m0, s88
	s_nop 2
	global_load_lds_dwordx4 v164, s[86:87]
	s_mov_b32 m0, s29
	s_waitcnt vmcnt(8)
	s_waitcnt lgkmcnt(0)
	s_setprio 1
	s_barrier
	v_mfma_f32_16x16x128_f8f6f4 v[94:97], v[18:25], v[176:183], v[94:97]
	v_mfma_f32_16x16x128_f8f6f4 v[90:93], v[26:33], v[176:183], v[90:93]
	v_mfma_f32_16x16x128_f8f6f4 v[82:85], v[18:25], v[184:191], v[82:85]
	v_mfma_f32_16x16x128_f8f6f4 v[74:77], v[26:33], v[184:191], v[74:77]
	v_mfma_f32_16x16x128_f8f6f4 v[66:69], v[18:25], v[192:199], v[66:69]
	v_mfma_f32_16x16x128_f8f6f4 v[58:61], v[26:33], v[192:199], v[58:61]
	v_mfma_f32_16x16x128_f8f6f4 v[50:53], v[18:25], v[200:207], v[50:53]
	v_mfma_f32_16x16x128_f8f6f4 v[42:45], v[26:33], v[200:207], v[42:45]
	v_mfma_f32_16x16x128_f8f6f4 v[86:89], v[2:9], v[176:183], v[86:89]
	v_mfma_f32_16x16x128_f8f6f4 v[78:81], v[10:17], v[176:183], v[78:81]
	v_mfma_f32_16x16x128_f8f6f4 v[70:73], v[2:9], v[184:191], v[70:73]
	v_mfma_f32_16x16x128_f8f6f4 v[62:65], v[10:17], v[184:191], v[62:65]
	v_mfma_f32_16x16x128_f8f6f4 v[54:57], v[2:9], v[192:199], v[54:57]
	v_mfma_f32_16x16x128_f8f6f4 v[46:49], v[10:17], v[192:199], v[46:49]
	v_mfma_f32_16x16x128_f8f6f4 v[38:41], v[2:9], v[200:207], v[38:41]
	v_mfma_f32_16x16x128_f8f6f4 v[34:37], v[10:17], v[200:207], v[34:37]
	s_setprio 0
	s_barrier
.Lmid1:
	ds_read_b128 v[2:5], v172
	ds_read_b128 v[6:9], v172 offset:1024
	ds_read_b128 v[10:13], v172 offset:2048
	ds_read_b128 v[14:17], v172 offset:3072
	ds_read_b128 v[18:21], v174
	ds_read_b128 v[22:25], v174 offset:1024
	ds_read_b128 v[26:29], v174 offset:2048
	ds_read_b128 v[30:33], v174 offset:3072
	ds_read_b128 v[176:179], v170 offset:32768
	ds_read_b128 v[180:183], v170 offset:33792
	ds_read_b128 v[184:187], v170 offset:34816
	ds_read_b128 v[188:191], v170 offset:35840
	ds_read_b128 v[192:195], v170 offset:36864
	ds_read_b128 v[196:199], v170 offset:37888
	ds_read_b128 v[200:203], v170 offset:38912
	ds_read_b128 v[204:207], v170 offset:39936
	s_add_u32 s80, s86, 0x20000
	s_addc_u32 s81, s87, 0
	s_mov_b32 s29, m0
	s_mov_b32 m0, s97
	s_nop 2
	global_load_lds_dwordx4 v162, s[80:81]
	s_mov_b32 m0, s29
	s_nop 0
	s_mov_b32 s29, m0
	s_mov_b32 m0, s3
	s_nop 2
	global_load_lds_dwordx4 v164, s[80:81]
	s_mov_b32 m0, s29
	s_waitcnt vmcnt(8)
	s_waitcnt lgkmcnt(0)
	s_setprio 1
	s_barrier
	v_mfma_f32_16x16x128_f8f6f4 v[158:161], v[2:9], v[176:183], v[158:161]
	v_mfma_f32_16x16x128_f8f6f4 v[154:157], v[10:17], v[176:183], v[154:157]
	v_mfma_f32_16x16x128_f8f6f4 v[146:149], v[2:9], v[184:191], v[146:149]
	v_mfma_f32_16x16x128_f8f6f4 v[138:141], v[10:17], v[184:191], v[138:141]
	v_mfma_f32_16x16x128_f8f6f4 v[130:133], v[2:9], v[192:199], v[130:133]
	v_mfma_f32_16x16x128_f8f6f4 v[122:125], v[10:17], v[192:199], v[122:125]
	v_mfma_f32_16x16x128_f8f6f4 v[114:117], v[2:9], v[200:207], v[114:117]
	v_mfma_f32_16x16x128_f8f6f4 v[106:109], v[10:17], v[200:207], v[106:109]
	v_mfma_f32_16x16x128_f8f6f4 v[150:153], v[18:25], v[176:183], v[150:153]
	v_mfma_f32_16x16x128_f8f6f4 v[142:145], v[26:33], v[176:183], v[142:145]
	v_mfma_f32_16x16x128_f8f6f4 v[134:137], v[18:25], v[184:191], v[134:137]
	v_mfma_f32_16x16x128_f8f6f4 v[126:129], v[26:33], v[184:191], v[126:129]
	v_mfma_f32_16x16x128_f8f6f4 v[118:121], v[18:25], v[192:199], v[118:121]
	v_mfma_f32_16x16x128_f8f6f4 v[110:113], v[26:33], v[192:199], v[110:113]
	v_mfma_f32_16x16x128_f8f6f4 v[102:105], v[18:25], v[200:207], v[102:105]
	v_mfma_f32_16x16x128_f8f6f4 v[98:101], v[26:33], v[200:207], v[98:101]
	s_setprio 0
	s_barrier
	ds_read_b128 v[176:179], v170 offset:49152
	ds_read_b128 v[180:183], v170 offset:50176
	ds_read_b128 v[184:187], v170 offset:51200
	ds_read_b128 v[188:191], v170 offset:52224
	ds_read_b128 v[192:195], v170 offset:53248
	ds_read_b128 v[196:199], v170 offset:54272
	ds_read_b128 v[200:203], v170 offset:55296
	ds_read_b128 v[204:207], v170 offset:56320
	s_add_u32 s80, s84, 0x80
	s_addc_u32 s81, s85, 0
	s_mov_b32 s29, m0
	s_mov_b32 m0, s90
	s_nop 2
	global_load_lds_dwordx4 v163, s[80:81]
	s_mov_b32 m0, s29
	s_nop 0
	s_mov_b32 s29, m0
	s_mov_b32 m0, s28
	s_nop 2
	global_load_lds_dwordx4 v165, s[80:81]
	s_mov_b32 m0, s29
	s_add_u32 s80, s84, 0x20080
	s_addc_u32 s81, s85, 0
	s_mov_b32 s29, m0
	s_mov_b32 m0, s94
	s_nop 2
	global_load_lds_dwordx4 v163, s[80:81]
	s_mov_b32 m0, s29
	s_nop 0
	s_mov_b32 s29, m0
	s_mov_b32 m0, s95
	s_nop 2
	global_load_lds_dwordx4 v165, s[80:81]
	s_mov_b32 m0, s29
	s_nop 0
	s_mov_b32 s29, m0
	s_mov_b32 m0, s93
	s_nop 2
	global_load_lds_dwordx4 v162, s[82:83]
	s_mov_b32 m0, s29
	s_nop 0
	s_mov_b32 s29, m0
	s_mov_b32 m0, s2
	s_nop 2
	global_load_lds_dwordx4 v164, s[82:83]
	s_mov_b32 m0, s29
	s_waitcnt vmcnt(8)
	s_waitcnt lgkmcnt(0)
	s_setprio 1
	s_barrier
	v_mfma_f32_16x16x128_f8f6f4 v[94:97], v[2:9], v[176:183], v[94:97]
	v_mfma_f32_16x16x128_f8f6f4 v[90:93], v[10:17], v[176:183], v[90:93]
	v_mfma_f32_16x16x128_f8f6f4 v[82:85], v[2:9], v[184:191], v[82:85]
	v_mfma_f32_16x16x128_f8f6f4 v[74:77], v[10:17], v[184:191], v[74:77]
	v_mfma_f32_16x16x128_f8f6f4 v[66:69], v[2:9], v[192:199], v[66:69]
	v_mfma_f32_16x16x128_f8f6f4 v[58:61], v[10:17], v[192:199], v[58:61]
	v_mfma_f32_16x16x128_f8f6f4 v[50:53], v[2:9], v[200:207], v[50:53]
	v_mfma_f32_16x16x128_f8f6f4 v[42:45], v[10:17], v[200:207], v[42:45]
	v_mfma_f32_16x16x128_f8f6f4 v[86:89], v[18:25], v[176:183], v[86:89]
	v_mfma_f32_16x16x128_f8f6f4 v[78:81], v[26:33], v[176:183], v[78:81]
	v_mfma_f32_16x16x128_f8f6f4 v[70:73], v[18:25], v[184:191], v[70:73]
	v_mfma_f32_16x16x128_f8f6f4 v[62:65], v[26:33], v[184:191], v[62:65]
	v_mfma_f32_16x16x128_f8f6f4 v[54:57], v[18:25], v[192:199], v[54:57]
	v_mfma_f32_16x16x128_f8f6f4 v[46:49], v[26:33], v[192:199], v[46:49]
	v_mfma_f32_16x16x128_f8f6f4 v[38:41], v[18:25], v[200:207], v[38:41]
	v_mfma_f32_16x16x128_f8f6f4 v[34:37], v[26:33], v[200:207], v[34:37]
	s_setprio 0
	s_cmp_lt_i32 s33, 4
	s_cbranch_scc1 .Lkb1_do
	s_cmp_lg_u64 s[10:11], 0
	s_cbranch_scc0 .Lkb1_skip

.Lpeel1:
	ds_read_b128 v[18:21], v168
	ds_read_b128 v[22:25], v168 offset:1024
	ds_read_b128 v[26:29], v168 offset:2048
	ds_read_b128 v[30:33], v168 offset:3072
	ds_read_b128 v[2:5], v169
	ds_read_b128 v[6:9], v169 offset:1024
	ds_read_b128 v[10:13], v169 offset:2048
	ds_read_b128 v[14:17], v169 offset:3072
	s_add_u32 s78, s80, 0x100
	s_addc_u32 s79, s81, 0
	s_cmp_eq_u32 s33, 4
	s_cselect_b32 s86, s57, s78
	s_cselect_b32 s87, s7, s79
	s_cselect_b32 s84, vcc_lo, vcc_hi
	s_cselect_b32 s85, s59, s89
	s_add_u32 s82, s86, 0x80
	s_addc_u32 s83, s87, 0
	ds_read_b128 v[176:179], v170
	ds_read_b128 v[180:183], v170 offset:1024
	ds_read_b128 v[184:187], v170 offset:2048
	ds_read_b128 v[188:191], v170 offset:3072
	ds_read_b128 v[192:195], v170 offset:4096
	ds_read_b128 v[196:199], v170 offset:5120
	ds_read_b128 v[200:203], v170 offset:6144
	ds_read_b128 v[204:207], v170 offset:7168
	s_add_u32 s80, s80, 0x20080
	s_addc_u32 s81, s81, 0
	s_mov_b32 s29, m0
	s_mov_b32 m0, s91
	s_nop 2
	global_load_lds_dwordx4 v162, s[80:81]
	s_mov_b32 m0, s29
	s_nop 0
	s_mov_b32 s29, m0
	s_mov_b32 m0, s92
	s_nop 2
	global_load_lds_dwordx4 v164, s[80:81]
	s_mov_b32 m0, s29
	s_waitcnt vmcnt(8)
	s_waitcnt lgkmcnt(0)
	s_setprio 1
	s_barrier
	v_mfma_f32_16x16x128_f8f6f4 v[158:161], v[18:25], v[176:183], 0
	v_mfma_f32_16x16x128_f8f6f4 v[154:157], v[26:33], v[176:183], 0
	v_mfma_f32_16x16x128_f8f6f4 v[146:149], v[18:25], v[184:191], 0
	v_mfma_f32_16x16x128_f8f6f4 v[138:141], v[26:33], v[184:191], 0
	v_mfma_f32_16x16x128_f8f6f4 v[130:133], v[18:25], v[192:199], 0
	v_mfma_f32_16x16x128_f8f6f4 v[122:125], v[26:33], v[192:199], 0
	v_mfma_f32_16x16x128_f8f6f4 v[114:117], v[18:25], v[200:207], 0
	v_mfma_f32_16x16x128_f8f6f4 v[106:109], v[26:33], v[200:207], 0
	v_mfma_f32_16x16x128_f8f6f4 v[150:153], v[2:9], v[176:183], 0
	v_mfma_f32_16x16x128_f8f6f4 v[142:145], v[10:17], v[176:183], 0
	v_mfma_f32_16x16x128_f8f6f4 v[134:137], v[2:9], v[184:191], 0
	v_mfma_f32_16x16x128_f8f6f4 v[126:129], v[10:17], v[184:191], 0
	v_mfma_f32_16x16x128_f8f6f4 v[118:121], v[2:9], v[192:199], 0
	v_mfma_f32_16x16x128_f8f6f4 v[110:113], v[10:17], v[192:199], 0
	v_mfma_f32_16x16x128_f8f6f4 v[102:105], v[2:9], v[200:207], 0
	v_mfma_f32_16x16x128_f8f6f4 v[98:101], v[10:17], v[200:207], 0
	s_setprio 0
	s_barrier
	ds_read_b128 v[176:179], v170 offset:16384
	ds_read_b128 v[180:183], v170 offset:17408
	ds_read_b128 v[184:187], v170 offset:18432
	ds_read_b128 v[188:191], v170 offset:19456
	ds_read_b128 v[192:195], v170 offset:20480
	ds_read_b128 v[196:199], v170 offset:21504
	ds_read_b128 v[200:203], v170 offset:22528
	ds_read_b128 v[204:207], v170 offset:23552
	s_mov_b32 s29, m0
	s_mov_b32 m0, s36
	s_nop 2
	global_load_lds_dwordx4 v163, s[84:85]
	s_mov_b32 m0, s29
	s_add_u32 s80, s84, 0x20000
	s_mov_b32 s29, m0
	s_mov_b32 m0, s37
	s_nop 2
	global_load_lds_dwordx4 v165, s[84:85]
	s_mov_b32 m0, s29
	s_addc_u32 s81, s85, 0
	s_mov_b32 s29, m0
	s_mov_b32 m0, s55
	s_nop 2
	global_load_lds_dwordx4 v163, s[80:81]
	s_mov_b32 m0, s29
	s_nop 0
	s_mov_b32 s29, m0
	s_mov_b32 m0, s77
	s_nop 2
	global_load_lds_dwordx4 v165, s[80:81]
	s_mov_b32 m0, s29
	s_nop 0
	s_mov_b32 s29, m0
	s_mov_b32 m0, s35
	s_nop 2
	global_load_lds_dwordx4 v162, s[86:87]
	s_mov_b32 m0, s29
	s_nop 0
	s_mov_b32 s29, m0
	s_mov_b32 m0, s88
	s_nop 2
	global_load_lds_dwordx4 v164, s[86:87]
	s_mov_b32 m0, s29
	s_waitcnt vmcnt(8)
	s_waitcnt lgkmcnt(0)
	s_setprio 1
	s_barrier
	v_mfma_f32_16x16x128_f8f6f4 v[94:97], v[18:25], v[176:183], 0
	v_mfma_f32_16x16x128_f8f6f4 v[90:93], v[26:33], v[176:183], 0
	v_mfma_f32_16x16x128_f8f6f4 v[82:85], v[18:25], v[184:191], 0
	v_mfma_f32_16x16x128_f8f6f4 v[74:77], v[26:33], v[184:191], 0
	v_mfma_f32_16x16x128_f8f6f4 v[66:69], v[18:25], v[192:199], 0
	v_mfma_f32_16x16x128_f8f6f4 v[58:61], v[26:33], v[192:199], 0
	v_mfma_f32_16x16x128_f8f6f4 v[50:53], v[18:25], v[200:207], 0
	v_mfma_f32_16x16x128_f8f6f4 v[42:45], v[26:33], v[200:207], 0
	v_mfma_f32_16x16x128_f8f6f4 v[86:89], v[2:9], v[176:183], 0
	v_mfma_f32_16x16x128_f8f6f4 v[78:81], v[10:17], v[176:183], 0
	v_mfma_f32_16x16x128_f8f6f4 v[70:73], v[2:9], v[184:191], 0
	v_mfma_f32_16x16x128_f8f6f4 v[62:65], v[10:17], v[184:191], 0
	v_mfma_f32_16x16x128_f8f6f4 v[54:57], v[2:9], v[192:199], 0
	v_mfma_f32_16x16x128_f8f6f4 v[46:49], v[10:17], v[192:199], 0
	v_mfma_f32_16x16x128_f8f6f4 v[38:41], v[2:9], v[200:207], 0
	v_mfma_f32_16x16x128_f8f6f4 v[34:37], v[10:17], v[200:207], 0
	s_setprio 0
	s_barrier
	s_branch .Lmid1

.Lpeel1046:
	ds_read_b128 v[136:139], v172
	ds_read_b128 v[140:143], v172 offset:1024
	ds_read_b128 v[144:147], v172 offset:2048
	ds_read_b128 v[148:151], v172 offset:3072
	ds_read_b128 v[152:155], v173
	ds_read_b128 v[156:159], v173 offset:1024
	ds_read_b128 v[160:163], v173 offset:2048
	ds_read_b128 v[178:181], v173 offset:3072
	s_add_u32 s25, s64, s56
	s_addc_u32 s33, s65, s57
	s_add_u32 s66, s25, 0x100
	s_addc_u32 s67, s33, 0
	s_add_u32 s23, s62, s56
	s_addc_u32 s24, s63, s57
	s_add_u32 s28, s23, 0x100
	s_addc_u32 s29, s24, 0
	s_add_u32 s58, s25, 0x180
	s_addc_u32 s59, s33, 0
	ds_read_b128 v[182:185], v174
	ds_read_b128 v[186:189], v174 offset:1024
	ds_read_b128 v[190:193], v174 offset:2048
	ds_read_b128 v[194:197], v174 offset:3072
	ds_read_b128 v[198:201], v174 offset:4096
	ds_read_b128 v[202:205], v174 offset:5120
	ds_read_b128 v[206:209], v174 offset:6144
	ds_read_b128 v[210:213], v174 offset:7168
	s_add_u32 s30, s25, 0x40080
	s_addc_u32 s31, s33, 0
	s_mov_b32 s36, m0
	s_mov_b32 m0, s26
	s_nop 2
	global_load_lds_dwordx4 v165, s[30:31]
	s_mov_b32 m0, s36
	s_nop 0
	s_mov_b32 s36, m0
	s_mov_b32 m0, s27
	s_nop 2
	global_load_lds_dwordx4 v167, s[30:31]
	s_mov_b32 m0, s36
	s_waitcnt vmcnt(8)
	s_waitcnt lgkmcnt(0)
	s_setprio 1
	s_barrier
	v_mfma_f32_16x16x32_bf16 v[26:29], v[136:139], v[182:185], 0
	v_mfma_f32_16x16x32_bf16 v[30:33], v[144:147], v[182:185], 0
	v_mfma_f32_16x16x32_bf16 v[50:53], v[136:139], v[190:193], 0
	v_mfma_f32_16x16x32_bf16 v[54:57], v[144:147], v[190:193], 0
	v_mfma_f32_16x16x32_bf16 v[74:77], v[136:139], v[198:201], 0
	v_mfma_f32_16x16x32_bf16 v[78:81], v[144:147], v[198:201], 0
	v_mfma_f32_16x16x32_bf16 v[94:97], v[136:139], v[206:209], 0
	v_mfma_f32_16x16x32_bf16 v[102:105], v[144:147], v[206:209], 0
	v_mfma_f32_16x16x32_bf16 v[26:29], v[140:143], v[186:189], v[26:29]
	v_mfma_f32_16x16x32_bf16 v[30:33], v[148:151], v[186:189], v[30:33]
	v_mfma_f32_16x16x32_bf16 v[50:53], v[140:143], v[194:197], v[50:53]
	v_mfma_f32_16x16x32_bf16 v[54:57], v[148:151], v[194:197], v[54:57]
	v_mfma_f32_16x16x32_bf16 v[74:77], v[140:143], v[202:205], v[74:77]
	v_mfma_f32_16x16x32_bf16 v[78:81], v[148:151], v[202:205], v[78:81]
	v_mfma_f32_16x16x32_bf16 v[94:97], v[140:143], v[210:213], v[94:97]
	v_mfma_f32_16x16x32_bf16 v[102:105], v[148:151], v[210:213], v[102:105]
	v_mfma_f32_16x16x32_bf16 v[38:41], v[152:155], v[182:185], 0
	v_mfma_f32_16x16x32_bf16 v[42:45], v[160:163], v[182:185], 0
	v_mfma_f32_16x16x32_bf16 v[62:65], v[152:155], v[190:193], 0
	v_mfma_f32_16x16x32_bf16 v[66:69], v[160:163], v[190:193], 0
	v_mfma_f32_16x16x32_bf16 v[82:85], v[152:155], v[198:201], 0
	v_mfma_f32_16x16x32_bf16 v[90:93], v[160:163], v[198:201], 0
	v_mfma_f32_16x16x32_bf16 v[106:109], v[152:155], v[206:209], 0
	v_mfma_f32_16x16x32_bf16 v[114:117], v[160:163], v[206:209], 0
	v_mfma_f32_16x16x32_bf16 v[38:41], v[156:159], v[186:189], v[38:41]
	v_mfma_f32_16x16x32_bf16 v[42:45], v[178:181], v[186:189], v[42:45]
	v_mfma_f32_16x16x32_bf16 v[62:65], v[156:159], v[194:197], v[62:65]
	v_mfma_f32_16x16x32_bf16 v[66:69], v[178:181], v[194:197], v[66:69]
	v_mfma_f32_16x16x32_bf16 v[82:85], v[156:159], v[202:205], v[82:85]
	v_mfma_f32_16x16x32_bf16 v[90:93], v[178:181], v[202:205], v[90:93]
	v_mfma_f32_16x16x32_bf16 v[106:109], v[156:159], v[210:213], v[106:109]
	v_mfma_f32_16x16x32_bf16 v[114:117], v[178:181], v[210:213], v[114:117]
	s_setprio 0
	s_barrier
	ds_read_b128 v[182:185], v174 offset:16384
	ds_read_b128 v[186:189], v174 offset:17408
	ds_read_b128 v[190:193], v174 offset:18432
	ds_read_b128 v[194:197], v174 offset:19456
	ds_read_b128 v[198:201], v174 offset:20480
	ds_read_b128 v[202:205], v174 offset:21504
	ds_read_b128 v[206:209], v174 offset:22528
	ds_read_b128 v[210:213], v174 offset:23552
	s_mov_b32 s30, m0
	s_mov_b32 m0, s80
	s_nop 2
	global_load_lds_dwordx4 v166, s[28:29]
	s_mov_b32 m0, s30
	s_nop 0
	s_mov_b32 s30, m0
	s_mov_b32 m0, s81
	s_nop 2
	global_load_lds_dwordx4 v168, s[28:29]
	s_mov_b32 m0, s30
	s_add_u32 s28, s23, 0x40100
	s_addc_u32 s29, s24, 0
	s_mov_b32 s30, m0
	s_mov_b32 m0, s82
	s_nop 2
	global_load_lds_dwordx4 v166, s[28:29]
	s_mov_b32 m0, s30
	s_nop 0
	s_mov_b32 s30, m0
	s_mov_b32 m0, s83
	s_nop 2
	global_load_lds_dwordx4 v168, s[28:29]
	s_mov_b32 m0, s30
	s_mov_b32 s28, m0
	s_mov_b32 m0, s79
	s_nop 2
	global_load_lds_dwordx4 v165, s[66:67]
	s_mov_b32 m0, s28
	s_nop 0
	s_mov_b32 s28, m0
	s_mov_b32 m0, s84
	s_nop 2
	global_load_lds_dwordx4 v167, s[66:67]
	s_mov_b32 m0, s28
	s_waitcnt vmcnt(8)
	s_waitcnt lgkmcnt(0)
	s_setprio 1
	s_barrier
	v_mfma_f32_16x16x32_bf16 v[118:121], v[136:139], v[182:185], 0
	v_mfma_f32_16x16x32_bf16 v[126:129], v[144:147], v[182:185], 0
	v_mfma_f32_16x16x32_bf16 v[98:101], v[136:139], v[190:193], 0
	v_mfma_f32_16x16x32_bf16 v[86:89], v[144:147], v[190:193], 0
	v_mfma_f32_16x16x32_bf16 v[46:49], v[136:139], v[198:201], 0
	v_mfma_f32_16x16x32_bf16 v[34:37], v[144:147], v[198:201], 0
	v_mfma_f32_16x16x32_bf16 v[14:17], v[136:139], v[206:209], 0
	v_mfma_f32_16x16x32_bf16 v[10:13], v[144:147], v[206:209], 0
	v_mfma_f32_16x16x32_bf16 v[118:121], v[140:143], v[186:189], v[118:121]
	v_mfma_f32_16x16x32_bf16 v[126:129], v[148:151], v[186:189], v[126:129]
	v_mfma_f32_16x16x32_bf16 v[98:101], v[140:143], v[194:197], v[98:101]
	v_mfma_f32_16x16x32_bf16 v[86:89], v[148:151], v[194:197], v[86:89]
	v_mfma_f32_16x16x32_bf16 v[46:49], v[140:143], v[202:205], v[46:49]
	v_mfma_f32_16x16x32_bf16 v[34:37], v[148:151], v[202:205], v[34:37]
	v_mfma_f32_16x16x32_bf16 v[14:17], v[140:143], v[210:213], v[14:17]
	v_mfma_f32_16x16x32_bf16 v[10:13], v[148:151], v[210:213], v[10:13]
	v_mfma_f32_16x16x32_bf16 v[122:125], v[152:155], v[182:185], 0
	v_mfma_f32_16x16x32_bf16 v[110:113], v[160:163], v[182:185], 0
	v_mfma_f32_16x16x32_bf16 v[70:73], v[152:155], v[190:193], 0
	v_mfma_f32_16x16x32_bf16 v[58:61], v[160:163], v[190:193], 0
	v_mfma_f32_16x16x32_bf16 v[22:25], v[152:155], v[198:201], 0
	v_mfma_f32_16x16x32_bf16 v[18:21], v[160:163], v[198:201], 0
	v_mfma_f32_16x16x32_bf16 v[6:9], v[152:155], v[206:209], 0
	v_mfma_f32_16x16x32_bf16 v[2:5], v[160:163], v[206:209], 0
	v_mfma_f32_16x16x32_bf16 v[122:125], v[156:159], v[186:189], v[122:125]
	v_mfma_f32_16x16x32_bf16 v[110:113], v[178:181], v[186:189], v[110:113]
	v_mfma_f32_16x16x32_bf16 v[70:73], v[156:159], v[194:197], v[70:73]
	v_mfma_f32_16x16x32_bf16 v[58:61], v[178:181], v[194:197], v[58:61]
	v_mfma_f32_16x16x32_bf16 v[22:25], v[156:159], v[202:205], v[22:25]
	v_mfma_f32_16x16x32_bf16 v[18:21], v[178:181], v[202:205], v[18:21]
	v_mfma_f32_16x16x32_bf16 v[6:9], v[156:159], v[210:213], v[6:9]
	v_mfma_f32_16x16x32_bf16 v[2:5], v[178:181], v[210:213], v[2:5]
	s_setprio 0
	s_barrier
	s_branch .Lmid1046
.LBB0_1046:
	ds_read_b128 v[136:139], v172
	ds_read_b128 v[140:143], v172 offset:1024
	ds_read_b128 v[144:147], v172 offset:2048
	ds_read_b128 v[148:151], v172 offset:3072
	ds_read_b128 v[152:155], v173
	ds_read_b128 v[156:159], v173 offset:1024
	ds_read_b128 v[160:163], v173 offset:2048
	ds_read_b128 v[178:181], v173 offset:3072
	s_add_u32 s25, s64, s56
	s_addc_u32 s33, s65, s57
	s_add_u32 s66, s25, 0x100
	s_addc_u32 s67, s33, 0
	s_add_u32 s23, s62, s56
	s_addc_u32 s24, s63, s57
	s_add_u32 s28, s23, 0x100
	s_addc_u32 s29, s24, 0
	s_add_u32 s58, s25, 0x180
	s_addc_u32 s59, s33, 0
	ds_read_b128 v[182:185], v174
	ds_read_b128 v[186:189], v174 offset:1024
	ds_read_b128 v[190:193], v174 offset:2048
	ds_read_b128 v[194:197], v174 offset:3072
	ds_read_b128 v[198:201], v174 offset:4096
	ds_read_b128 v[202:205], v174 offset:5120
	ds_read_b128 v[206:209], v174 offset:6144
	ds_read_b128 v[210:213], v174 offset:7168
	s_add_u32 s30, s25, 0x40080
	s_addc_u32 s31, s33, 0
	s_mov_b32 s36, m0
	s_mov_b32 m0, s26
	s_nop 2
	global_load_lds_dwordx4 v165, s[30:31]
	s_mov_b32 m0, s36
	s_nop 0
	s_mov_b32 s36, m0
	s_mov_b32 m0, s27
	s_nop 2
	global_load_lds_dwordx4 v167, s[30:31]
	s_mov_b32 m0, s36
	s_waitcnt vmcnt(8)
	s_waitcnt lgkmcnt(0)
	s_setprio 1
	s_barrier
	v_mfma_f32_16x16x32_bf16 v[26:29], v[136:139], v[182:185], v[26:29]
	v_mfma_f32_16x16x32_bf16 v[30:33], v[144:147], v[182:185], v[30:33]
	v_mfma_f32_16x16x32_bf16 v[50:53], v[136:139], v[190:193], v[50:53]
	v_mfma_f32_16x16x32_bf16 v[54:57], v[144:147], v[190:193], v[54:57]
	v_mfma_f32_16x16x32_bf16 v[74:77], v[136:139], v[198:201], v[74:77]
	v_mfma_f32_16x16x32_bf16 v[78:81], v[144:147], v[198:201], v[78:81]
	v_mfma_f32_16x16x32_bf16 v[94:97], v[136:139], v[206:209], v[94:97]
	v_mfma_f32_16x16x32_bf16 v[102:105], v[144:147], v[206:209], v[102:105]
	v_mfma_f32_16x16x32_bf16 v[26:29], v[140:143], v[186:189], v[26:29]
	v_mfma_f32_16x16x32_bf16 v[30:33], v[148:151], v[186:189], v[30:33]
	v_mfma_f32_16x16x32_bf16 v[50:53], v[140:143], v[194:197], v[50:53]
	v_mfma_f32_16x16x32_bf16 v[54:57], v[148:151], v[194:197], v[54:57]
	v_mfma_f32_16x16x32_bf16 v[74:77], v[140:143], v[202:205], v[74:77]
	v_mfma_f32_16x16x32_bf16 v[78:81], v[148:151], v[202:205], v[78:81]
	v_mfma_f32_16x16x32_bf16 v[94:97], v[140:143], v[210:213], v[94:97]
	v_mfma_f32_16x16x32_bf16 v[102:105], v[148:151], v[210:213], v[102:105]
	v_mfma_f32_16x16x32_bf16 v[38:41], v[152:155], v[182:185], v[38:41]
	v_mfma_f32_16x16x32_bf16 v[42:45], v[160:163], v[182:185], v[42:45]
	v_mfma_f32_16x16x32_bf16 v[62:65], v[152:155], v[190:193], v[62:65]
	v_mfma_f32_16x16x32_bf16 v[66:69], v[160:163], v[190:193], v[66:69]
	v_mfma_f32_16x16x32_bf16 v[82:85], v[152:155], v[198:201], v[82:85]
	v_mfma_f32_16x16x32_bf16 v[90:93], v[160:163], v[198:201], v[90:93]
	v_mfma_f32_16x16x32_bf16 v[106:109], v[152:155], v[206:209], v[106:109]
	v_mfma_f32_16x16x32_bf16 v[114:117], v[160:163], v[206:209], v[114:117]
	v_mfma_f32_16x16x32_bf16 v[38:41], v[156:159], v[186:189], v[38:41]
	v_mfma_f32_16x16x32_bf16 v[42:45], v[178:181], v[186:189], v[42:45]
	v_mfma_f32_16x16x32_bf16 v[62:65], v[156:159], v[194:197], v[62:65]
	v_mfma_f32_16x16x32_bf16 v[66:69], v[178:181], v[194:197], v[66:69]
	v_mfma_f32_16x16x32_bf16 v[82:85], v[156:159], v[202:205], v[82:85]
	v_mfma_f32_16x16x32_bf16 v[90:93], v[178:181], v[202:205], v[90:93]
	v_mfma_f32_16x16x32_bf16 v[106:109], v[156:159], v[210:213], v[106:109]
	v_mfma_f32_16x16x32_bf16 v[114:117], v[178:181], v[210:213], v[114:117]
	s_setprio 0
	s_barrier
	ds_read_b128 v[182:185], v174 offset:16384
	ds_read_b128 v[186:189], v174 offset:17408
	ds_read_b128 v[190:193], v174 offset:18432
	ds_read_b128 v[194:197], v174 offset:19456
	ds_read_b128 v[198:201], v174 offset:20480
	ds_read_b128 v[202:205], v174 offset:21504
	ds_read_b128 v[206:209], v174 offset:22528
	ds_read_b128 v[210:213], v174 offset:23552
	s_mov_b32 s30, m0
	s_mov_b32 m0, s80
	s_nop 2
	global_load_lds_dwordx4 v166, s[28:29]
	s_mov_b32 m0, s30
	s_nop 0
	s_mov_b32 s30, m0
	s_mov_b32 m0, s81
	s_nop 2
	global_load_lds_dwordx4 v168, s[28:29]
	s_mov_b32 m0, s30
	s_add_u32 s28, s23, 0x40100
	s_addc_u32 s29, s24, 0
	s_mov_b32 s30, m0
	s_mov_b32 m0, s82
	s_nop 2
	global_load_lds_dwordx4 v166, s[28:29]
	s_mov_b32 m0, s30
	s_nop 0
	s_mov_b32 s30, m0
	s_mov_b32 m0, s83
	s_nop 2
	global_load_lds_dwordx4 v168, s[28:29]
	s_mov_b32 m0, s30
	s_mov_b32 s28, m0
	s_mov_b32 m0, s79
	s_nop 2
	global_load_lds_dwordx4 v165, s[66:67]
	s_mov_b32 m0, s28
	s_nop 0
	s_mov_b32 s28, m0
	s_mov_b32 m0, s84
	s_nop 2
	global_load_lds_dwordx4 v167, s[66:67]
	s_mov_b32 m0, s28
	s_waitcnt vmcnt(8)
	s_waitcnt lgkmcnt(0)
	s_setprio 1
	s_barrier
	v_mfma_f32_16x16x32_bf16 v[118:121], v[136:139], v[182:185], v[118:121]
	v_mfma_f32_16x16x32_bf16 v[126:129], v[144:147], v[182:185], v[126:129]
	v_mfma_f32_16x16x32_bf16 v[98:101], v[136:139], v[190:193], v[98:101]
	v_mfma_f32_16x16x32_bf16 v[86:89], v[144:147], v[190:193], v[86:89]
	v_mfma_f32_16x16x32_bf16 v[46:49], v[136:139], v[198:201], v[46:49]
	v_mfma_f32_16x16x32_bf16 v[34:37], v[144:147], v[198:201], v[34:37]
	v_mfma_f32_16x16x32_bf16 v[14:17], v[136:139], v[206:209], v[14:17]
	v_mfma_f32_16x16x32_bf16 v[10:13], v[144:147], v[206:209], v[10:13]
	v_mfma_f32_16x16x32_bf16 v[118:121], v[140:143], v[186:189], v[118:121]
	v_mfma_f32_16x16x32_bf16 v[126:129], v[148:151], v[186:189], v[126:129]
	v_mfma_f32_16x16x32_bf16 v[98:101], v[140:143], v[194:197], v[98:101]
	v_mfma_f32_16x16x32_bf16 v[86:89], v[148:151], v[194:197], v[86:89]
	v_mfma_f32_16x16x32_bf16 v[46:49], v[140:143], v[202:205], v[46:49]
	v_mfma_f32_16x16x32_bf16 v[34:37], v[148:151], v[202:205], v[34:37]
	v_mfma_f32_16x16x32_bf16 v[14:17], v[140:143], v[210:213], v[14:17]
	v_mfma_f32_16x16x32_bf16 v[10:13], v[148:151], v[210:213], v[10:13]
	v_mfma_f32_16x16x32_bf16 v[122:125], v[152:155], v[182:185], v[122:125]
	v_mfma_f32_16x16x32_bf16 v[110:113], v[160:163], v[182:185], v[110:113]
	v_mfma_f32_16x16x32_bf16 v[70:73], v[152:155], v[190:193], v[70:73]
	v_mfma_f32_16x16x32_bf16 v[58:61], v[160:163], v[190:193], v[58:61]
	v_mfma_f32_16x16x32_bf16 v[22:25], v[152:155], v[198:201], v[22:25]
	v_mfma_f32_16x16x32_bf16 v[18:21], v[160:163], v[198:201], v[18:21]
	v_mfma_f32_16x16x32_bf16 v[6:9], v[152:155], v[206:209], v[6:9]
	v_mfma_f32_16x16x32_bf16 v[2:5], v[160:163], v[206:209], v[2:5]
	v_mfma_f32_16x16x32_bf16 v[122:125], v[156:159], v[186:189], v[122:125]
	v_mfma_f32_16x16x32_bf16 v[110:113], v[178:181], v[186:189], v[110:113]
	v_mfma_f32_16x16x32_bf16 v[70:73], v[156:159], v[194:197], v[70:73]
	v_mfma_f32_16x16x32_bf16 v[58:61], v[178:181], v[194:197], v[58:61]
	v_mfma_f32_16x16x32_bf16 v[22:25], v[156:159], v[202:205], v[22:25]
	v_mfma_f32_16x16x32_bf16 v[18:21], v[178:181], v[202:205], v[18:21]
	v_mfma_f32_16x16x32_bf16 v[6:9], v[156:159], v[210:213], v[6:9]
	v_mfma_f32_16x16x32_bf16 v[2:5], v[178:181], v[210:213], v[2:5]
	s_setprio 0
	s_barrier
.Lmid1046:
	ds_read_b128 v[136:139], v175
	ds_read_b128 v[140:143], v175 offset:1024
	ds_read_b128 v[144:147], v175 offset:2048
	ds_read_b128 v[148:151], v175 offset:3072
	ds_read_b128 v[152:155], v176
	ds_read_b128 v[156:159], v176 offset:1024
	ds_read_b128 v[160:163], v176 offset:2048
	ds_read_b128 v[178:181], v176 offset:3072
	ds_read_b128 v[182:185], v174 offset:32768
	ds_read_b128 v[186:189], v174 offset:33792
	ds_read_b128 v[190:193], v174 offset:34816
	ds_read_b128 v[194:197], v174 offset:35840
	ds_read_b128 v[198:201], v174 offset:36864
	ds_read_b128 v[202:205], v174 offset:37888
	ds_read_b128 v[206:209], v174 offset:38912
	ds_read_b128 v[210:213], v174 offset:39936
	s_add_u32 s28, s25, 0x40100
	s_addc_u32 s29, s33, 0
	s_mov_b32 s25, m0
	s_mov_b32 m0, s85
	s_nop 2
	global_load_lds_dwordx4 v165, s[28:29]
	s_mov_b32 m0, s25
	s_nop 0
	s_mov_b32 s25, m0
	s_mov_b32 m0, s86
	s_nop 2
	global_load_lds_dwordx4 v167, s[28:29]
	s_mov_b32 m0, s25
	s_waitcnt vmcnt(8)
	s_waitcnt lgkmcnt(0)
	s_setprio 1
	s_barrier
	v_mfma_f32_16x16x32_bf16 v[26:29], v[136:139], v[182:185], v[26:29]
	v_mfma_f32_16x16x32_bf16 v[30:33], v[144:147], v[182:185], v[30:33]
	v_mfma_f32_16x16x32_bf16 v[50:53], v[136:139], v[190:193], v[50:53]
	v_mfma_f32_16x16x32_bf16 v[54:57], v[144:147], v[190:193], v[54:57]
	v_mfma_f32_16x16x32_bf16 v[74:77], v[136:139], v[198:201], v[74:77]
	v_mfma_f32_16x16x32_bf16 v[78:81], v[144:147], v[198:201], v[78:81]
	v_mfma_f32_16x16x32_bf16 v[94:97], v[136:139], v[206:209], v[94:97]
	v_mfma_f32_16x16x32_bf16 v[102:105], v[144:147], v[206:209], v[102:105]
	v_mfma_f32_16x16x32_bf16 v[26:29], v[140:143], v[186:189], v[26:29]
	v_mfma_f32_16x16x32_bf16 v[30:33], v[148:151], v[186:189], v[30:33]
	v_mfma_f32_16x16x32_bf16 v[50:53], v[140:143], v[194:197], v[50:53]
	v_mfma_f32_16x16x32_bf16 v[54:57], v[148:151], v[194:197], v[54:57]
	v_mfma_f32_16x16x32_bf16 v[74:77], v[140:143], v[202:205], v[74:77]
	v_mfma_f32_16x16x32_bf16 v[78:81], v[148:151], v[202:205], v[78:81]
	v_mfma_f32_16x16x32_bf16 v[94:97], v[140:143], v[210:213], v[94:97]
	v_mfma_f32_16x16x32_bf16 v[102:105], v[148:151], v[210:213], v[102:105]
	v_mfma_f32_16x16x32_bf16 v[38:41], v[152:155], v[182:185], v[38:41]
	v_mfma_f32_16x16x32_bf16 v[42:45], v[160:163], v[182:185], v[42:45]
	v_mfma_f32_16x16x32_bf16 v[62:65], v[152:155], v[190:193], v[62:65]
	v_mfma_f32_16x16x32_bf16 v[66:69], v[160:163], v[190:193], v[66:69]
	v_mfma_f32_16x16x32_bf16 v[82:85], v[152:155], v[198:201], v[82:85]
	v_mfma_f32_16x16x32_bf16 v[90:93], v[160:163], v[198:201], v[90:93]
	v_mfma_f32_16x16x32_bf16 v[106:109], v[152:155], v[206:209], v[106:109]
	v_mfma_f32_16x16x32_bf16 v[114:117], v[160:163], v[206:209], v[114:117]
	v_mfma_f32_16x16x32_bf16 v[38:41], v[156:159], v[186:189], v[38:41]
	v_mfma_f32_16x16x32_bf16 v[42:45], v[178:181], v[186:189], v[42:45]
	v_mfma_f32_16x16x32_bf16 v[62:65], v[156:159], v[194:197], v[62:65]
	v_mfma_f32_16x16x32_bf16 v[66:69], v[178:181], v[194:197], v[66:69]
	v_mfma_f32_16x16x32_bf16 v[82:85], v[156:159], v[202:205], v[82:85]
	v_mfma_f32_16x16x32_bf16 v[90:93], v[178:181], v[202:205], v[90:93]
	v_mfma_f32_16x16x32_bf16 v[106:109], v[156:159], v[210:213], v[106:109]
	v_mfma_f32_16x16x32_bf16 v[114:117], v[178:181], v[210:213], v[114:117]
	s_setprio 0
	s_barrier
	ds_read_b128 v[182:185], v174 offset:49152
	ds_read_b128 v[186:189], v174 offset:50176
	ds_read_b128 v[190:193], v174 offset:51200
	ds_read_b128 v[194:197], v174 offset:52224
	ds_read_b128 v[198:201], v174 offset:53248
	ds_read_b128 v[202:205], v174 offset:54272
	ds_read_b128 v[206:209], v174 offset:55296
	ds_read_b128 v[210:213], v174 offset:56320
	s_add_u32 s28, s23, 0x180
	s_addc_u32 s29, s24, 0
	s_mov_b32 s25, m0
	s_mov_b32 m0, s92
	s_nop 2
	global_load_lds_dwordx4 v166, s[28:29]
	s_mov_b32 m0, s25
	s_nop 0
	s_mov_b32 s25, m0
	s_mov_b32 m0, s93
	s_nop 2
	global_load_lds_dwordx4 v168, s[28:29]
	s_mov_b32 m0, s25
	s_add_u32 s28, s23, 0x40180
	s_addc_u32 s29, s24, 0
	s_mov_b32 s23, m0
	s_mov_b32 m0, s96
	s_nop 2
	global_load_lds_dwordx4 v166, s[28:29]
	s_mov_b32 m0, s23
	s_nop 0
	s_mov_b32 s23, m0
	s_mov_b32 m0, s97
	s_nop 2
	global_load_lds_dwordx4 v168, s[28:29]
	s_mov_b32 m0, s23
	s_nop 0
	s_mov_b32 s23, m0
	s_mov_b32 m0, s94
	s_nop 2
	global_load_lds_dwordx4 v165, s[58:59]
	s_mov_b32 m0, s23
	s_nop 0
	s_mov_b32 s23, m0
	s_mov_b32 m0, s95
	s_nop 2
	global_load_lds_dwordx4 v167, s[58:59]
	s_mov_b32 m0, s23
	s_waitcnt vmcnt(8)
	s_waitcnt lgkmcnt(0)
	s_setprio 1
	s_barrier
	v_mfma_f32_16x16x32_bf16 v[118:121], v[136:139], v[182:185], v[118:121]
	v_mfma_f32_16x16x32_bf16 v[126:129], v[144:147], v[182:185], v[126:129]
	v_mfma_f32_16x16x32_bf16 v[98:101], v[136:139], v[190:193], v[98:101]
	v_mfma_f32_16x16x32_bf16 v[86:89], v[144:147], v[190:193], v[86:89]
	v_mfma_f32_16x16x32_bf16 v[46:49], v[136:139], v[198:201], v[46:49]
	v_mfma_f32_16x16x32_bf16 v[34:37], v[144:147], v[198:201], v[34:37]
	v_mfma_f32_16x16x32_bf16 v[14:17], v[136:139], v[206:209], v[14:17]
	v_mfma_f32_16x16x32_bf16 v[10:13], v[144:147], v[206:209], v[10:13]
	v_mfma_f32_16x16x32_bf16 v[118:121], v[140:143], v[186:189], v[118:121]
	v_mfma_f32_16x16x32_bf16 v[126:129], v[148:151], v[186:189], v[126:129]
	v_mfma_f32_16x16x32_bf16 v[98:101], v[140:143], v[194:197], v[98:101]
	v_mfma_f32_16x16x32_bf16 v[86:89], v[148:151], v[194:197], v[86:89]
	v_mfma_f32_16x16x32_bf16 v[46:49], v[140:143], v[202:205], v[46:49]
	v_mfma_f32_16x16x32_bf16 v[34:37], v[148:151], v[202:205], v[34:37]
	v_mfma_f32_16x16x32_bf16 v[14:17], v[140:143], v[210:213], v[14:17]
	v_mfma_f32_16x16x32_bf16 v[10:13], v[148:151], v[210:213], v[10:13]
	v_mfma_f32_16x16x32_bf16 v[122:125], v[152:155], v[182:185], v[122:125]
	v_mfma_f32_16x16x32_bf16 v[110:113], v[160:163], v[182:185], v[110:113]
	v_mfma_f32_16x16x32_bf16 v[70:73], v[152:155], v[190:193], v[70:73]
	v_mfma_f32_16x16x32_bf16 v[58:61], v[160:163], v[190:193], v[58:61]
	v_mfma_f32_16x16x32_bf16 v[22:25], v[152:155], v[198:201], v[22:25]
	v_mfma_f32_16x16x32_bf16 v[18:21], v[160:163], v[198:201], v[18:21]
	v_mfma_f32_16x16x32_bf16 v[6:9], v[152:155], v[206:209], v[6:9]
	v_mfma_f32_16x16x32_bf16 v[2:5], v[160:163], v[206:209], v[2:5]
	v_mfma_f32_16x16x32_bf16 v[122:125], v[156:159], v[186:189], v[122:125]
	v_mfma_f32_16x16x32_bf16 v[110:113], v[178:181], v[186:189], v[110:113]
	v_mfma_f32_16x16x32_bf16 v[70:73], v[156:159], v[194:197], v[70:73]
	v_mfma_f32_16x16x32_bf16 v[58:61], v[178:181], v[194:197], v[58:61]
	v_mfma_f32_16x16x32_bf16 v[22:25], v[156:159], v[202:205], v[22:25]
	v_mfma_f32_16x16x32_bf16 v[18:21], v[178:181], v[202:205], v[18:21]
	v_mfma_f32_16x16x32_bf16 v[6:9], v[156:159], v[210:213], v[6:9]
	v_mfma_f32_16x16x32_bf16 v[2:5], v[178:181], v[210:213], v[2:5]
	s_setprio 0
	s_barrier
	s_add_i32 s3, s3, 2
	s_add_u32 s56, s56, 0x100
	s_addc_u32 s57, s57, 0
	s_cmp_gt_u32 s3, 5
	s_cbranch_scc0 .LBB0_1046
	s_ashr_i32 s55, s54, 31
	s_lshl_b64 s[24:25], s[54:55], 19
	s_add_u32 s56, s69, s24
	s_addc_u32 s57, s76, s25
	s_ashr_i32 s23, s22, 31
	s_lshl_b64 s[24:25], s[22:23], 19
	s_add_u32 s58, s77, s24
	s_addc_u32 s59, s78, s25
	s_lshl_b32 s3, s60, 18
	s_lshl_b32 s23, s2, 8
	s_lshl_b32 s32, s2, 16
	s_add_i32 s2, s32, s3
	v_lshrrev_b32_e32 v214, 6, v0
	v_lshlrev_b32_e32 v214, 13, v214
	v_and_b32_e32 v215, 63, v0
	v_lshl_add_u32 v214, v215, 3, v214
	v_add_u32_e32 v134, s2, v214
	s_cmp_lg_u32 s37, 0
	s_cbranch_scc1 .Lmpf_have
	global_load_dwordx2 v[162:163], v134, s[14:15]
	global_load_dwordx2 v[178:179], v134, s[16:17]
	v_or_b32_e32 v136, 0x200, v134
	v_add_u32_e32 v137, 0x400, v134
	v_add_u32_e32 v138, 0x600, v134
	v_add_u32_e32 v139, 0x800, v134
	v_add_u32_e32 v140, 0xa00, v134
	v_add_u32_e32 v141, 0xc00, v134
	v_add_u32_e32 v161, 0xe00, v134
	global_load_dwordx2 v[180:181], v136, s[14:15]
	global_load_dwordx2 v[182:183], v136, s[16:17]
	global_load_dwordx2 v[158:159], v137, s[14:15]
	global_load_dwordx2 v[156:157], v137, s[16:17]
	global_load_dwordx2 v[154:155], v138, s[14:15]
	global_load_dwordx2 v[152:153], v138, s[16:17]
	global_load_dwordx2 v[150:151], v139, s[14:15]
	global_load_dwordx2 v[148:149], v139, s[16:17]
	global_load_dwordx2 v[146:147], v140, s[14:15]
	global_load_dwordx2 v[144:145], v140, s[16:17]
	global_load_dwordx2 v[142:143], v141, s[14:15]
	s_nop 0
	global_load_dwordx2 v[140:141], v141, s[16:17]
	s_nop 0
	global_load_dwordx2 v[138:139], v161, s[14:15]
	global_load_dwordx2 v[136:137], v161, s[16:17]
	s_branch .Lmpf_join

.LBB0_1048:
	ds_read_b128 v[136:139], v172
	ds_read_b128 v[140:143], v172 offset:1024
	ds_read_b128 v[144:147], v172 offset:2048
	ds_read_b128 v[148:151], v172 offset:3072
	ds_read_b128 v[152:155], v173
	ds_read_b128 v[156:159], v173 offset:1024
	ds_read_b128 v[160:163], v173 offset:2048
	ds_read_b128 v[178:181], v173 offset:3072
	s_cmp_eq_u32 s33, 12
	s_cselect_b32 s66, s3, s28
	s_cselect_b32 s67, s2, s29
	s_cselect_b32 s64, s25, s30
	s_cselect_b32 s65, s24, s31
	s_add_u32 s62, s66, 0x80
	s_addc_u32 s63, s67, 0
	ds_read_b128 v[182:185], v174
	ds_read_b128 v[186:189], v174 offset:1024
	ds_read_b128 v[190:193], v174 offset:2048
	ds_read_b128 v[194:197], v174 offset:3072
	ds_read_b128 v[198:201], v174 offset:4096
	ds_read_b128 v[202:205], v174 offset:5120
	ds_read_b128 v[206:209], v174 offset:6144
	ds_read_b128 v[210:213], v174 offset:7168
	s_add_u32 s36, s28, 0x3ff80
	s_addc_u32 s37, s29, 0
	s_mov_b32 s52, m0
	s_mov_b32 m0, s26
	s_nop 2
	global_load_lds_dwordx4 v165, s[36:37]
	s_mov_b32 m0, s52
	s_nop 0
	s_mov_b32 s52, m0
	s_mov_b32 m0, s27
	s_nop 2
	global_load_lds_dwordx4 v167, s[36:37]
	s_mov_b32 m0, s52
	s_waitcnt vmcnt(8)
	s_waitcnt lgkmcnt(0)
	s_setprio 1
	s_barrier
	v_mfma_f32_16x16x32_bf16 v[26:29], v[136:139], v[182:185], v[26:29]
	v_mfma_f32_16x16x32_bf16 v[30:33], v[144:147], v[182:185], v[30:33]
	v_mfma_f32_16x16x32_bf16 v[50:53], v[136:139], v[190:193], v[50:53]
	v_mfma_f32_16x16x32_bf16 v[54:57], v[144:147], v[190:193], v[54:57]
	v_mfma_f32_16x16x32_bf16 v[74:77], v[136:139], v[198:201], v[74:77]
	v_mfma_f32_16x16x32_bf16 v[78:81], v[144:147], v[198:201], v[78:81]
	v_mfma_f32_16x16x32_bf16 v[94:97], v[136:139], v[206:209], v[94:97]
	v_mfma_f32_16x16x32_bf16 v[102:105], v[144:147], v[206:209], v[102:105]
	v_mfma_f32_16x16x32_bf16 v[26:29], v[140:143], v[186:189], v[26:29]
	v_mfma_f32_16x16x32_bf16 v[30:33], v[148:151], v[186:189], v[30:33]
	v_mfma_f32_16x16x32_bf16 v[50:53], v[140:143], v[194:197], v[50:53]
	v_mfma_f32_16x16x32_bf16 v[54:57], v[148:151], v[194:197], v[54:57]
	v_mfma_f32_16x16x32_bf16 v[74:77], v[140:143], v[202:205], v[74:77]
	v_mfma_f32_16x16x32_bf16 v[78:81], v[148:151], v[202:205], v[78:81]
	v_mfma_f32_16x16x32_bf16 v[94:97], v[140:143], v[210:213], v[94:97]
	v_mfma_f32_16x16x32_bf16 v[102:105], v[148:151], v[210:213], v[102:105]
	v_mfma_f32_16x16x32_bf16 v[38:41], v[152:155], v[182:185], v[38:41]
	v_mfma_f32_16x16x32_bf16 v[42:45], v[160:163], v[182:185], v[42:45]
	v_mfma_f32_16x16x32_bf16 v[62:65], v[152:155], v[190:193], v[62:65]
	v_mfma_f32_16x16x32_bf16 v[66:69], v[160:163], v[190:193], v[66:69]
	v_mfma_f32_16x16x32_bf16 v[82:85], v[152:155], v[198:201], v[82:85]
	v_mfma_f32_16x16x32_bf16 v[90:93], v[160:163], v[198:201], v[90:93]
	v_mfma_f32_16x16x32_bf16 v[106:109], v[152:155], v[206:209], v[106:109]
	v_mfma_f32_16x16x32_bf16 v[114:117], v[160:163], v[206:209], v[114:117]
	v_mfma_f32_16x16x32_bf16 v[38:41], v[156:159], v[186:189], v[38:41]
	v_mfma_f32_16x16x32_bf16 v[42:45], v[178:181], v[186:189], v[42:45]
	v_mfma_f32_16x16x32_bf16 v[62:65], v[156:159], v[194:197], v[62:65]
	v_mfma_f32_16x16x32_bf16 v[66:69], v[178:181], v[194:197], v[66:69]
	v_mfma_f32_16x16x32_bf16 v[82:85], v[156:159], v[202:205], v[82:85]
	v_mfma_f32_16x16x32_bf16 v[90:93], v[178:181], v[202:205], v[90:93]
	v_mfma_f32_16x16x32_bf16 v[106:109], v[156:159], v[210:213], v[106:109]
	v_mfma_f32_16x16x32_bf16 v[114:117], v[178:181], v[210:213], v[114:117]
	s_setprio 0
	s_barrier
	ds_read_b128 v[182:185], v174 offset:16384
	ds_read_b128 v[186:189], v174 offset:17408
	ds_read_b128 v[190:193], v174 offset:18432
	ds_read_b128 v[194:197], v174 offset:19456
	ds_read_b128 v[198:201], v174 offset:20480
	ds_read_b128 v[202:205], v174 offset:21504
	ds_read_b128 v[206:209], v174 offset:22528
	ds_read_b128 v[210:213], v174 offset:23552
	s_mov_b32 s36, m0
	s_mov_b32 m0, s80
	s_nop 2
	global_load_lds_dwordx4 v166, s[64:65]
	s_mov_b32 m0, s36
	s_nop 0
	s_mov_b32 s36, m0
	s_mov_b32 m0, s81
	s_nop 2
	global_load_lds_dwordx4 v168, s[64:65]
	s_mov_b32 m0, s36
	s_add_u32 s36, s64, 0x40000
	s_addc_u32 s37, s65, 0
	s_mov_b32 s52, m0
	s_mov_b32 m0, s82
	s_nop 2
	global_load_lds_dwordx4 v166, s[36:37]
	s_mov_b32 m0, s52
	s_nop 0
	s_mov_b32 s52, m0
	s_mov_b32 m0, s83
	s_nop 2
	global_load_lds_dwordx4 v168, s[36:37]
	s_mov_b32 m0, s52
	s_mov_b32 s36, m0
	s_mov_b32 m0, s79
	s_nop 2
	global_load_lds_dwordx4 v165, s[66:67]
	s_mov_b32 m0, s36
	s_nop 0
	s_mov_b32 s36, m0
	s_mov_b32 m0, s84
	s_nop 2
	global_load_lds_dwordx4 v167, s[66:67]
	s_mov_b32 m0, s36
	s_waitcnt vmcnt(8)
	s_waitcnt lgkmcnt(0)
	s_setprio 1
	s_barrier
	v_mfma_f32_16x16x32_bf16 v[118:121], v[136:139], v[182:185], v[118:121]
	v_mfma_f32_16x16x32_bf16 v[126:129], v[144:147], v[182:185], v[126:129]
	v_mfma_f32_16x16x32_bf16 v[98:101], v[136:139], v[190:193], v[98:101]
	v_mfma_f32_16x16x32_bf16 v[86:89], v[144:147], v[190:193], v[86:89]
	v_mfma_f32_16x16x32_bf16 v[46:49], v[136:139], v[198:201], v[46:49]
	v_mfma_f32_16x16x32_bf16 v[34:37], v[144:147], v[198:201], v[34:37]
	v_mfma_f32_16x16x32_bf16 v[14:17], v[136:139], v[206:209], v[14:17]
	v_mfma_f32_16x16x32_bf16 v[10:13], v[144:147], v[206:209], v[10:13]
	v_mfma_f32_16x16x32_bf16 v[118:121], v[140:143], v[186:189], v[118:121]
	v_mfma_f32_16x16x32_bf16 v[126:129], v[148:151], v[186:189], v[126:129]
	v_mfma_f32_16x16x32_bf16 v[98:101], v[140:143], v[194:197], v[98:101]
	v_mfma_f32_16x16x32_bf16 v[86:89], v[148:151], v[194:197], v[86:89]
	v_mfma_f32_16x16x32_bf16 v[46:49], v[140:143], v[202:205], v[46:49]
	v_mfma_f32_16x16x32_bf16 v[34:37], v[148:151], v[202:205], v[34:37]
	v_mfma_f32_16x16x32_bf16 v[14:17], v[140:143], v[210:213], v[14:17]
	v_mfma_f32_16x16x32_bf16 v[10:13], v[148:151], v[210:213], v[10:13]
	v_mfma_f32_16x16x32_bf16 v[122:125], v[152:155], v[182:185], v[122:125]
	v_mfma_f32_16x16x32_bf16 v[110:113], v[160:163], v[182:185], v[110:113]
	v_mfma_f32_16x16x32_bf16 v[70:73], v[152:155], v[190:193], v[70:73]
	v_mfma_f32_16x16x32_bf16 v[58:61], v[160:163], v[190:193], v[58:61]
	v_mfma_f32_16x16x32_bf16 v[22:25], v[152:155], v[198:201], v[22:25]
	v_mfma_f32_16x16x32_bf16 v[18:21], v[160:163], v[198:201], v[18:21]
	v_mfma_f32_16x16x32_bf16 v[6:9], v[152:155], v[206:209], v[6:9]
	v_mfma_f32_16x16x32_bf16 v[2:5], v[160:163], v[206:209], v[2:5]
	v_mfma_f32_16x16x32_bf16 v[122:125], v[156:159], v[186:189], v[122:125]
	v_mfma_f32_16x16x32_bf16 v[110:113], v[178:181], v[186:189], v[110:113]
	v_mfma_f32_16x16x32_bf16 v[70:73], v[156:159], v[194:197], v[70:73]
	v_mfma_f32_16x16x32_bf16 v[58:61], v[178:181], v[194:197], v[58:61]
	v_mfma_f32_16x16x32_bf16 v[22:25], v[156:159], v[202:205], v[22:25]
	v_mfma_f32_16x16x32_bf16 v[18:21], v[178:181], v[202:205], v[18:21]
	v_mfma_f32_16x16x32_bf16 v[6:9], v[156:159], v[210:213], v[6:9]
	v_mfma_f32_16x16x32_bf16 v[2:5], v[178:181], v[210:213], v[2:5]
	s_setprio 0
	s_barrier
	ds_read_b128 v[136:139], v175
	ds_read_b128 v[140:143], v175 offset:1024
	ds_read_b128 v[144:147], v175 offset:2048
	ds_read_b128 v[148:151], v175 offset:3072
	ds_read_b128 v[152:155], v176
	ds_read_b128 v[156:159], v176 offset:1024
	ds_read_b128 v[160:163], v176 offset:2048
	ds_read_b128 v[178:181], v176 offset:3072
	ds_read_b128 v[182:185], v174 offset:32768
	ds_read_b128 v[186:189], v174 offset:33792
	ds_read_b128 v[190:193], v174 offset:34816
	ds_read_b128 v[194:197], v174 offset:35840
	ds_read_b128 v[198:201], v174 offset:36864
	ds_read_b128 v[202:205], v174 offset:37888
	ds_read_b128 v[206:209], v174 offset:38912
	ds_read_b128 v[210:213], v174 offset:39936
	s_add_u32 s36, s66, 0x40000
	s_addc_u32 s37, s67, 0
	s_mov_b32 s52, m0
	s_mov_b32 m0, s85
	s_nop 2
	global_load_lds_dwordx4 v165, s[36:37]
	s_mov_b32 m0, s52
	s_nop 0
	s_mov_b32 s52, m0
	s_mov_b32 m0, s86
	s_nop 2
	global_load_lds_dwordx4 v167, s[36:37]
	s_mov_b32 m0, s52
	s_waitcnt vmcnt(8)
	s_waitcnt lgkmcnt(0)
	s_setprio 1
	s_barrier
	v_mfma_f32_16x16x32_bf16 v[26:29], v[136:139], v[182:185], v[26:29]
	v_mfma_f32_16x16x32_bf16 v[30:33], v[144:147], v[182:185], v[30:33]
	v_mfma_f32_16x16x32_bf16 v[50:53], v[136:139], v[190:193], v[50:53]
	v_mfma_f32_16x16x32_bf16 v[54:57], v[144:147], v[190:193], v[54:57]
	v_mfma_f32_16x16x32_bf16 v[74:77], v[136:139], v[198:201], v[74:77]
	v_mfma_f32_16x16x32_bf16 v[78:81], v[144:147], v[198:201], v[78:81]
	v_mfma_f32_16x16x32_bf16 v[94:97], v[136:139], v[206:209], v[94:97]
	v_mfma_f32_16x16x32_bf16 v[102:105], v[144:147], v[206:209], v[102:105]
	v_mfma_f32_16x16x32_bf16 v[26:29], v[140:143], v[186:189], v[26:29]
	v_mfma_f32_16x16x32_bf16 v[30:33], v[148:151], v[186:189], v[30:33]
	v_mfma_f32_16x16x32_bf16 v[50:53], v[140:143], v[194:197], v[50:53]
	v_mfma_f32_16x16x32_bf16 v[54:57], v[148:151], v[194:197], v[54:57]
	v_mfma_f32_16x16x32_bf16 v[74:77], v[140:143], v[202:205], v[74:77]
	v_mfma_f32_16x16x32_bf16 v[78:81], v[148:151], v[202:205], v[78:81]
	v_mfma_f32_16x16x32_bf16 v[94:97], v[140:143], v[210:213], v[94:97]
	v_mfma_f32_16x16x32_bf16 v[102:105], v[148:151], v[210:213], v[102:105]
	v_mfma_f32_16x16x32_bf16 v[38:41], v[152:155], v[182:185], v[38:41]
	v_mfma_f32_16x16x32_bf16 v[42:45], v[160:163], v[182:185], v[42:45]
	v_mfma_f32_16x16x32_bf16 v[62:65], v[152:155], v[190:193], v[62:65]
	v_mfma_f32_16x16x32_bf16 v[66:69], v[160:163], v[190:193], v[66:69]
	v_mfma_f32_16x16x32_bf16 v[82:85], v[152:155], v[198:201], v[82:85]
	v_mfma_f32_16x16x32_bf16 v[90:93], v[160:163], v[198:201], v[90:93]
	v_mfma_f32_16x16x32_bf16 v[106:109], v[152:155], v[206:209], v[106:109]
	v_mfma_f32_16x16x32_bf16 v[114:117], v[160:163], v[206:209], v[114:117]
	v_mfma_f32_16x16x32_bf16 v[38:41], v[156:159], v[186:189], v[38:41]
	v_mfma_f32_16x16x32_bf16 v[42:45], v[178:181], v[186:189], v[42:45]
	v_mfma_f32_16x16x32_bf16 v[62:65], v[156:159], v[194:197], v[62:65]
	v_mfma_f32_16x16x32_bf16 v[66:69], v[178:181], v[194:197], v[66:69]
	v_mfma_f32_16x16x32_bf16 v[82:85], v[156:159], v[202:205], v[82:85]
	v_mfma_f32_16x16x32_bf16 v[90:93], v[178:181], v[202:205], v[90:93]
	v_mfma_f32_16x16x32_bf16 v[106:109], v[156:159], v[210:213], v[106:109]
	v_mfma_f32_16x16x32_bf16 v[114:117], v[178:181], v[210:213], v[114:117]
	s_setprio 0
	s_barrier
	ds_read_b128 v[182:185], v174 offset:49152
	ds_read_b128 v[186:189], v174 offset:50176
	ds_read_b128 v[190:193], v174 offset:51200
	ds_read_b128 v[194:197], v174 offset:52224
	ds_read_b128 v[198:201], v174 offset:53248
	ds_read_b128 v[202:205], v174 offset:54272
	ds_read_b128 v[206:209], v174 offset:55296
	ds_read_b128 v[210:213], v174 offset:56320
	s_add_u32 s36, s64, 0x80
	s_addc_u32 s37, s65, 0
	s_mov_b32 s52, m0
	s_mov_b32 m0, s92
	s_nop 2
	global_load_lds_dwordx4 v166, s[36:37]
	s_mov_b32 m0, s52
	s_nop 0
	s_mov_b32 s52, m0
	s_mov_b32 m0, s93
	s_nop 2
	global_load_lds_dwordx4 v168, s[36:37]
	s_mov_b32 m0, s52
	s_add_u32 s36, s64, 0x40080
	s_addc_u32 s37, s65, 0
	s_mov_b32 s52, m0
	s_mov_b32 m0, s96
	s_nop 2
	global_load_lds_dwordx4 v166, s[36:37]
	s_mov_b32 m0, s52
	s_nop 0
	s_mov_b32 s52, m0
	s_mov_b32 m0, s97
	s_nop 2
	global_load_lds_dwordx4 v168, s[36:37]
	s_mov_b32 m0, s52
	s_mov_b32 s36, m0
	s_mov_b32 m0, s94
	s_nop 2
	global_load_lds_dwordx4 v165, s[62:63]
	s_mov_b32 m0, s36
	s_nop 0
	s_mov_b32 s36, m0
	s_mov_b32 m0, s95
	s_nop 2
	global_load_lds_dwordx4 v167, s[62:63]
	s_mov_b32 m0, s36
	s_waitcnt vmcnt(8)
	s_waitcnt lgkmcnt(0)
	s_setprio 1
	s_barrier
	v_mfma_f32_16x16x32_bf16 v[118:121], v[136:139], v[182:185], v[118:121]
	v_mfma_f32_16x16x32_bf16 v[126:129], v[144:147], v[182:185], v[126:129]
	v_mfma_f32_16x16x32_bf16 v[98:101], v[136:139], v[190:193], v[98:101]
	v_mfma_f32_16x16x32_bf16 v[86:89], v[144:147], v[190:193], v[86:89]
	v_mfma_f32_16x16x32_bf16 v[46:49], v[136:139], v[198:201], v[46:49]
	v_mfma_f32_16x16x32_bf16 v[34:37], v[144:147], v[198:201], v[34:37]
	v_mfma_f32_16x16x32_bf16 v[14:17], v[136:139], v[206:209], v[14:17]
	v_mfma_f32_16x16x32_bf16 v[10:13], v[144:147], v[206:209], v[10:13]
	v_mfma_f32_16x16x32_bf16 v[118:121], v[140:143], v[186:189], v[118:121]
	v_mfma_f32_16x16x32_bf16 v[126:129], v[148:151], v[186:189], v[126:129]
	v_mfma_f32_16x16x32_bf16 v[98:101], v[140:143], v[194:197], v[98:101]
	v_mfma_f32_16x16x32_bf16 v[86:89], v[148:151], v[194:197], v[86:89]
	v_mfma_f32_16x16x32_bf16 v[46:49], v[140:143], v[202:205], v[46:49]
	v_mfma_f32_16x16x32_bf16 v[34:37], v[148:151], v[202:205], v[34:37]
	v_mfma_f32_16x16x32_bf16 v[14:17], v[140:143], v[210:213], v[14:17]
	v_mfma_f32_16x16x32_bf16 v[10:13], v[148:151], v[210:213], v[10:13]
	v_mfma_f32_16x16x32_bf16 v[122:125], v[152:155], v[182:185], v[122:125]
	v_mfma_f32_16x16x32_bf16 v[110:113], v[160:163], v[182:185], v[110:113]
	v_mfma_f32_16x16x32_bf16 v[70:73], v[152:155], v[190:193], v[70:73]
	v_mfma_f32_16x16x32_bf16 v[58:61], v[160:163], v[190:193], v[58:61]
	v_mfma_f32_16x16x32_bf16 v[22:25], v[152:155], v[198:201], v[22:25]
	v_mfma_f32_16x16x32_bf16 v[18:21], v[160:163], v[198:201], v[18:21]
	v_mfma_f32_16x16x32_bf16 v[6:9], v[152:155], v[206:209], v[6:9]
	v_mfma_f32_16x16x32_bf16 v[2:5], v[160:163], v[206:209], v[2:5]
	v_mfma_f32_16x16x32_bf16 v[122:125], v[156:159], v[186:189], v[122:125]
	v_mfma_f32_16x16x32_bf16 v[110:113], v[178:181], v[186:189], v[110:113]
	v_mfma_f32_16x16x32_bf16 v[70:73], v[156:159], v[194:197], v[70:73]
	v_mfma_f32_16x16x32_bf16 v[58:61], v[178:181], v[194:197], v[58:61]
	v_mfma_f32_16x16x32_bf16 v[22:25], v[156:159], v[202:205], v[22:25]
	v_mfma_f32_16x16x32_bf16 v[18:21], v[178:181], v[202:205], v[18:21]
	v_mfma_f32_16x16x32_bf16 v[6:9], v[156:159], v[210:213], v[6:9]
	v_mfma_f32_16x16x32_bf16 v[2:5], v[178:181], v[210:213], v[2:5]
	s_setprio 0
	s_barrier
	s_add_i32 s33, s33, 2
	s_add_u32 s28, s28, 0x100
	s_addc_u32 s29, s29, 0
	s_add_u32 s30, s30, 0x100
	s_addc_u32 s31, s31, 0
	s_cmp_lt_u32 s33, 14
	s_cbranch_scc1 .LBB0_1048
	s_and_b64 vcc, exec, s[20:21]
	s_cbranch_vccz .LBB0_1051
	s_barrier

.Lpeel1440:
	ds_read_b128 v[130:133], v234
	ds_read_b128 v[134:137], v234 offset:1024
	ds_read_b128 v[138:141], v234 offset:2048
	ds_read_b128 v[142:145], v234 offset:3072
	ds_read_b128 v[146:149], v235
	ds_read_b128 v[150:153], v235 offset:1024
	ds_read_b128 v[154:157], v235 offset:2048
	ds_read_b128 v[158:161], v235 offset:3072
	s_add_u32 s60, s58, 0x100
	s_addc_u32 s61, s59, 0
	s_cmp_eq_u32 s87, 12
	s_cselect_b32 s66, s33, s60
	s_cselect_b32 s67, s21, s61
	s_cselect_b32 s64, s84, s85
	s_cselect_b32 s65, s19, s86
	s_add_u32 s62, s66, 0x80
	s_addc_u32 s63, s67, 0
	ds_read_b128 v[162:165], v236
	ds_read_b128 v[166:169], v236 offset:1024
	ds_read_b128 v[170:173], v236 offset:2048
	ds_read_b128 v[174:177], v236 offset:3072
	ds_read_b128 v[178:181], v236 offset:4096
	ds_read_b128 v[182:185], v236 offset:5120
	ds_read_b128 v[186:189], v236 offset:6144
	ds_read_b128 v[190:193], v236 offset:7168
	s_add_u32 s58, s58, 0x40080
	s_addc_u32 s59, s59, 0
	s_mov_b32 s88, m0
	s_mov_b32 m0, s80
	s_nop 2
	global_load_lds_dwordx4 v228, s[58:59]
	s_mov_b32 m0, s88
	s_nop 0
	s_mov_b32 s88, m0
	s_mov_b32 m0, s81
	s_nop 2
	global_load_lds_dwordx4 v230, s[58:59]
	s_mov_b32 m0, s88
	s_waitcnt vmcnt(8)
	s_waitcnt lgkmcnt(0)
	s_setprio 1
	s_barrier
	v_mfma_f32_16x16x32_bf16 v[126:129], v[130:133], v[162:165], 0
	v_mfma_f32_16x16x32_bf16 v[122:125], v[138:141], v[162:165], 0
	v_mfma_f32_16x16x32_bf16 v[114:117], v[130:133], v[170:173], 0
	v_mfma_f32_16x16x32_bf16 v[106:109], v[138:141], v[170:173], 0
	v_mfma_f32_16x16x32_bf16 v[94:97], v[130:133], v[178:181], 0
	v_mfma_f32_16x16x32_bf16 v[90:93], v[138:141], v[178:181], 0
	v_mfma_f32_16x16x32_bf16 v[86:89], v[130:133], v[186:189], 0
	v_mfma_f32_16x16x32_bf16 v[78:81], v[138:141], v[186:189], 0
	v_mfma_f32_16x16x32_bf16 v[126:129], v[134:137], v[166:169], v[126:129]
	v_mfma_f32_16x16x32_bf16 v[122:125], v[142:145], v[166:169], v[122:125]
	v_mfma_f32_16x16x32_bf16 v[114:117], v[134:137], v[174:177], v[114:117]
	v_mfma_f32_16x16x32_bf16 v[106:109], v[142:145], v[174:177], v[106:109]
	v_mfma_f32_16x16x32_bf16 v[94:97], v[134:137], v[182:185], v[94:97]
	v_mfma_f32_16x16x32_bf16 v[90:93], v[142:145], v[182:185], v[90:93]
	v_mfma_f32_16x16x32_bf16 v[86:89], v[134:137], v[190:193], v[86:89]
	v_mfma_f32_16x16x32_bf16 v[78:81], v[142:145], v[190:193], v[78:81]
	v_mfma_f32_16x16x32_bf16 v[118:121], v[146:149], v[162:165], 0
	v_mfma_f32_16x16x32_bf16 v[110:113], v[154:157], v[162:165], 0
	v_mfma_f32_16x16x32_bf16 v[102:105], v[146:149], v[170:173], 0
	v_mfma_f32_16x16x32_bf16 v[98:101], v[154:157], v[170:173], 0
	v_mfma_f32_16x16x32_bf16 v[82:85], v[146:149], v[178:181], 0
	v_mfma_f32_16x16x32_bf16 v[74:77], v[154:157], v[178:181], 0
	v_mfma_f32_16x16x32_bf16 v[70:73], v[146:149], v[186:189], 0
	v_mfma_f32_16x16x32_bf16 v[66:69], v[154:157], v[186:189], 0
	v_mfma_f32_16x16x32_bf16 v[118:121], v[150:153], v[166:169], v[118:121]
	v_mfma_f32_16x16x32_bf16 v[110:113], v[158:161], v[166:169], v[110:113]
	v_mfma_f32_16x16x32_bf16 v[102:105], v[150:153], v[174:177], v[102:105]
	v_mfma_f32_16x16x32_bf16 v[98:101], v[158:161], v[174:177], v[98:101]
	v_mfma_f32_16x16x32_bf16 v[82:85], v[150:153], v[182:185], v[82:85]
	v_mfma_f32_16x16x32_bf16 v[74:77], v[158:161], v[182:185], v[74:77]
	v_mfma_f32_16x16x32_bf16 v[70:73], v[150:153], v[190:193], v[70:73]
	v_mfma_f32_16x16x32_bf16 v[66:69], v[158:161], v[190:193], v[66:69]
	s_setprio 0
	s_barrier
	ds_read_b128 v[162:165], v236 offset:16384
	ds_read_b128 v[166:169], v236 offset:17408
	ds_read_b128 v[170:173], v236 offset:18432
	ds_read_b128 v[174:177], v236 offset:19456
	ds_read_b128 v[178:181], v236 offset:20480
	ds_read_b128 v[182:185], v236 offset:21504
	ds_read_b128 v[186:189], v236 offset:22528
	ds_read_b128 v[190:193], v236 offset:23552
	s_mov_b32 s58, m0
	s_mov_b32 m0, s30
	s_nop 2
	global_load_lds_dwordx4 v229, s[64:65]
	s_mov_b32 m0, s58
	s_nop 0
	s_mov_b32 s58, m0
	s_mov_b32 m0, s31
	s_nop 2
	global_load_lds_dwordx4 v231, s[64:65]
	s_mov_b32 m0, s58
	s_add_u32 s58, s64, 0x40000
	s_addc_u32 s59, s65, 0
	s_mov_b32 s88, m0
	s_mov_b32 m0, s34
	s_nop 2
	global_load_lds_dwordx4 v229, s[58:59]
	s_mov_b32 m0, s88
	s_nop 0
	s_mov_b32 s88, m0
	s_mov_b32 m0, s35
	s_nop 2
	global_load_lds_dwordx4 v231, s[58:59]
	s_mov_b32 m0, s88
	s_mov_b32 s58, m0
	s_mov_b32 m0, s28
	s_nop 2
	global_load_lds_dwordx4 v228, s[66:67]
	s_mov_b32 m0, s58
	s_nop 0
	s_mov_b32 s58, m0
	s_mov_b32 m0, s36
	s_nop 2
	global_load_lds_dwordx4 v230, s[66:67]
	s_mov_b32 m0, s58
	s_waitcnt vmcnt(8)
	s_waitcnt lgkmcnt(0)
	s_setprio 1
	s_barrier
	v_mfma_f32_16x16x32_bf16 v[62:65], v[130:133], v[162:165], 0
	v_mfma_f32_16x16x32_bf16 v[58:61], v[138:141], v[162:165], 0
	v_mfma_f32_16x16x32_bf16 v[54:57], v[130:133], v[170:173], 0
	v_mfma_f32_16x16x32_bf16 v[46:49], v[138:141], v[170:173], 0
	v_mfma_f32_16x16x32_bf16 v[38:41], v[130:133], v[178:181], 0
	v_mfma_f32_16x16x32_bf16 v[30:33], v[138:141], v[178:181], 0
	v_mfma_f32_16x16x32_bf16 v[22:25], v[130:133], v[186:189], 0
	v_mfma_f32_16x16x32_bf16 v[14:17], v[138:141], v[186:189], 0
	v_mfma_f32_16x16x32_bf16 v[62:65], v[134:137], v[166:169], v[62:65]
	v_mfma_f32_16x16x32_bf16 v[58:61], v[142:145], v[166:169], v[58:61]
	v_mfma_f32_16x16x32_bf16 v[54:57], v[134:137], v[174:177], v[54:57]
	v_mfma_f32_16x16x32_bf16 v[46:49], v[142:145], v[174:177], v[46:49]
	v_mfma_f32_16x16x32_bf16 v[38:41], v[134:137], v[182:185], v[38:41]
	v_mfma_f32_16x16x32_bf16 v[30:33], v[142:145], v[182:185], v[30:33]
	v_mfma_f32_16x16x32_bf16 v[22:25], v[134:137], v[190:193], v[22:25]
	v_mfma_f32_16x16x32_bf16 v[14:17], v[142:145], v[190:193], v[14:17]
	v_mfma_f32_16x16x32_bf16 v[50:53], v[146:149], v[162:165], 0
	v_mfma_f32_16x16x32_bf16 v[42:45], v[154:157], v[162:165], 0
	v_mfma_f32_16x16x32_bf16 v[34:37], v[146:149], v[170:173], 0
	v_mfma_f32_16x16x32_bf16 v[26:29], v[154:157], v[170:173], 0
	v_mfma_f32_16x16x32_bf16 v[18:21], v[146:149], v[178:181], 0
	v_mfma_f32_16x16x32_bf16 v[10:13], v[154:157], v[178:181], 0
	v_mfma_f32_16x16x32_bf16 v[6:9], v[146:149], v[186:189], 0
	v_mfma_f32_16x16x32_bf16 v[2:5], v[154:157], v[186:189], 0
	v_mfma_f32_16x16x32_bf16 v[50:53], v[150:153], v[166:169], v[50:53]
	v_mfma_f32_16x16x32_bf16 v[42:45], v[158:161], v[166:169], v[42:45]
	v_mfma_f32_16x16x32_bf16 v[34:37], v[150:153], v[174:177], v[34:37]
	v_mfma_f32_16x16x32_bf16 v[26:29], v[158:161], v[174:177], v[26:29]
	v_mfma_f32_16x16x32_bf16 v[18:21], v[150:153], v[182:185], v[18:21]
	v_mfma_f32_16x16x32_bf16 v[10:13], v[158:161], v[182:185], v[10:13]
	v_mfma_f32_16x16x32_bf16 v[6:9], v[150:153], v[190:193], v[6:9]
	v_mfma_f32_16x16x32_bf16 v[2:5], v[158:161], v[190:193], v[2:5]
	s_setprio 0
	s_barrier
	s_branch .Lmid1440
.LBB0_1440:
	ds_read_b128 v[130:133], v234
	ds_read_b128 v[134:137], v234 offset:1024
	ds_read_b128 v[138:141], v234 offset:2048
	ds_read_b128 v[142:145], v234 offset:3072
	ds_read_b128 v[146:149], v235
	ds_read_b128 v[150:153], v235 offset:1024
	ds_read_b128 v[154:157], v235 offset:2048
	ds_read_b128 v[158:161], v235 offset:3072
	s_add_u32 s60, s58, 0x100
	s_addc_u32 s61, s59, 0
	s_cmp_eq_u32 s87, 12
	s_cselect_b32 s66, s33, s60
	s_cselect_b32 s67, s21, s61
	s_cselect_b32 s64, s84, s85
	s_cselect_b32 s65, s19, s86
	s_add_u32 s62, s66, 0x80
	s_addc_u32 s63, s67, 0
	ds_read_b128 v[162:165], v236
	ds_read_b128 v[166:169], v236 offset:1024
	ds_read_b128 v[170:173], v236 offset:2048
	ds_read_b128 v[174:177], v236 offset:3072
	ds_read_b128 v[178:181], v236 offset:4096
	ds_read_b128 v[182:185], v236 offset:5120
	ds_read_b128 v[186:189], v236 offset:6144
	ds_read_b128 v[190:193], v236 offset:7168
	s_add_u32 s58, s58, 0x40080
	s_addc_u32 s59, s59, 0
	s_mov_b32 s88, m0
	s_mov_b32 m0, s80
	s_nop 2
	global_load_lds_dwordx4 v228, s[58:59]
	s_mov_b32 m0, s88
	s_nop 0
	s_mov_b32 s88, m0
	s_mov_b32 m0, s81
	s_nop 2
	global_load_lds_dwordx4 v230, s[58:59]
	s_mov_b32 m0, s88
	s_waitcnt vmcnt(8)
	s_waitcnt lgkmcnt(0)
	s_setprio 1
	s_barrier
	v_mfma_f32_16x16x32_bf16 v[126:129], v[130:133], v[162:165], v[126:129]
	v_mfma_f32_16x16x32_bf16 v[122:125], v[138:141], v[162:165], v[122:125]
	v_mfma_f32_16x16x32_bf16 v[114:117], v[130:133], v[170:173], v[114:117]
	v_mfma_f32_16x16x32_bf16 v[106:109], v[138:141], v[170:173], v[106:109]
	v_mfma_f32_16x16x32_bf16 v[94:97], v[130:133], v[178:181], v[94:97]
	v_mfma_f32_16x16x32_bf16 v[90:93], v[138:141], v[178:181], v[90:93]
	v_mfma_f32_16x16x32_bf16 v[86:89], v[130:133], v[186:189], v[86:89]
	v_mfma_f32_16x16x32_bf16 v[78:81], v[138:141], v[186:189], v[78:81]
	v_mfma_f32_16x16x32_bf16 v[126:129], v[134:137], v[166:169], v[126:129]
	v_mfma_f32_16x16x32_bf16 v[122:125], v[142:145], v[166:169], v[122:125]
	v_mfma_f32_16x16x32_bf16 v[114:117], v[134:137], v[174:177], v[114:117]
	v_mfma_f32_16x16x32_bf16 v[106:109], v[142:145], v[174:177], v[106:109]
	v_mfma_f32_16x16x32_bf16 v[94:97], v[134:137], v[182:185], v[94:97]
	v_mfma_f32_16x16x32_bf16 v[90:93], v[142:145], v[182:185], v[90:93]
	v_mfma_f32_16x16x32_bf16 v[86:89], v[134:137], v[190:193], v[86:89]
	v_mfma_f32_16x16x32_bf16 v[78:81], v[142:145], v[190:193], v[78:81]
	v_mfma_f32_16x16x32_bf16 v[118:121], v[146:149], v[162:165], v[118:121]
	v_mfma_f32_16x16x32_bf16 v[110:113], v[154:157], v[162:165], v[110:113]
	v_mfma_f32_16x16x32_bf16 v[102:105], v[146:149], v[170:173], v[102:105]
	v_mfma_f32_16x16x32_bf16 v[98:101], v[154:157], v[170:173], v[98:101]
	v_mfma_f32_16x16x32_bf16 v[82:85], v[146:149], v[178:181], v[82:85]
	v_mfma_f32_16x16x32_bf16 v[74:77], v[154:157], v[178:181], v[74:77]
	v_mfma_f32_16x16x32_bf16 v[70:73], v[146:149], v[186:189], v[70:73]
	v_mfma_f32_16x16x32_bf16 v[66:69], v[154:157], v[186:189], v[66:69]
	v_mfma_f32_16x16x32_bf16 v[118:121], v[150:153], v[166:169], v[118:121]
	v_mfma_f32_16x16x32_bf16 v[110:113], v[158:161], v[166:169], v[110:113]
	v_mfma_f32_16x16x32_bf16 v[102:105], v[150:153], v[174:177], v[102:105]
	v_mfma_f32_16x16x32_bf16 v[98:101], v[158:161], v[174:177], v[98:101]
	v_mfma_f32_16x16x32_bf16 v[82:85], v[150:153], v[182:185], v[82:85]
	v_mfma_f32_16x16x32_bf16 v[74:77], v[158:161], v[182:185], v[74:77]
	v_mfma_f32_16x16x32_bf16 v[70:73], v[150:153], v[190:193], v[70:73]
	v_mfma_f32_16x16x32_bf16 v[66:69], v[158:161], v[190:193], v[66:69]
	s_setprio 0
	s_barrier
	ds_read_b128 v[162:165], v236 offset:16384
	ds_read_b128 v[166:169], v236 offset:17408
	ds_read_b128 v[170:173], v236 offset:18432
	ds_read_b128 v[174:177], v236 offset:19456
	ds_read_b128 v[178:181], v236 offset:20480
	ds_read_b128 v[182:185], v236 offset:21504
	ds_read_b128 v[186:189], v236 offset:22528
	ds_read_b128 v[190:193], v236 offset:23552
	s_mov_b32 s58, m0
	s_mov_b32 m0, s30
	s_nop 2
	global_load_lds_dwordx4 v229, s[64:65]
	s_mov_b32 m0, s58
	s_nop 0
	s_mov_b32 s58, m0
	s_mov_b32 m0, s31
	s_nop 2
	global_load_lds_dwordx4 v231, s[64:65]
	s_mov_b32 m0, s58
	s_add_u32 s58, s64, 0x40000
	s_addc_u32 s59, s65, 0
	s_mov_b32 s88, m0
	s_mov_b32 m0, s34
	s_nop 2
	global_load_lds_dwordx4 v229, s[58:59]
	s_mov_b32 m0, s88
	s_nop 0
	s_mov_b32 s88, m0
	s_mov_b32 m0, s35
	s_nop 2
	global_load_lds_dwordx4 v231, s[58:59]
	s_mov_b32 m0, s88
	s_mov_b32 s58, m0
	s_mov_b32 m0, s28
	s_nop 2
	global_load_lds_dwordx4 v228, s[66:67]
	s_mov_b32 m0, s58
	s_nop 0
	s_mov_b32 s58, m0
	s_mov_b32 m0, s36
	s_nop 2
	global_load_lds_dwordx4 v230, s[66:67]
	s_mov_b32 m0, s58
	s_waitcnt vmcnt(8)
	s_waitcnt lgkmcnt(0)
	s_setprio 1
	s_barrier
	v_mfma_f32_16x16x32_bf16 v[62:65], v[130:133], v[162:165], v[62:65]
	v_mfma_f32_16x16x32_bf16 v[58:61], v[138:141], v[162:165], v[58:61]
	v_mfma_f32_16x16x32_bf16 v[54:57], v[130:133], v[170:173], v[54:57]
	v_mfma_f32_16x16x32_bf16 v[46:49], v[138:141], v[170:173], v[46:49]
	v_mfma_f32_16x16x32_bf16 v[38:41], v[130:133], v[178:181], v[38:41]
	v_mfma_f32_16x16x32_bf16 v[30:33], v[138:141], v[178:181], v[30:33]
	v_mfma_f32_16x16x32_bf16 v[22:25], v[130:133], v[186:189], v[22:25]
	v_mfma_f32_16x16x32_bf16 v[14:17], v[138:141], v[186:189], v[14:17]
	v_mfma_f32_16x16x32_bf16 v[62:65], v[134:137], v[166:169], v[62:65]
	v_mfma_f32_16x16x32_bf16 v[58:61], v[142:145], v[166:169], v[58:61]
	v_mfma_f32_16x16x32_bf16 v[54:57], v[134:137], v[174:177], v[54:57]
	v_mfma_f32_16x16x32_bf16 v[46:49], v[142:145], v[174:177], v[46:49]
	v_mfma_f32_16x16x32_bf16 v[38:41], v[134:137], v[182:185], v[38:41]
	v_mfma_f32_16x16x32_bf16 v[30:33], v[142:145], v[182:185], v[30:33]
	v_mfma_f32_16x16x32_bf16 v[22:25], v[134:137], v[190:193], v[22:25]
	v_mfma_f32_16x16x32_bf16 v[14:17], v[142:145], v[190:193], v[14:17]
	v_mfma_f32_16x16x32_bf16 v[50:53], v[146:149], v[162:165], v[50:53]
	v_mfma_f32_16x16x32_bf16 v[42:45], v[154:157], v[162:165], v[42:45]
	v_mfma_f32_16x16x32_bf16 v[34:37], v[146:149], v[170:173], v[34:37]
	v_mfma_f32_16x16x32_bf16 v[26:29], v[154:157], v[170:173], v[26:29]
	v_mfma_f32_16x16x32_bf16 v[18:21], v[146:149], v[178:181], v[18:21]
	v_mfma_f32_16x16x32_bf16 v[10:13], v[154:157], v[178:181], v[10:13]
	v_mfma_f32_16x16x32_bf16 v[6:9], v[146:149], v[186:189], v[6:9]
	v_mfma_f32_16x16x32_bf16 v[2:5], v[154:157], v[186:189], v[2:5]
	v_mfma_f32_16x16x32_bf16 v[50:53], v[150:153], v[166:169], v[50:53]
	v_mfma_f32_16x16x32_bf16 v[42:45], v[158:161], v[166:169], v[42:45]
	v_mfma_f32_16x16x32_bf16 v[34:37], v[150:153], v[174:177], v[34:37]
	v_mfma_f32_16x16x32_bf16 v[26:29], v[158:161], v[174:177], v[26:29]
	v_mfma_f32_16x16x32_bf16 v[18:21], v[150:153], v[182:185], v[18:21]
	v_mfma_f32_16x16x32_bf16 v[10:13], v[158:161], v[182:185], v[10:13]
	v_mfma_f32_16x16x32_bf16 v[6:9], v[150:153], v[190:193], v[6:9]
	v_mfma_f32_16x16x32_bf16 v[2:5], v[158:161], v[190:193], v[2:5]
	s_setprio 0
	s_barrier
.Lmid1440:
	ds_read_b128 v[130:133], v237
	ds_read_b128 v[134:137], v237 offset:1024
	ds_read_b128 v[138:141], v237 offset:2048
	ds_read_b128 v[142:145], v237 offset:3072
	ds_read_b128 v[146:149], v238
	ds_read_b128 v[150:153], v238 offset:1024
	ds_read_b128 v[154:157], v238 offset:2048
	ds_read_b128 v[158:161], v238 offset:3072
	ds_read_b128 v[162:165], v236 offset:32768
	ds_read_b128 v[166:169], v236 offset:33792
	ds_read_b128 v[170:173], v236 offset:34816
	ds_read_b128 v[174:177], v236 offset:35840
	ds_read_b128 v[178:181], v236 offset:36864
	ds_read_b128 v[182:185], v236 offset:37888
	ds_read_b128 v[186:189], v236 offset:38912
	ds_read_b128 v[190:193], v236 offset:39936
	s_add_u32 s58, s66, 0x40000
	s_addc_u32 s59, s67, 0
	s_mov_b32 s66, m0
	s_mov_b32 m0, s37
	s_nop 2
	global_load_lds_dwordx4 v228, s[58:59]
	s_mov_b32 m0, s66
	s_nop 0
	s_mov_b32 s66, m0
	s_mov_b32 m0, s52
	s_nop 2
	global_load_lds_dwordx4 v230, s[58:59]
	s_mov_b32 m0, s66
	s_waitcnt vmcnt(8)
	s_waitcnt lgkmcnt(0)
	s_setprio 1
	s_barrier
	v_mfma_f32_16x16x32_bf16 v[126:129], v[130:133], v[162:165], v[126:129]
	v_mfma_f32_16x16x32_bf16 v[122:125], v[138:141], v[162:165], v[122:125]
	v_mfma_f32_16x16x32_bf16 v[114:117], v[130:133], v[170:173], v[114:117]
	v_mfma_f32_16x16x32_bf16 v[106:109], v[138:141], v[170:173], v[106:109]
	v_mfma_f32_16x16x32_bf16 v[94:97], v[130:133], v[178:181], v[94:97]
	v_mfma_f32_16x16x32_bf16 v[90:93], v[138:141], v[178:181], v[90:93]
	v_mfma_f32_16x16x32_bf16 v[86:89], v[130:133], v[186:189], v[86:89]
	v_mfma_f32_16x16x32_bf16 v[78:81], v[138:141], v[186:189], v[78:81]
	v_mfma_f32_16x16x32_bf16 v[126:129], v[134:137], v[166:169], v[126:129]
	v_mfma_f32_16x16x32_bf16 v[122:125], v[142:145], v[166:169], v[122:125]
	v_mfma_f32_16x16x32_bf16 v[114:117], v[134:137], v[174:177], v[114:117]
	v_mfma_f32_16x16x32_bf16 v[106:109], v[142:145], v[174:177], v[106:109]
	v_mfma_f32_16x16x32_bf16 v[94:97], v[134:137], v[182:185], v[94:97]
	v_mfma_f32_16x16x32_bf16 v[90:93], v[142:145], v[182:185], v[90:93]
	v_mfma_f32_16x16x32_bf16 v[86:89], v[134:137], v[190:193], v[86:89]
	v_mfma_f32_16x16x32_bf16 v[78:81], v[142:145], v[190:193], v[78:81]
	v_mfma_f32_16x16x32_bf16 v[118:121], v[146:149], v[162:165], v[118:121]
	v_mfma_f32_16x16x32_bf16 v[110:113], v[154:157], v[162:165], v[110:113]
	v_mfma_f32_16x16x32_bf16 v[102:105], v[146:149], v[170:173], v[102:105]
	v_mfma_f32_16x16x32_bf16 v[98:101], v[154:157], v[170:173], v[98:101]
	v_mfma_f32_16x16x32_bf16 v[82:85], v[146:149], v[178:181], v[82:85]
	v_mfma_f32_16x16x32_bf16 v[74:77], v[154:157], v[178:181], v[74:77]
	v_mfma_f32_16x16x32_bf16 v[70:73], v[146:149], v[186:189], v[70:73]
	v_mfma_f32_16x16x32_bf16 v[66:69], v[154:157], v[186:189], v[66:69]
	v_mfma_f32_16x16x32_bf16 v[118:121], v[150:153], v[166:169], v[118:121]
	v_mfma_f32_16x16x32_bf16 v[110:113], v[158:161], v[166:169], v[110:113]
	v_mfma_f32_16x16x32_bf16 v[102:105], v[150:153], v[174:177], v[102:105]
	v_mfma_f32_16x16x32_bf16 v[98:101], v[158:161], v[174:177], v[98:101]
	v_mfma_f32_16x16x32_bf16 v[82:85], v[150:153], v[182:185], v[82:85]
	v_mfma_f32_16x16x32_bf16 v[74:77], v[158:161], v[182:185], v[74:77]
	v_mfma_f32_16x16x32_bf16 v[70:73], v[150:153], v[190:193], v[70:73]
	v_mfma_f32_16x16x32_bf16 v[66:69], v[158:161], v[190:193], v[66:69]
	s_setprio 0
	s_barrier
	ds_read_b128 v[162:165], v236 offset:49152
	ds_read_b128 v[166:169], v236 offset:50176
	ds_read_b128 v[170:173], v236 offset:51200
	ds_read_b128 v[174:177], v236 offset:52224
	ds_read_b128 v[178:181], v236 offset:53248
	ds_read_b128 v[182:185], v236 offset:54272
	ds_read_b128 v[186:189], v236 offset:55296
	ds_read_b128 v[190:193], v236 offset:56320
	s_add_u32 s58, s64, 0x80
	s_addc_u32 s59, s65, 0
	s_mov_b32 s66, m0
	s_mov_b32 m0, s68
	s_nop 2
	global_load_lds_dwordx4 v229, s[58:59]
	s_mov_b32 m0, s66
	s_nop 0
	s_mov_b32 s66, m0
	s_mov_b32 m0, s69
	s_nop 2
	global_load_lds_dwordx4 v231, s[58:59]
	s_mov_b32 m0, s66
	s_add_u32 s58, s64, 0x40080
	s_addc_u32 s59, s65, 0
	s_mov_b32 s64, m0
	s_mov_b32 m0, s78
	s_nop 2
	global_load_lds_dwordx4 v229, s[58:59]
	s_mov_b32 m0, s64
	s_nop 0
	s_mov_b32 s64, m0
	s_mov_b32 m0, s79
	s_nop 2
	global_load_lds_dwordx4 v231, s[58:59]
	s_mov_b32 m0, s64
	s_mov_b32 s58, m0
	s_mov_b32 m0, s76
	s_nop 2
	global_load_lds_dwordx4 v228, s[62:63]
	s_mov_b32 m0, s58
	s_nop 0
	s_mov_b32 s58, m0
	s_mov_b32 m0, s77
	s_nop 2
	global_load_lds_dwordx4 v230, s[62:63]
	s_mov_b32 m0, s58
	s_waitcnt vmcnt(8)
	s_waitcnt lgkmcnt(0)
	s_setprio 1
	s_barrier
	v_mfma_f32_16x16x32_bf16 v[62:65], v[130:133], v[162:165], v[62:65]
	v_mfma_f32_16x16x32_bf16 v[58:61], v[138:141], v[162:165], v[58:61]
	v_mfma_f32_16x16x32_bf16 v[54:57], v[130:133], v[170:173], v[54:57]
	v_mfma_f32_16x16x32_bf16 v[46:49], v[138:141], v[170:173], v[46:49]
	v_mfma_f32_16x16x32_bf16 v[38:41], v[130:133], v[178:181], v[38:41]
	v_mfma_f32_16x16x32_bf16 v[30:33], v[138:141], v[178:181], v[30:33]
	v_mfma_f32_16x16x32_bf16 v[22:25], v[130:133], v[186:189], v[22:25]
	v_mfma_f32_16x16x32_bf16 v[14:17], v[138:141], v[186:189], v[14:17]
	v_mfma_f32_16x16x32_bf16 v[62:65], v[134:137], v[166:169], v[62:65]
	v_mfma_f32_16x16x32_bf16 v[58:61], v[142:145], v[166:169], v[58:61]
	v_mfma_f32_16x16x32_bf16 v[54:57], v[134:137], v[174:177], v[54:57]
	v_mfma_f32_16x16x32_bf16 v[46:49], v[142:145], v[174:177], v[46:49]
	v_mfma_f32_16x16x32_bf16 v[38:41], v[134:137], v[182:185], v[38:41]
	v_mfma_f32_16x16x32_bf16 v[30:33], v[142:145], v[182:185], v[30:33]
	v_mfma_f32_16x16x32_bf16 v[22:25], v[134:137], v[190:193], v[22:25]
	v_mfma_f32_16x16x32_bf16 v[14:17], v[142:145], v[190:193], v[14:17]
	v_mfma_f32_16x16x32_bf16 v[50:53], v[146:149], v[162:165], v[50:53]
	v_mfma_f32_16x16x32_bf16 v[42:45], v[154:157], v[162:165], v[42:45]
	v_mfma_f32_16x16x32_bf16 v[34:37], v[146:149], v[170:173], v[34:37]
	v_mfma_f32_16x16x32_bf16 v[26:29], v[154:157], v[170:173], v[26:29]
	v_mfma_f32_16x16x32_bf16 v[18:21], v[146:149], v[178:181], v[18:21]
	v_mfma_f32_16x16x32_bf16 v[10:13], v[154:157], v[178:181], v[10:13]
	v_mfma_f32_16x16x32_bf16 v[6:9], v[146:149], v[186:189], v[6:9]
	v_mfma_f32_16x16x32_bf16 v[2:5], v[154:157], v[186:189], v[2:5]
	v_mfma_f32_16x16x32_bf16 v[50:53], v[150:153], v[166:169], v[50:53]
	v_mfma_f32_16x16x32_bf16 v[42:45], v[158:161], v[166:169], v[42:45]
	v_mfma_f32_16x16x32_bf16 v[34:37], v[150:153], v[174:177], v[34:37]
	v_mfma_f32_16x16x32_bf16 v[26:29], v[158:161], v[174:177], v[26:29]
	v_mfma_f32_16x16x32_bf16 v[18:21], v[150:153], v[182:185], v[18:21]
	v_mfma_f32_16x16x32_bf16 v[10:13], v[158:161], v[182:185], v[10:13]
	v_mfma_f32_16x16x32_bf16 v[6:9], v[150:153], v[190:193], v[6:9]
	v_mfma_f32_16x16x32_bf16 v[2:5], v[158:161], v[190:193], v[2:5]
	s_setprio 0
	s_barrier
	s_add_i32 s87, s87, 2
	s_add_u32 s85, s85, 0x100
	s_addc_u32 s86, s86, 0
	s_cmp_gt_u32 s87, 13
	s_mov_b64 s[58:59], s[60:61]
	s_cbranch_scc0 .LBB0_1440
	s_and_b64 vcc, exec, s[16:17]
	s_cbranch_vccz .LBB0_1443
	s_barrier

.LBB0_1896:
	s_cmp_eq_u32 s40, 0
	s_cbranch_scc1 .Lpeel6
	s_add_u32 s33, s74, s40
	s_addc_u32 s44, s75, s41
	s_add_u32 s56, s33, 0x1d800080
	s_addc_u32 s57, s44, 0
	s_add_u32 s33, s33, 0x1d800100
	s_addc_u32 s52, s44, 0
	v_add_u32_e32 v2, 0x10000, v173
	v_add_u32_e32 v14, 0x14000, v173
	s_and_b64 s[44:45], s[42:43], exec
	ds_read_b128 v[18:21], v2
	ds_read_b128 v[22:25], v2 offset:1024
	ds_read_b128 v[26:29], v2 offset:2048
	ds_read_b128 v[30:33], v2 offset:3072
	ds_read_b128 v[2:5], v14
	ds_read_b128 v[6:9], v14 offset:1024
	ds_read_b128 v[10:13], v14 offset:2048
	ds_read_b128 v[14:17], v14 offset:3072
	s_cselect_b32 s55, s11, s52
	s_cselect_b32 s54, s10, s33
	s_add_u32 s33, s2, s40
	s_addc_u32 s44, s23, s41
	s_and_b64 s[42:43], s[42:43], exec
	s_cselect_b32 s43, s39, s44
	s_cselect_b32 s42, s38, s33
	s_add_u32 s44, s54, 0x80
	s_addc_u32 s45, s55, 0
	s_add_u32 s52, s42, 0x80
	s_addc_u32 s53, s43, 0
	ds_read_b128 v[180:183], v174
	ds_read_b128 v[184:187], v174 offset:1024
	ds_read_b128 v[188:191], v174 offset:2048
	ds_read_b128 v[192:195], v174 offset:3072
	ds_read_b128 v[196:199], v174 offset:4096
	ds_read_b128 v[200:203], v174 offset:5120
	ds_read_b128 v[204:207], v174 offset:6144
	ds_read_b128 v[208:211], v174 offset:7168
	s_mov_b32 s33, m0
	s_mov_b32 m0, s93
	s_nop 2
	global_load_lds_dwordx4 v178, s[56:57]
	s_mov_b32 m0, s33
	s_nop 0
	s_mov_b32 s33, m0
	s_mov_b32 m0, s94
	s_nop 2
	global_load_lds_dwordx4 v177, s[56:57]
	s_mov_b32 m0, s33
	s_waitcnt vmcnt(8)
	s_waitcnt lgkmcnt(0)
	s_setprio 1
	s_barrier
	v_mfma_f32_16x16x128_f8f6f4 v[158:161], v[18:25], v[180:187], v[158:161]
	v_mfma_f32_16x16x128_f8f6f4 v[154:157], v[26:33], v[180:187], v[154:157]
	v_mfma_f32_16x16x128_f8f6f4 v[150:153], v[18:25], v[188:195], v[150:153]
	v_mfma_f32_16x16x128_f8f6f4 v[146:149], v[26:33], v[188:195], v[146:149]
	v_mfma_f32_16x16x128_f8f6f4 v[142:145], v[18:25], v[196:203], v[142:145]
	v_mfma_f32_16x16x128_f8f6f4 v[138:141], v[26:33], v[196:203], v[138:141]
	v_mfma_f32_16x16x128_f8f6f4 v[134:137], v[18:25], v[204:211], v[134:137]
	v_mfma_f32_16x16x128_f8f6f4 v[130:133], v[26:33], v[204:211], v[130:133]
	v_mfma_f32_16x16x128_f8f6f4 v[126:129], v[2:9], v[180:187], v[126:129]
	v_mfma_f32_16x16x128_f8f6f4 v[122:125], v[10:17], v[180:187], v[122:125]
	v_mfma_f32_16x16x128_f8f6f4 v[118:121], v[2:9], v[188:195], v[118:121]
	v_mfma_f32_16x16x128_f8f6f4 v[114:117], v[10:17], v[188:195], v[114:117]
	v_mfma_f32_16x16x128_f8f6f4 v[110:113], v[2:9], v[196:203], v[110:113]
	v_mfma_f32_16x16x128_f8f6f4 v[106:109], v[10:17], v[196:203], v[106:109]
	v_mfma_f32_16x16x128_f8f6f4 v[102:105], v[2:9], v[204:211], v[102:105]
	v_mfma_f32_16x16x128_f8f6f4 v[98:101], v[10:17], v[204:211], v[98:101]
	s_setprio 0
	s_barrier
	ds_read_b128 v[180:183], v174 offset:16384
	ds_read_b128 v[184:187], v174 offset:17408
	ds_read_b128 v[188:191], v174 offset:18432
	ds_read_b128 v[192:195], v174 offset:19456
	ds_read_b128 v[196:199], v174 offset:20480
	ds_read_b128 v[200:203], v174 offset:21504
	ds_read_b128 v[204:207], v174 offset:22528
	ds_read_b128 v[208:211], v174 offset:23552
	s_mov_b32 s33, m0
	s_mov_b32 m0, s67
	s_nop 2
	global_load_lds_dwordx4 v1, s[42:43]
	s_mov_b32 m0, s33
	s_add_u32 s56, s42, 0x20000
	s_mov_b32 s33, m0
	s_mov_b32 m0, s68
	s_nop 2
	global_load_lds_dwordx4 v163, s[42:43]
	s_mov_b32 m0, s33
	s_addc_u32 s57, s43, 0
	s_mov_b32 s33, m0
	s_mov_b32 m0, s69
	s_nop 2
	global_load_lds_dwordx4 v1, s[56:57]
	s_mov_b32 m0, s33
	s_nop 0
	s_mov_b32 s33, m0
	s_mov_b32 m0, s76
	s_nop 2
	global_load_lds_dwordx4 v163, s[56:57]
	s_mov_b32 m0, s33
	s_nop 0
	s_mov_b32 s33, m0
	s_mov_b32 m0, s15
	s_nop 2
	global_load_lds_dwordx4 v168, s[54:55]
	s_mov_b32 m0, s33
	s_nop 0
	s_mov_b32 s33, m0
	s_mov_b32 m0, s79
	s_nop 2
	global_load_lds_dwordx4 v172, s[54:55]
	s_mov_b32 m0, s33
	s_waitcnt vmcnt(8)
	s_waitcnt lgkmcnt(0)
	s_setprio 1
	s_barrier
	v_mfma_f32_16x16x128_f8f6f4 v[94:97], v[18:25], v[180:187], v[94:97]
	v_mfma_f32_16x16x128_f8f6f4 v[90:93], v[26:33], v[180:187], v[90:93]
	v_mfma_f32_16x16x128_f8f6f4 v[86:89], v[18:25], v[188:195], v[86:89]
	v_mfma_f32_16x16x128_f8f6f4 v[82:85], v[26:33], v[188:195], v[82:85]
	v_mfma_f32_16x16x128_f8f6f4 v[78:81], v[18:25], v[196:203], v[78:81]
	v_mfma_f32_16x16x128_f8f6f4 v[74:77], v[26:33], v[196:203], v[74:77]
	v_mfma_f32_16x16x128_f8f6f4 v[70:73], v[18:25], v[204:211], v[70:73]
	v_mfma_f32_16x16x128_f8f6f4 v[66:69], v[26:33], v[204:211], v[66:69]
	v_mfma_f32_16x16x128_f8f6f4 v[62:65], v[2:9], v[180:187], v[62:65]
	v_mfma_f32_16x16x128_f8f6f4 v[58:61], v[10:17], v[180:187], v[58:61]
	v_mfma_f32_16x16x128_f8f6f4 v[54:57], v[2:9], v[188:195], v[54:57]
	v_mfma_f32_16x16x128_f8f6f4 v[50:53], v[10:17], v[188:195], v[50:53]
	v_mfma_f32_16x16x128_f8f6f4 v[46:49], v[2:9], v[196:203], v[46:49]
	v_mfma_f32_16x16x128_f8f6f4 v[42:45], v[10:17], v[196:203], v[42:45]
	v_mfma_f32_16x16x128_f8f6f4 v[38:41], v[2:9], v[204:211], v[38:41]
	v_mfma_f32_16x16x128_f8f6f4 v[34:37], v[10:17], v[204:211], v[34:37]
	s_setprio 0
	s_barrier
.Lmid6:
	v_add_u32_e32 v14, 0x18000, v173
	v_add_u32_e32 v30, 0x1c000, v173
	ds_read_b128 v[2:5], v14
	ds_read_b128 v[6:9], v14 offset:1024
	ds_read_b128 v[10:13], v14 offset:2048
	ds_read_b128 v[14:17], v14 offset:3072
	ds_read_b128 v[18:21], v30
	ds_read_b128 v[22:25], v30 offset:1024
	ds_read_b128 v[26:29], v30 offset:2048
	ds_read_b128 v[30:33], v30 offset:3072
	ds_read_b128 v[180:183], v174 offset:32768
	ds_read_b128 v[184:187], v174 offset:33792
	ds_read_b128 v[188:191], v174 offset:34816
	ds_read_b128 v[192:195], v174 offset:35840
	ds_read_b128 v[196:199], v174 offset:36864
	ds_read_b128 v[200:203], v174 offset:37888
	ds_read_b128 v[204:207], v174 offset:38912
	ds_read_b128 v[208:211], v174 offset:39936
	s_mov_b32 s33, m0
	s_mov_b32 m0, s80
	s_nop 2
	global_load_lds_dwordx4 v169, s[54:55]
	s_mov_b32 m0, s33
	s_nop 0
	s_mov_b32 s33, m0
	s_mov_b32 m0, s81
	s_nop 2
	global_load_lds_dwordx4 v175, s[54:55]
	s_mov_b32 m0, s33
	s_waitcnt vmcnt(8)
	s_waitcnt lgkmcnt(0)
	s_setprio 1
	s_barrier
	v_mfma_f32_16x16x128_f8f6f4 v[158:161], v[2:9], v[180:187], v[158:161]
	v_mfma_f32_16x16x128_f8f6f4 v[154:157], v[10:17], v[180:187], v[154:157]
	v_mfma_f32_16x16x128_f8f6f4 v[150:153], v[2:9], v[188:195], v[150:153]
	v_mfma_f32_16x16x128_f8f6f4 v[146:149], v[10:17], v[188:195], v[146:149]
	v_mfma_f32_16x16x128_f8f6f4 v[142:145], v[2:9], v[196:203], v[142:145]
	v_mfma_f32_16x16x128_f8f6f4 v[138:141], v[10:17], v[196:203], v[138:141]
	v_mfma_f32_16x16x128_f8f6f4 v[134:137], v[2:9], v[204:211], v[134:137]
	v_mfma_f32_16x16x128_f8f6f4 v[130:133], v[10:17], v[204:211], v[130:133]
	v_mfma_f32_16x16x128_f8f6f4 v[126:129], v[18:25], v[180:187], v[126:129]
	v_mfma_f32_16x16x128_f8f6f4 v[122:125], v[26:33], v[180:187], v[122:125]
	v_mfma_f32_16x16x128_f8f6f4 v[118:121], v[18:25], v[188:195], v[118:121]
	v_mfma_f32_16x16x128_f8f6f4 v[114:117], v[26:33], v[188:195], v[114:117]
	v_mfma_f32_16x16x128_f8f6f4 v[110:113], v[18:25], v[196:203], v[110:113]
	v_mfma_f32_16x16x128_f8f6f4 v[106:109], v[26:33], v[196:203], v[106:109]
	v_mfma_f32_16x16x128_f8f6f4 v[102:105], v[18:25], v[204:211], v[102:105]
	v_mfma_f32_16x16x128_f8f6f4 v[98:101], v[26:33], v[204:211], v[98:101]
	s_setprio 0
	s_barrier
	ds_read_b128 v[180:183], v174 offset:49152
	ds_read_b128 v[184:187], v174 offset:50176
	ds_read_b128 v[188:191], v174 offset:51200
	ds_read_b128 v[192:195], v174 offset:52224
	ds_read_b128 v[196:199], v174 offset:53248
	ds_read_b128 v[200:203], v174 offset:54272
	ds_read_b128 v[204:207], v174 offset:55296
	ds_read_b128 v[208:211], v174 offset:56320
	s_mov_b32 s33, m0
	s_mov_b32 m0, s84
	s_nop 2
	global_load_lds_dwordx4 v1, s[52:53]
	s_mov_b32 m0, s33
	s_add_u32 s42, s42, 0x20080
	s_mov_b32 s33, m0
	s_mov_b32 m0, s85
	s_nop 2
	global_load_lds_dwordx4 v163, s[52:53]
	s_mov_b32 m0, s33
	s_addc_u32 s43, s43, 0
	s_mov_b32 s33, m0
	s_mov_b32 m0, s91
	s_nop 2
	global_load_lds_dwordx4 v1, s[42:43]
	s_mov_b32 m0, s33
	s_nop 0
	s_mov_b32 s33, m0
	s_mov_b32 m0, s92
	s_nop 2
	global_load_lds_dwordx4 v163, s[42:43]
	s_mov_b32 m0, s33
	s_nop 0
	s_mov_b32 s33, m0
	s_mov_b32 m0, s86
	s_nop 2
	global_load_lds_dwordx4 v168, s[44:45]
	s_mov_b32 m0, s33
	s_nop 0
	s_mov_b32 s33, m0
	s_mov_b32 m0, s87
	s_nop 2
	global_load_lds_dwordx4 v172, s[44:45]
	s_mov_b32 m0, s33
	s_waitcnt vmcnt(8)
	s_waitcnt lgkmcnt(0)
	s_setprio 1
	s_barrier
	v_mfma_f32_16x16x128_f8f6f4 v[94:97], v[2:9], v[180:187], v[94:97]
	v_mfma_f32_16x16x128_f8f6f4 v[90:93], v[10:17], v[180:187], v[90:93]
	v_mfma_f32_16x16x128_f8f6f4 v[86:89], v[2:9], v[188:195], v[86:89]
	v_mfma_f32_16x16x128_f8f6f4 v[82:85], v[10:17], v[188:195], v[82:85]
	v_mfma_f32_16x16x128_f8f6f4 v[78:81], v[2:9], v[196:203], v[78:81]
	v_mfma_f32_16x16x128_f8f6f4 v[74:77], v[10:17], v[196:203], v[74:77]
	v_mfma_f32_16x16x128_f8f6f4 v[70:73], v[2:9], v[204:211], v[70:73]
	v_mfma_f32_16x16x128_f8f6f4 v[66:69], v[10:17], v[204:211], v[66:69]
	v_mfma_f32_16x16x128_f8f6f4 v[62:65], v[18:25], v[180:187], v[62:65]
	v_mfma_f32_16x16x128_f8f6f4 v[58:61], v[26:33], v[180:187], v[58:61]
	v_mfma_f32_16x16x128_f8f6f4 v[54:57], v[18:25], v[188:195], v[54:57]
	v_mfma_f32_16x16x128_f8f6f4 v[50:53], v[26:33], v[188:195], v[50:53]
	v_mfma_f32_16x16x128_f8f6f4 v[46:49], v[18:25], v[196:203], v[46:49]
	v_mfma_f32_16x16x128_f8f6f4 v[42:45], v[26:33], v[196:203], v[42:45]
	v_mfma_f32_16x16x128_f8f6f4 v[38:41], v[18:25], v[204:211], v[38:41]
	v_mfma_f32_16x16x128_f8f6f4 v[34:37], v[26:33], v[204:211], v[34:37]
	s_setprio 0
	s_cmp_lt_i32 s9, 4
	s_cbranch_scc1 .Lkb6_do
	s_cmp_lg_u64 s[16:17], 0
	s_cbranch_scc0 .Lkb6_skip

.Lpeel6:
	s_add_u32 s33, s74, s40
	s_addc_u32 s44, s75, s41
	s_add_u32 s56, s33, 0x1d800080
	s_addc_u32 s57, s44, 0
	s_add_u32 s33, s33, 0x1d800100
	s_addc_u32 s52, s44, 0
	v_add_u32_e32 v2, 0x10000, v173
	v_add_u32_e32 v14, 0x14000, v173
	s_and_b64 s[44:45], s[42:43], exec
	ds_read_b128 v[18:21], v2
	ds_read_b128 v[22:25], v2 offset:1024
	ds_read_b128 v[26:29], v2 offset:2048
	ds_read_b128 v[30:33], v2 offset:3072
	ds_read_b128 v[2:5], v14
	ds_read_b128 v[6:9], v14 offset:1024
	ds_read_b128 v[10:13], v14 offset:2048
	ds_read_b128 v[14:17], v14 offset:3072
	s_cselect_b32 s55, s11, s52
	s_cselect_b32 s54, s10, s33
	s_add_u32 s33, s2, s40
	s_addc_u32 s44, s23, s41
	s_and_b64 s[42:43], s[42:43], exec
	s_cselect_b32 s43, s39, s44
	s_cselect_b32 s42, s38, s33
	s_add_u32 s44, s54, 0x80
	s_addc_u32 s45, s55, 0
	s_add_u32 s52, s42, 0x80
	s_addc_u32 s53, s43, 0
	ds_read_b128 v[180:183], v174
	ds_read_b128 v[184:187], v174 offset:1024
	ds_read_b128 v[188:191], v174 offset:2048
	ds_read_b128 v[192:195], v174 offset:3072
	ds_read_b128 v[196:199], v174 offset:4096
	ds_read_b128 v[200:203], v174 offset:5120
	ds_read_b128 v[204:207], v174 offset:6144
	ds_read_b128 v[208:211], v174 offset:7168
	s_mov_b32 s33, m0
	s_mov_b32 m0, s93
	s_nop 2
	global_load_lds_dwordx4 v178, s[56:57]
	s_mov_b32 m0, s33
	s_nop 0
	s_mov_b32 s33, m0
	s_mov_b32 m0, s94
	s_nop 2
	global_load_lds_dwordx4 v177, s[56:57]
	s_mov_b32 m0, s33
	s_waitcnt vmcnt(8)
	s_waitcnt lgkmcnt(0)
	s_setprio 1
	s_barrier
	v_mfma_f32_16x16x128_f8f6f4 v[158:161], v[18:25], v[180:187], 0
	v_mfma_f32_16x16x128_f8f6f4 v[154:157], v[26:33], v[180:187], 0
	v_mfma_f32_16x16x128_f8f6f4 v[150:153], v[18:25], v[188:195], 0
	v_mfma_f32_16x16x128_f8f6f4 v[146:149], v[26:33], v[188:195], 0
	v_mfma_f32_16x16x128_f8f6f4 v[142:145], v[18:25], v[196:203], 0
	v_mfma_f32_16x16x128_f8f6f4 v[138:141], v[26:33], v[196:203], 0
	v_mfma_f32_16x16x128_f8f6f4 v[134:137], v[18:25], v[204:211], 0
	v_mfma_f32_16x16x128_f8f6f4 v[130:133], v[26:33], v[204:211], 0
	v_mfma_f32_16x16x128_f8f6f4 v[126:129], v[2:9], v[180:187], 0
	v_mfma_f32_16x16x128_f8f6f4 v[122:125], v[10:17], v[180:187], 0
	v_mfma_f32_16x16x128_f8f6f4 v[118:121], v[2:9], v[188:195], 0
	v_mfma_f32_16x16x128_f8f6f4 v[114:117], v[10:17], v[188:195], 0
	v_mfma_f32_16x16x128_f8f6f4 v[110:113], v[2:9], v[196:203], 0
	v_mfma_f32_16x16x128_f8f6f4 v[106:109], v[10:17], v[196:203], 0
	v_mfma_f32_16x16x128_f8f6f4 v[102:105], v[2:9], v[204:211], 0
	v_mfma_f32_16x16x128_f8f6f4 v[98:101], v[10:17], v[204:211], 0
	s_setprio 0
	s_barrier
	ds_read_b128 v[180:183], v174 offset:16384
	ds_read_b128 v[184:187], v174 offset:17408
	ds_read_b128 v[188:191], v174 offset:18432
	ds_read_b128 v[192:195], v174 offset:19456
	ds_read_b128 v[196:199], v174 offset:20480
	ds_read_b128 v[200:203], v174 offset:21504
	ds_read_b128 v[204:207], v174 offset:22528
	ds_read_b128 v[208:211], v174 offset:23552
	s_mov_b32 s33, m0
	s_mov_b32 m0, s67
	s_nop 2
	global_load_lds_dwordx4 v1, s[42:43]
	s_mov_b32 m0, s33
	s_add_u32 s56, s42, 0x20000
	s_mov_b32 s33, m0
	s_mov_b32 m0, s68
	s_nop 2
	global_load_lds_dwordx4 v163, s[42:43]
	s_mov_b32 m0, s33
	s_addc_u32 s57, s43, 0
	s_mov_b32 s33, m0
	s_mov_b32 m0, s69
	s_nop 2
	global_load_lds_dwordx4 v1, s[56:57]
	s_mov_b32 m0, s33
	s_nop 0
	s_mov_b32 s33, m0
	s_mov_b32 m0, s76
	s_nop 2
	global_load_lds_dwordx4 v163, s[56:57]
	s_mov_b32 m0, s33
	s_nop 0
	s_mov_b32 s33, m0
	s_mov_b32 m0, s15
	s_nop 2
	global_load_lds_dwordx4 v168, s[54:55]
	s_mov_b32 m0, s33
	s_nop 0
	s_mov_b32 s33, m0
	s_mov_b32 m0, s79
	s_nop 2
	global_load_lds_dwordx4 v172, s[54:55]
	s_mov_b32 m0, s33
	s_waitcnt vmcnt(8)
	s_waitcnt lgkmcnt(0)
	s_setprio 1
	s_barrier
	v_mfma_f32_16x16x128_f8f6f4 v[94:97], v[18:25], v[180:187], 0
	v_mfma_f32_16x16x128_f8f6f4 v[90:93], v[26:33], v[180:187], 0
	v_mfma_f32_16x16x128_f8f6f4 v[86:89], v[18:25], v[188:195], 0
	v_mfma_f32_16x16x128_f8f6f4 v[82:85], v[26:33], v[188:195], 0
	v_mfma_f32_16x16x128_f8f6f4 v[78:81], v[18:25], v[196:203], 0
	v_mfma_f32_16x16x128_f8f6f4 v[74:77], v[26:33], v[196:203], 0
	v_mfma_f32_16x16x128_f8f6f4 v[70:73], v[18:25], v[204:211], 0
	v_mfma_f32_16x16x128_f8f6f4 v[66:69], v[26:33], v[204:211], 0
	v_mfma_f32_16x16x128_f8f6f4 v[62:65], v[2:9], v[180:187], 0
	v_mfma_f32_16x16x128_f8f6f4 v[58:61], v[10:17], v[180:187], 0
	v_mfma_f32_16x16x128_f8f6f4 v[54:57], v[2:9], v[188:195], 0
	v_mfma_f32_16x16x128_f8f6f4 v[50:53], v[10:17], v[188:195], 0
	v_mfma_f32_16x16x128_f8f6f4 v[46:49], v[2:9], v[196:203], 0
	v_mfma_f32_16x16x128_f8f6f4 v[42:45], v[10:17], v[196:203], 0
	v_mfma_f32_16x16x128_f8f6f4 v[38:41], v[2:9], v[204:211], 0
	v_mfma_f32_16x16x128_f8f6f4 v[34:37], v[10:17], v[204:211], 0
	s_setprio 0
	s_barrier
	s_branch .Lmid6

.LBB0_1943:
	s_add_u32 s54, s38, 0x80
	s_addc_u32 s55, s39, 0
	v_add_u32_e32 v2, 0x10000, v174
	v_add_u32_e32 v14, 0x14000, v174
	s_add_u32 s38, s38, 0x100
	ds_read_b128 v[18:21], v2
	ds_read_b128 v[22:25], v2 offset:1024
	ds_read_b128 v[26:29], v2 offset:2048
	ds_read_b128 v[30:33], v2 offset:3072
	ds_read_b128 v[2:5], v14
	ds_read_b128 v[6:9], v14 offset:1024
	ds_read_b128 v[10:13], v14 offset:2048
	ds_read_b128 v[14:17], v14 offset:3072
	s_addc_u32 s39, s39, 0
	s_and_b64 s[40:41], s[40:41], exec
	s_cselect_b32 s52, s10, s38
	s_cselect_b32 s53, s11, s39
	s_cselect_b32 s41, s1, s87
	s_cselect_b32 s40, s0, s86
	s_add_u32 s42, s52, 0x80
	s_addc_u32 s43, s53, 0
	s_add_u32 s44, s40, 0x80
	s_addc_u32 s45, s41, 0
	ds_read_b128 v[180:183], v175
	ds_read_b128 v[184:187], v175 offset:1024
	ds_read_b128 v[188:191], v175 offset:2048
	ds_read_b128 v[192:195], v175 offset:3072
	ds_read_b128 v[196:199], v175 offset:4096
	ds_read_b128 v[200:203], v175 offset:5120
	ds_read_b128 v[204:207], v175 offset:6144
	ds_read_b128 v[208:211], v175 offset:7168
	s_mov_b32 s33, m0
	s_mov_b32 m0, s78
	s_nop 2
	global_load_lds_dwordx4 v164, s[54:55]
	s_mov_b32 m0, s33
	s_nop 0
	s_mov_b32 s33, m0
	s_mov_b32 m0, s79
	s_nop 2
	global_load_lds_dwordx4 v166, s[54:55]
	s_mov_b32 m0, s33
	s_waitcnt vmcnt(8)
	s_waitcnt lgkmcnt(0)
	s_setprio 1
	s_barrier
	v_mfma_f32_16x16x128_f8f6f4 v[158:161], v[18:25], v[180:187], v[158:161]
	v_mfma_f32_16x16x128_f8f6f4 v[150:153], v[26:33], v[180:187], v[150:153]
	v_mfma_f32_16x16x128_f8f6f4 v[142:145], v[18:25], v[188:195], v[142:145]
	v_mfma_f32_16x16x128_f8f6f4 v[134:137], v[26:33], v[188:195], v[134:137]
	v_mfma_f32_16x16x128_f8f6f4 v[126:129], v[18:25], v[196:203], v[126:129]
	v_mfma_f32_16x16x128_f8f6f4 v[118:121], v[26:33], v[196:203], v[118:121]
	v_mfma_f32_16x16x128_f8f6f4 v[110:113], v[18:25], v[204:211], v[110:113]
	v_mfma_f32_16x16x128_f8f6f4 v[102:105], v[26:33], v[204:211], v[102:105]
	v_mfma_f32_16x16x128_f8f6f4 v[154:157], v[2:9], v[180:187], v[154:157]
	v_mfma_f32_16x16x128_f8f6f4 v[146:149], v[10:17], v[180:187], v[146:149]
	v_mfma_f32_16x16x128_f8f6f4 v[138:141], v[2:9], v[188:195], v[138:141]
	v_mfma_f32_16x16x128_f8f6f4 v[130:133], v[10:17], v[188:195], v[130:133]
	v_mfma_f32_16x16x128_f8f6f4 v[122:125], v[2:9], v[196:203], v[122:125]
	v_mfma_f32_16x16x128_f8f6f4 v[114:117], v[10:17], v[196:203], v[114:117]
	v_mfma_f32_16x16x128_f8f6f4 v[106:109], v[2:9], v[204:211], v[106:109]
	v_mfma_f32_16x16x128_f8f6f4 v[98:101], v[10:17], v[204:211], v[98:101]
	s_setprio 0
	s_barrier
	ds_read_b128 v[180:183], v175 offset:16384
	ds_read_b128 v[184:187], v175 offset:17408
	ds_read_b128 v[188:191], v175 offset:18432
	ds_read_b128 v[192:195], v175 offset:19456
	ds_read_b128 v[196:199], v175 offset:20480
	ds_read_b128 v[200:203], v175 offset:21504
	ds_read_b128 v[204:207], v175 offset:22528
	ds_read_b128 v[208:211], v175 offset:23552
	s_mov_b32 s33, m0
	s_mov_b32 m0, s34
	s_nop 2
	global_load_lds_dwordx4 v165, s[40:41]
	s_mov_b32 m0, s33
	s_add_u32 s54, s40, 0x20000
	s_mov_b32 s33, m0
	s_mov_b32 m0, s35
	s_nop 2
	global_load_lds_dwordx4 v167, s[40:41]
	s_mov_b32 m0, s33
	s_addc_u32 s55, s41, 0
	s_mov_b32 s33, m0
	s_mov_b32 m0, s36
	s_nop 2
	global_load_lds_dwordx4 v165, s[54:55]
	s_mov_b32 m0, s33
	s_nop 0
	s_mov_b32 s33, m0
	s_mov_b32 m0, s37
	s_nop 2
	global_load_lds_dwordx4 v167, s[54:55]
	s_mov_b32 m0, s33
	s_nop 0
	s_mov_b32 s33, m0
	s_mov_b32 m0, s31
	s_nop 2
	global_load_lds_dwordx4 v171, s[52:53]
	s_mov_b32 m0, s33
	s_nop 0
	s_mov_b32 s33, m0
	s_mov_b32 m0, s56
	s_nop 2
	global_load_lds_dwordx4 v173, s[52:53]
	s_mov_b32 m0, s33
	s_waitcnt vmcnt(8)
	s_waitcnt lgkmcnt(0)
	s_setprio 1
	s_barrier
	v_mfma_f32_16x16x128_f8f6f4 v[94:97], v[18:25], v[180:187], v[94:97]
	v_mfma_f32_16x16x128_f8f6f4 v[86:89], v[26:33], v[180:187], v[86:89]
	v_mfma_f32_16x16x128_f8f6f4 v[78:81], v[18:25], v[188:195], v[78:81]
	v_mfma_f32_16x16x128_f8f6f4 v[70:73], v[26:33], v[188:195], v[70:73]
	v_mfma_f32_16x16x128_f8f6f4 v[62:65], v[18:25], v[196:203], v[62:65]
	v_mfma_f32_16x16x128_f8f6f4 v[54:57], v[26:33], v[196:203], v[54:57]
	v_mfma_f32_16x16x128_f8f6f4 v[46:49], v[18:25], v[204:211], v[46:49]
	v_mfma_f32_16x16x128_f8f6f4 v[38:41], v[26:33], v[204:211], v[38:41]
	v_mfma_f32_16x16x128_f8f6f4 v[90:93], v[2:9], v[180:187], v[90:93]
	v_mfma_f32_16x16x128_f8f6f4 v[82:85], v[10:17], v[180:187], v[82:85]
	v_mfma_f32_16x16x128_f8f6f4 v[74:77], v[2:9], v[188:195], v[74:77]
	v_mfma_f32_16x16x128_f8f6f4 v[66:69], v[10:17], v[188:195], v[66:69]
	v_mfma_f32_16x16x128_f8f6f4 v[58:61], v[2:9], v[196:203], v[58:61]
	v_mfma_f32_16x16x128_f8f6f4 v[50:53], v[10:17], v[196:203], v[50:53]
	v_mfma_f32_16x16x128_f8f6f4 v[42:45], v[2:9], v[204:211], v[42:45]
	v_mfma_f32_16x16x128_f8f6f4 v[34:37], v[10:17], v[204:211], v[34:37]
	s_setprio 0
	s_barrier
	v_add_u32_e32 v14, 0x18000, v174
	v_add_u32_e32 v30, 0x1c000, v174
	ds_read_b128 v[2:5], v14
	ds_read_b128 v[6:9], v14 offset:1024
	ds_read_b128 v[10:13], v14 offset:2048
	ds_read_b128 v[14:17], v14 offset:3072
	ds_read_b128 v[18:21], v30
	ds_read_b128 v[22:25], v30 offset:1024
	ds_read_b128 v[26:29], v30 offset:2048
	ds_read_b128 v[30:33], v30 offset:3072
	ds_read_b128 v[180:183], v175 offset:32768
	ds_read_b128 v[184:187], v175 offset:33792
	ds_read_b128 v[188:191], v175 offset:34816
	ds_read_b128 v[192:195], v175 offset:35840
	ds_read_b128 v[196:199], v175 offset:36864
	ds_read_b128 v[200:203], v175 offset:37888
	ds_read_b128 v[204:207], v175 offset:38912
	ds_read_b128 v[208:211], v175 offset:39936
	s_mov_b32 s33, m0
	s_mov_b32 m0, s57
	s_nop 2
	global_load_lds_dwordx4 v177, s[52:53]
	s_mov_b32 m0, s33
	s_nop 0
	s_mov_b32 s33, m0
	s_mov_b32 m0, s63
	s_nop 2
	global_load_lds_dwordx4 v178, s[52:53]
	s_mov_b32 m0, s33
	s_waitcnt vmcnt(8)
	s_waitcnt lgkmcnt(0)
	s_setprio 1
	s_barrier
	v_mfma_f32_16x16x128_f8f6f4 v[158:161], v[2:9], v[180:187], v[158:161]
	v_mfma_f32_16x16x128_f8f6f4 v[150:153], v[10:17], v[180:187], v[150:153]
	v_mfma_f32_16x16x128_f8f6f4 v[142:145], v[2:9], v[188:195], v[142:145]
	v_mfma_f32_16x16x128_f8f6f4 v[134:137], v[10:17], v[188:195], v[134:137]
	v_mfma_f32_16x16x128_f8f6f4 v[126:129], v[2:9], v[196:203], v[126:129]
	v_mfma_f32_16x16x128_f8f6f4 v[118:121], v[10:17], v[196:203], v[118:121]
	v_mfma_f32_16x16x128_f8f6f4 v[110:113], v[2:9], v[204:211], v[110:113]
	v_mfma_f32_16x16x128_f8f6f4 v[102:105], v[10:17], v[204:211], v[102:105]
	v_mfma_f32_16x16x128_f8f6f4 v[154:157], v[18:25], v[180:187], v[154:157]
	v_mfma_f32_16x16x128_f8f6f4 v[146:149], v[26:33], v[180:187], v[146:149]
	v_mfma_f32_16x16x128_f8f6f4 v[138:141], v[18:25], v[188:195], v[138:141]
	v_mfma_f32_16x16x128_f8f6f4 v[130:133], v[26:33], v[188:195], v[130:133]
	v_mfma_f32_16x16x128_f8f6f4 v[122:125], v[18:25], v[196:203], v[122:125]
	v_mfma_f32_16x16x128_f8f6f4 v[114:117], v[26:33], v[196:203], v[114:117]
	v_mfma_f32_16x16x128_f8f6f4 v[106:109], v[18:25], v[204:211], v[106:109]
	v_mfma_f32_16x16x128_f8f6f4 v[98:101], v[26:33], v[204:211], v[98:101]
	s_setprio 0
	s_barrier
	ds_read_b128 v[180:183], v175 offset:49152
	ds_read_b128 v[184:187], v175 offset:50176
	ds_read_b128 v[188:191], v175 offset:51200
	ds_read_b128 v[192:195], v175 offset:52224
	ds_read_b128 v[196:199], v175 offset:53248
	ds_read_b128 v[200:203], v175 offset:54272
	ds_read_b128 v[204:207], v175 offset:55296
	ds_read_b128 v[208:211], v175 offset:56320
	s_mov_b32 s33, m0
	s_mov_b32 m0, s66
	s_nop 2
	global_load_lds_dwordx4 v165, s[44:45]
	s_mov_b32 m0, s33
	s_add_u32 s40, s40, 0x20080
	s_mov_b32 s33, m0
	s_mov_b32 m0, s67
	s_nop 2
	global_load_lds_dwordx4 v167, s[44:45]
	s_mov_b32 m0, s33
	s_addc_u32 s41, s41, 0
	s_mov_b32 s33, m0
	s_mov_b32 m0, s76
	s_nop 2
	global_load_lds_dwordx4 v165, s[40:41]
	s_mov_b32 m0, s33
	s_nop 0
	s_mov_b32 s33, m0
	s_mov_b32 m0, s77
	s_nop 2
	global_load_lds_dwordx4 v167, s[40:41]
	s_mov_b32 m0, s33
	s_nop 0
	s_mov_b32 s33, m0
	s_mov_b32 m0, s68
	s_nop 2
	global_load_lds_dwordx4 v171, s[42:43]
	s_mov_b32 m0, s33
	s_nop 0
	s_mov_b32 s33, m0
	s_mov_b32 m0, s69
	s_nop 2
	global_load_lds_dwordx4 v173, s[42:43]
	s_mov_b32 m0, s33
	s_waitcnt vmcnt(8)
	s_waitcnt lgkmcnt(0)
	s_setprio 1
	s_barrier
	v_mfma_f32_16x16x128_f8f6f4 v[94:97], v[2:9], v[180:187], v[94:97]
	v_mfma_f32_16x16x128_f8f6f4 v[86:89], v[10:17], v[180:187], v[86:89]
	v_mfma_f32_16x16x128_f8f6f4 v[78:81], v[2:9], v[188:195], v[78:81]
	v_mfma_f32_16x16x128_f8f6f4 v[70:73], v[10:17], v[188:195], v[70:73]
	v_mfma_f32_16x16x128_f8f6f4 v[62:65], v[2:9], v[196:203], v[62:65]
	v_mfma_f32_16x16x128_f8f6f4 v[54:57], v[10:17], v[196:203], v[54:57]
	v_mfma_f32_16x16x128_f8f6f4 v[46:49], v[2:9], v[204:211], v[46:49]
	v_mfma_f32_16x16x128_f8f6f4 v[38:41], v[10:17], v[204:211], v[38:41]
	v_mfma_f32_16x16x128_f8f6f4 v[90:93], v[18:25], v[180:187], v[90:93]
	v_mfma_f32_16x16x128_f8f6f4 v[82:85], v[26:33], v[180:187], v[82:85]
	v_mfma_f32_16x16x128_f8f6f4 v[74:77], v[18:25], v[188:195], v[74:77]
	v_mfma_f32_16x16x128_f8f6f4 v[66:69], v[26:33], v[188:195], v[66:69]
	v_mfma_f32_16x16x128_f8f6f4 v[58:61], v[18:25], v[196:203], v[58:61]
	v_mfma_f32_16x16x128_f8f6f4 v[50:53], v[26:33], v[196:203], v[50:53]
	v_mfma_f32_16x16x128_f8f6f4 v[42:45], v[18:25], v[204:211], v[42:45]
	v_mfma_f32_16x16x128_f8f6f4 v[34:37], v[26:33], v[204:211], v[34:37]
	s_setprio 0
	s_barrier
	s_add_i32 s88, s88, 2
	s_add_u32 s86, s86, 0x100
	s_addc_u32 s87, s87, 0
	s_cmp_gt_u32 s88, 5
	s_cbranch_scc1 .LBB0_1957

.LBB0_2092:
	s_cmp_eq_u32 s91, 0
	s_cbranch_scc1 .Lpeel7
	s_lshl_b32 s33, s91, 7
	s_add_u32 s52, s36, s33
	s_addc_u32 s53, s37, 0
	s_add_u32 s46, s52, 0x100
	s_addc_u32 s47, s53, 0
	s_and_b64 s[44:45], s[42:43], exec
	s_cselect_b32 s49, s15, s47
	s_cselect_b32 s48, s17, s46
	s_add_u32 s33, s26, s33
	v_add_u32_e32 v2, 0x10000, v171
	v_add_u32_e32 v14, 0x14000, v171
	s_addc_u32 s44, s27, 0
	ds_read_b128 v[18:21], v2
	ds_read_b128 v[22:25], v2 offset:1024
	ds_read_b128 v[26:29], v2 offset:2048
	ds_read_b128 v[30:33], v2 offset:3072
	ds_read_b128 v[2:5], v14
	ds_read_b128 v[6:9], v14 offset:1024
	ds_read_b128 v[10:13], v14 offset:2048
	ds_read_b128 v[14:17], v14 offset:3072
	s_add_u32 s33, s33, 0x100
	s_addc_u32 s44, s44, 0
	s_and_b64 s[42:43], s[42:43], exec
	s_cselect_b32 s43, s19, s44
	s_cselect_b32 s42, s18, s33
	s_add_u32 s44, s48, 0x80
	s_addc_u32 s45, s49, 0
	s_add_u32 s46, s42, 0x80
	s_addc_u32 s47, s43, 0
	ds_read_b128 v[176:179], v172
	ds_read_b128 v[180:183], v172 offset:1024
	ds_read_b128 v[184:187], v172 offset:2048
	ds_read_b128 v[188:191], v172 offset:3072
	ds_read_b128 v[192:195], v172 offset:4096
	ds_read_b128 v[196:199], v172 offset:5120
	ds_read_b128 v[200:203], v172 offset:6144
	ds_read_b128 v[204:207], v172 offset:7168
	s_add_u32 s52, s52, 0x20080
	s_addc_u32 s53, s53, 0
	s_mov_b32 s33, m0
	s_mov_b32 m0, s79
	s_nop 2
	global_load_lds_dwordx4 v163, s[52:53]
	s_mov_b32 m0, s33
	s_nop 0
	s_mov_b32 s33, m0
	s_mov_b32 m0, s80
	s_nop 2
	global_load_lds_dwordx4 v164, s[52:53]
	s_mov_b32 m0, s33
	s_waitcnt vmcnt(8)
	s_waitcnt lgkmcnt(0)
	s_setprio 1
	s_barrier
	v_mfma_f32_16x16x128_f8f6f4 v[158:161], v[18:25], v[176:183], v[158:161]
	v_mfma_f32_16x16x128_f8f6f4 v[154:157], v[26:33], v[176:183], v[154:157]
	v_mfma_f32_16x16x128_f8f6f4 v[142:145], v[18:25], v[184:191], v[142:145]
	v_mfma_f32_16x16x128_f8f6f4 v[138:141], v[26:33], v[184:191], v[138:141]
	v_mfma_f32_16x16x128_f8f6f4 v[126:129], v[18:25], v[192:199], v[126:129]
	v_mfma_f32_16x16x128_f8f6f4 v[122:125], v[26:33], v[192:199], v[122:125]
	v_mfma_f32_16x16x128_f8f6f4 v[110:113], v[18:25], v[200:207], v[110:113]
	v_mfma_f32_16x16x128_f8f6f4 v[106:109], v[26:33], v[200:207], v[106:109]
	v_mfma_f32_16x16x128_f8f6f4 v[150:153], v[2:9], v[176:183], v[150:153]
	v_mfma_f32_16x16x128_f8f6f4 v[146:149], v[10:17], v[176:183], v[146:149]
	v_mfma_f32_16x16x128_f8f6f4 v[134:137], v[2:9], v[184:191], v[134:137]
	v_mfma_f32_16x16x128_f8f6f4 v[130:133], v[10:17], v[184:191], v[130:133]
	v_mfma_f32_16x16x128_f8f6f4 v[118:121], v[2:9], v[192:199], v[118:121]
	v_mfma_f32_16x16x128_f8f6f4 v[114:117], v[10:17], v[192:199], v[114:117]
	v_mfma_f32_16x16x128_f8f6f4 v[102:105], v[2:9], v[200:207], v[102:105]
	v_mfma_f32_16x16x128_f8f6f4 v[98:101], v[10:17], v[200:207], v[98:101]
	s_setprio 0
	s_barrier
	ds_read_b128 v[176:179], v172 offset:16384
	ds_read_b128 v[180:183], v172 offset:17408
	ds_read_b128 v[184:187], v172 offset:18432
	ds_read_b128 v[188:191], v172 offset:19456
	ds_read_b128 v[192:195], v172 offset:20480
	ds_read_b128 v[196:199], v172 offset:21504
	ds_read_b128 v[200:203], v172 offset:22528
	ds_read_b128 v[204:207], v172 offset:23552
	s_mov_b32 s33, m0
	s_mov_b32 m0, s64
	s_nop 2
	global_load_lds_dwordx4 v1, s[42:43]
	s_mov_b32 m0, s33
	s_add_u32 s52, s42, 0x20000
	s_mov_b32 s33, m0
	s_mov_b32 m0, s65
	s_nop 2
	global_load_lds_dwordx4 v162, s[42:43]
	s_mov_b32 m0, s33
	s_addc_u32 s53, s43, 0
	s_mov_b32 s33, m0
	s_mov_b32 m0, s24
	s_nop 2
	global_load_lds_dwordx4 v1, s[52:53]
	s_mov_b32 m0, s33
	s_nop 0
	s_mov_b32 s33, m0
	s_mov_b32 m0, s25
	s_nop 2
	global_load_lds_dwordx4 v162, s[52:53]
	s_mov_b32 m0, s33
	s_nop 0
	s_mov_b32 s33, m0
	s_mov_b32 m0, s63
	s_nop 2
	global_load_lds_dwordx4 v163, s[48:49]
	s_mov_b32 m0, s33
	s_nop 0
	s_mov_b32 s33, m0
	s_mov_b32 m0, s2
	s_nop 2
	global_load_lds_dwordx4 v164, s[48:49]
	s_mov_b32 m0, s33
	s_waitcnt vmcnt(8)
	s_waitcnt lgkmcnt(0)
	s_setprio 1
	s_barrier
	v_mfma_f32_16x16x128_f8f6f4 v[94:97], v[18:25], v[176:183], v[94:97]
	v_mfma_f32_16x16x128_f8f6f4 v[90:93], v[26:33], v[176:183], v[90:93]
	v_mfma_f32_16x16x128_f8f6f4 v[78:81], v[18:25], v[184:191], v[78:81]
	v_mfma_f32_16x16x128_f8f6f4 v[74:77], v[26:33], v[184:191], v[74:77]
	v_mfma_f32_16x16x128_f8f6f4 v[62:65], v[18:25], v[192:199], v[62:65]
	v_mfma_f32_16x16x128_f8f6f4 v[58:61], v[26:33], v[192:199], v[58:61]
	v_mfma_f32_16x16x128_f8f6f4 v[46:49], v[18:25], v[200:207], v[46:49]
	v_mfma_f32_16x16x128_f8f6f4 v[42:45], v[26:33], v[200:207], v[42:45]
	v_mfma_f32_16x16x128_f8f6f4 v[86:89], v[2:9], v[176:183], v[86:89]
	v_mfma_f32_16x16x128_f8f6f4 v[82:85], v[10:17], v[176:183], v[82:85]
	v_mfma_f32_16x16x128_f8f6f4 v[70:73], v[2:9], v[184:191], v[70:73]
	v_mfma_f32_16x16x128_f8f6f4 v[66:69], v[10:17], v[184:191], v[66:69]
	v_mfma_f32_16x16x128_f8f6f4 v[54:57], v[2:9], v[192:199], v[54:57]
	v_mfma_f32_16x16x128_f8f6f4 v[50:53], v[10:17], v[192:199], v[50:53]
	v_mfma_f32_16x16x128_f8f6f4 v[38:41], v[2:9], v[200:207], v[38:41]
	v_mfma_f32_16x16x128_f8f6f4 v[34:37], v[10:17], v[200:207], v[34:37]
	s_setprio 0
	s_barrier
.Lmid7:
	v_add_u32_e32 v14, 0x18000, v171
	v_add_u32_e32 v30, 0x1c000, v171
	ds_read_b128 v[2:5], v14
	ds_read_b128 v[6:9], v14 offset:1024
	ds_read_b128 v[10:13], v14 offset:2048
	ds_read_b128 v[14:17], v14 offset:3072
	ds_read_b128 v[18:21], v30
	ds_read_b128 v[22:25], v30 offset:1024
	ds_read_b128 v[26:29], v30 offset:2048
	ds_read_b128 v[30:33], v30 offset:3072
	ds_read_b128 v[176:179], v172 offset:32768
	ds_read_b128 v[180:183], v172 offset:33792
	ds_read_b128 v[184:187], v172 offset:34816
	ds_read_b128 v[188:191], v172 offset:35840
	ds_read_b128 v[192:195], v172 offset:36864
	ds_read_b128 v[196:199], v172 offset:37888
	ds_read_b128 v[200:203], v172 offset:38912
	ds_read_b128 v[204:207], v172 offset:39936
	s_add_u32 s48, s48, 0x20000
	s_addc_u32 s49, s49, 0
	s_mov_b32 s33, m0
	s_mov_b32 m0, s23
	s_nop 2
	global_load_lds_dwordx4 v163, s[48:49]
	s_mov_b32 m0, s33
	s_nop 0
	s_mov_b32 s33, m0
	s_mov_b32 m0, s28
	s_nop 2
	global_load_lds_dwordx4 v164, s[48:49]
	s_mov_b32 m0, s33
	s_waitcnt vmcnt(8)
	s_waitcnt lgkmcnt(0)
	s_setprio 1
	s_barrier
	v_mfma_f32_16x16x128_f8f6f4 v[158:161], v[2:9], v[176:183], v[158:161]
	v_mfma_f32_16x16x128_f8f6f4 v[154:157], v[10:17], v[176:183], v[154:157]
	v_mfma_f32_16x16x128_f8f6f4 v[142:145], v[2:9], v[184:191], v[142:145]
	v_mfma_f32_16x16x128_f8f6f4 v[138:141], v[10:17], v[184:191], v[138:141]
	v_mfma_f32_16x16x128_f8f6f4 v[126:129], v[2:9], v[192:199], v[126:129]
	v_mfma_f32_16x16x128_f8f6f4 v[122:125], v[10:17], v[192:199], v[122:125]
	v_mfma_f32_16x16x128_f8f6f4 v[110:113], v[2:9], v[200:207], v[110:113]
	v_mfma_f32_16x16x128_f8f6f4 v[106:109], v[10:17], v[200:207], v[106:109]
	v_mfma_f32_16x16x128_f8f6f4 v[150:153], v[18:25], v[176:183], v[150:153]
	v_mfma_f32_16x16x128_f8f6f4 v[146:149], v[26:33], v[176:183], v[146:149]
	v_mfma_f32_16x16x128_f8f6f4 v[134:137], v[18:25], v[184:191], v[134:137]
	v_mfma_f32_16x16x128_f8f6f4 v[130:133], v[26:33], v[184:191], v[130:133]
	v_mfma_f32_16x16x128_f8f6f4 v[118:121], v[18:25], v[192:199], v[118:121]
	v_mfma_f32_16x16x128_f8f6f4 v[114:117], v[26:33], v[192:199], v[114:117]
	v_mfma_f32_16x16x128_f8f6f4 v[102:105], v[18:25], v[200:207], v[102:105]
	v_mfma_f32_16x16x128_f8f6f4 v[98:101], v[26:33], v[200:207], v[98:101]
	s_setprio 0
	s_barrier
	ds_read_b128 v[176:179], v172 offset:49152
	ds_read_b128 v[180:183], v172 offset:50176
	ds_read_b128 v[184:187], v172 offset:51200
	ds_read_b128 v[188:191], v172 offset:52224
	ds_read_b128 v[192:195], v172 offset:53248
	ds_read_b128 v[196:199], v172 offset:54272
	ds_read_b128 v[200:203], v172 offset:55296
	ds_read_b128 v[204:207], v172 offset:56320
	s_mov_b32 s33, m0
	s_mov_b32 m0, s67
	s_nop 2
	global_load_lds_dwordx4 v1, s[46:47]
	s_mov_b32 m0, s33
	s_add_u32 s42, s42, 0x20080
	s_mov_b32 s33, m0
	s_mov_b32 m0, s68
	s_nop 2
	global_load_lds_dwordx4 v162, s[46:47]
	s_mov_b32 m0, s33
	s_addc_u32 s43, s43, 0
	s_mov_b32 s33, m0
	s_mov_b32 m0, s77
	s_nop 2
	global_load_lds_dwordx4 v1, s[42:43]
	s_mov_b32 m0, s33
	s_nop 0
	s_mov_b32 s33, m0
	s_mov_b32 m0, s78
	s_nop 2
	global_load_lds_dwordx4 v162, s[42:43]
	s_mov_b32 m0, s33
	s_nop 0
	s_mov_b32 s33, m0
	s_mov_b32 m0, s69
	s_nop 2
	global_load_lds_dwordx4 v163, s[44:45]
	s_mov_b32 m0, s33
	s_nop 0
	s_mov_b32 s33, m0
	s_mov_b32 m0, s76
	s_nop 2
	global_load_lds_dwordx4 v164, s[44:45]
	s_mov_b32 m0, s33
	s_waitcnt vmcnt(8)
	s_waitcnt lgkmcnt(0)
	s_setprio 1
	s_barrier
	v_mfma_f32_16x16x128_f8f6f4 v[94:97], v[2:9], v[176:183], v[94:97]
	v_mfma_f32_16x16x128_f8f6f4 v[90:93], v[10:17], v[176:183], v[90:93]
	v_mfma_f32_16x16x128_f8f6f4 v[78:81], v[2:9], v[184:191], v[78:81]
	v_mfma_f32_16x16x128_f8f6f4 v[74:77], v[10:17], v[184:191], v[74:77]
	v_mfma_f32_16x16x128_f8f6f4 v[62:65], v[2:9], v[192:199], v[62:65]
	v_mfma_f32_16x16x128_f8f6f4 v[58:61], v[10:17], v[192:199], v[58:61]
	v_mfma_f32_16x16x128_f8f6f4 v[46:49], v[2:9], v[200:207], v[46:49]
	v_mfma_f32_16x16x128_f8f6f4 v[42:45], v[10:17], v[200:207], v[42:45]
	v_mfma_f32_16x16x128_f8f6f4 v[86:89], v[18:25], v[176:183], v[86:89]
	v_mfma_f32_16x16x128_f8f6f4 v[82:85], v[26:33], v[176:183], v[82:85]
	v_mfma_f32_16x16x128_f8f6f4 v[70:73], v[18:25], v[184:191], v[70:73]
	v_mfma_f32_16x16x128_f8f6f4 v[66:69], v[26:33], v[184:191], v[66:69]
	v_mfma_f32_16x16x128_f8f6f4 v[54:57], v[18:25], v[192:199], v[54:57]
	v_mfma_f32_16x16x128_f8f6f4 v[50:53], v[26:33], v[192:199], v[50:53]
	v_mfma_f32_16x16x128_f8f6f4 v[38:41], v[18:25], v[200:207], v[38:41]
	v_mfma_f32_16x16x128_f8f6f4 v[34:37], v[26:33], v[200:207], v[34:37]
	s_setprio 0
	s_cmp_lt_u32 s91, 6
	s_cbranch_scc1 .Lkb7_do
	s_cmp_lg_u64 s[12:13], 0
	s_cbranch_scc0 .Lkb7_skip

.Lpeel7:
	s_lshl_b32 s33, s91, 7
	s_add_u32 s52, s36, s33
	s_addc_u32 s53, s37, 0
	s_add_u32 s46, s52, 0x100
	s_addc_u32 s47, s53, 0
	s_and_b64 s[44:45], s[42:43], exec
	s_cselect_b32 s49, s15, s47
	s_cselect_b32 s48, s17, s46
	s_add_u32 s33, s26, s33
	v_add_u32_e32 v2, 0x10000, v171
	v_add_u32_e32 v14, 0x14000, v171
	s_addc_u32 s44, s27, 0
	ds_read_b128 v[18:21], v2
	ds_read_b128 v[22:25], v2 offset:1024
	ds_read_b128 v[26:29], v2 offset:2048
	ds_read_b128 v[30:33], v2 offset:3072
	ds_read_b128 v[2:5], v14
	ds_read_b128 v[6:9], v14 offset:1024
	ds_read_b128 v[10:13], v14 offset:2048
	ds_read_b128 v[14:17], v14 offset:3072
	s_add_u32 s33, s33, 0x100
	s_addc_u32 s44, s44, 0
	s_and_b64 s[42:43], s[42:43], exec
	s_cselect_b32 s43, s19, s44
	s_cselect_b32 s42, s18, s33
	s_add_u32 s44, s48, 0x80
	s_addc_u32 s45, s49, 0
	s_add_u32 s46, s42, 0x80
	s_addc_u32 s47, s43, 0
	ds_read_b128 v[176:179], v172
	ds_read_b128 v[180:183], v172 offset:1024
	ds_read_b128 v[184:187], v172 offset:2048
	ds_read_b128 v[188:191], v172 offset:3072
	ds_read_b128 v[192:195], v172 offset:4096
	ds_read_b128 v[196:199], v172 offset:5120
	ds_read_b128 v[200:203], v172 offset:6144
	ds_read_b128 v[204:207], v172 offset:7168
	s_add_u32 s52, s52, 0x20080
	s_addc_u32 s53, s53, 0
	s_mov_b32 s33, m0
	s_mov_b32 m0, s79
	s_nop 2
	global_load_lds_dwordx4 v163, s[52:53]
	s_mov_b32 m0, s33
	s_nop 0
	s_mov_b32 s33, m0
	s_mov_b32 m0, s80
	s_nop 2
	global_load_lds_dwordx4 v164, s[52:53]
	s_mov_b32 m0, s33
	s_waitcnt vmcnt(8)
	s_waitcnt lgkmcnt(0)
	s_setprio 1
	s_barrier
	v_mfma_f32_16x16x128_f8f6f4 v[158:161], v[18:25], v[176:183], 0
	v_mfma_f32_16x16x128_f8f6f4 v[154:157], v[26:33], v[176:183], 0
	v_mfma_f32_16x16x128_f8f6f4 v[142:145], v[18:25], v[184:191], 0
	v_mfma_f32_16x16x128_f8f6f4 v[138:141], v[26:33], v[184:191], 0
	v_mfma_f32_16x16x128_f8f6f4 v[126:129], v[18:25], v[192:199], 0
	v_mfma_f32_16x16x128_f8f6f4 v[122:125], v[26:33], v[192:199], 0
	v_mfma_f32_16x16x128_f8f6f4 v[110:113], v[18:25], v[200:207], 0
	v_mfma_f32_16x16x128_f8f6f4 v[106:109], v[26:33], v[200:207], 0
	v_mfma_f32_16x16x128_f8f6f4 v[150:153], v[2:9], v[176:183], 0
	v_mfma_f32_16x16x128_f8f6f4 v[146:149], v[10:17], v[176:183], 0
	v_mfma_f32_16x16x128_f8f6f4 v[134:137], v[2:9], v[184:191], 0
	v_mfma_f32_16x16x128_f8f6f4 v[130:133], v[10:17], v[184:191], 0
	v_mfma_f32_16x16x128_f8f6f4 v[118:121], v[2:9], v[192:199], 0
	v_mfma_f32_16x16x128_f8f6f4 v[114:117], v[10:17], v[192:199], 0
	v_mfma_f32_16x16x128_f8f6f4 v[102:105], v[2:9], v[200:207], 0
	v_mfma_f32_16x16x128_f8f6f4 v[98:101], v[10:17], v[200:207], 0
	s_setprio 0
	s_barrier
	ds_read_b128 v[176:179], v172 offset:16384
	ds_read_b128 v[180:183], v172 offset:17408
	ds_read_b128 v[184:187], v172 offset:18432
	ds_read_b128 v[188:191], v172 offset:19456
	ds_read_b128 v[192:195], v172 offset:20480
	ds_read_b128 v[196:199], v172 offset:21504
	ds_read_b128 v[200:203], v172 offset:22528
	ds_read_b128 v[204:207], v172 offset:23552
	s_mov_b32 s33, m0
	s_mov_b32 m0, s64
	s_nop 2
	global_load_lds_dwordx4 v1, s[42:43]
	s_mov_b32 m0, s33
	s_add_u32 s52, s42, 0x20000
	s_mov_b32 s33, m0
	s_mov_b32 m0, s65
	s_nop 2
	global_load_lds_dwordx4 v162, s[42:43]
	s_mov_b32 m0, s33
	s_addc_u32 s53, s43, 0
	s_mov_b32 s33, m0
	s_mov_b32 m0, s24
	s_nop 2
	global_load_lds_dwordx4 v1, s[52:53]
	s_mov_b32 m0, s33
	s_nop 0
	s_mov_b32 s33, m0
	s_mov_b32 m0, s25
	s_nop 2
	global_load_lds_dwordx4 v162, s[52:53]
	s_mov_b32 m0, s33
	s_nop 0
	s_mov_b32 s33, m0
	s_mov_b32 m0, s63
	s_nop 2
	global_load_lds_dwordx4 v163, s[48:49]
	s_mov_b32 m0, s33
	s_nop 0
	s_mov_b32 s33, m0
	s_mov_b32 m0, s2
	s_nop 2
	global_load_lds_dwordx4 v164, s[48:49]
	s_mov_b32 m0, s33
	s_waitcnt vmcnt(8)
	s_waitcnt lgkmcnt(0)
	s_setprio 1
	s_barrier
	v_mfma_f32_16x16x128_f8f6f4 v[94:97], v[18:25], v[176:183], 0
	v_mfma_f32_16x16x128_f8f6f4 v[90:93], v[26:33], v[176:183], 0
	v_mfma_f32_16x16x128_f8f6f4 v[78:81], v[18:25], v[184:191], 0
	v_mfma_f32_16x16x128_f8f6f4 v[74:77], v[26:33], v[184:191], 0
	v_mfma_f32_16x16x128_f8f6f4 v[62:65], v[18:25], v[192:199], 0
	v_mfma_f32_16x16x128_f8f6f4 v[58:61], v[26:33], v[192:199], 0
	v_mfma_f32_16x16x128_f8f6f4 v[46:49], v[18:25], v[200:207], 0
	v_mfma_f32_16x16x128_f8f6f4 v[42:45], v[26:33], v[200:207], 0
	v_mfma_f32_16x16x128_f8f6f4 v[86:89], v[2:9], v[176:183], 0
	v_mfma_f32_16x16x128_f8f6f4 v[82:85], v[10:17], v[176:183], 0
	v_mfma_f32_16x16x128_f8f6f4 v[70:73], v[2:9], v[184:191], 0
	v_mfma_f32_16x16x128_f8f6f4 v[66:69], v[10:17], v[184:191], 0
	v_mfma_f32_16x16x128_f8f6f4 v[54:57], v[2:9], v[192:199], 0
	v_mfma_f32_16x16x128_f8f6f4 v[50:53], v[10:17], v[192:199], 0
	v_mfma_f32_16x16x128_f8f6f4 v[38:41], v[2:9], v[200:207], 0
	v_mfma_f32_16x16x128_f8f6f4 v[34:37], v[10:17], v[200:207], 0
	s_setprio 0
	s_barrier
	s_branch .Lmid7

.LBB0_2128:
	v_add_u32_e32 v0, 0x10000, v169
	v_add_u32_e32 v12, 0x14000, v169
	s_add_u32 s26, s22, 0x100
	ds_read_b128 v[16:19], v0
	ds_read_b128 v[20:23], v0 offset:1024
	ds_read_b128 v[24:27], v0 offset:2048
	ds_read_b128 v[28:31], v0 offset:3072
	ds_read_b128 v[0:3], v12
	ds_read_b128 v[4:7], v12 offset:1024
	ds_read_b128 v[8:11], v12 offset:2048
	ds_read_b128 v[12:15], v12 offset:3072
	s_addc_u32 s27, s23, 0
	s_cmp_eq_u32 s83, 4
	s_cselect_b32 s42, s15, s26
	s_cselect_b32 s43, s13, s27
	s_cselect_b32 s37, s17, s82
	s_cselect_b32 s36, s16, s81
	s_add_u32 s38, s42, 0x80
	s_addc_u32 s39, s43, 0
	s_add_u32 s40, s36, 0x80
	s_addc_u32 s41, s37, 0
	ds_read_b128 v[172:175], v170
	ds_read_b128 v[176:179], v170 offset:1024
	ds_read_b128 v[180:183], v170 offset:2048
	ds_read_b128 v[184:187], v170 offset:3072
	ds_read_b128 v[188:191], v170 offset:4096
	ds_read_b128 v[192:195], v170 offset:5120
	ds_read_b128 v[196:199], v170 offset:6144
	ds_read_b128 v[200:203], v170 offset:7168
	s_add_u32 s22, s22, 0x20080
	s_addc_u32 s23, s23, 0
	s_mov_b32 s33, m0
	s_mov_b32 m0, s64
	s_nop 2
	global_load_lds_dwordx4 v162, s[22:23]
	s_mov_b32 m0, s33
	s_nop 0
	s_mov_b32 s33, m0
	s_mov_b32 m0, s65
	s_nop 2
	global_load_lds_dwordx4 v164, s[22:23]
	s_mov_b32 m0, s33
	s_waitcnt vmcnt(8)
	s_waitcnt lgkmcnt(0)
	s_setprio 1
	s_barrier
	v_mfma_f32_16x16x128_f8f6f4 v[156:159], v[16:23], v[172:179], v[156:159]
	v_mfma_f32_16x16x128_f8f6f4 v[152:155], v[24:31], v[172:179], v[152:155]
	v_mfma_f32_16x16x128_f8f6f4 v[140:143], v[16:23], v[180:187], v[140:143]
	v_mfma_f32_16x16x128_f8f6f4 v[136:139], v[24:31], v[180:187], v[136:139]
	v_mfma_f32_16x16x128_f8f6f4 v[124:127], v[16:23], v[188:195], v[124:127]
	v_mfma_f32_16x16x128_f8f6f4 v[120:123], v[24:31], v[188:195], v[120:123]
	v_mfma_f32_16x16x128_f8f6f4 v[108:111], v[16:23], v[196:203], v[108:111]
	v_mfma_f32_16x16x128_f8f6f4 v[104:107], v[24:31], v[196:203], v[104:107]
	v_mfma_f32_16x16x128_f8f6f4 v[148:151], v[0:7], v[172:179], v[148:151]
	v_mfma_f32_16x16x128_f8f6f4 v[144:147], v[8:15], v[172:179], v[144:147]
	v_mfma_f32_16x16x128_f8f6f4 v[132:135], v[0:7], v[180:187], v[132:135]
	v_mfma_f32_16x16x128_f8f6f4 v[128:131], v[8:15], v[180:187], v[128:131]
	v_mfma_f32_16x16x128_f8f6f4 v[116:119], v[0:7], v[188:195], v[116:119]
	v_mfma_f32_16x16x128_f8f6f4 v[112:115], v[8:15], v[188:195], v[112:115]
	v_mfma_f32_16x16x128_f8f6f4 v[100:103], v[0:7], v[196:203], v[100:103]
	v_mfma_f32_16x16x128_f8f6f4 v[96:99], v[8:15], v[196:203], v[96:99]
	s_setprio 0
	s_barrier
	ds_read_b128 v[172:175], v170 offset:16384
	ds_read_b128 v[176:179], v170 offset:17408
	ds_read_b128 v[180:183], v170 offset:18432
	ds_read_b128 v[184:187], v170 offset:19456
	ds_read_b128 v[188:191], v170 offset:20480
	ds_read_b128 v[192:195], v170 offset:21504
	ds_read_b128 v[196:199], v170 offset:22528
	ds_read_b128 v[200:203], v170 offset:23552
	s_mov_b32 s22, m0
	s_mov_b32 m0, s31
	s_nop 2
	global_load_lds_dwordx4 v163, s[36:37]
	s_mov_b32 m0, s22
	s_nop 0
	s_mov_b32 s22, m0
	s_mov_b32 m0, s44
	s_nop 2
	global_load_lds_dwordx4 v165, s[36:37]
	s_mov_b32 m0, s22
	s_add_u32 s22, s36, 0x20000
	s_addc_u32 s23, s37, 0
	s_mov_b32 s33, m0
	s_mov_b32 m0, s45
	s_nop 2
	global_load_lds_dwordx4 v163, s[22:23]
	s_mov_b32 m0, s33
	s_nop 0
	s_mov_b32 s33, m0
	s_mov_b32 m0, s46
	s_nop 2
	global_load_lds_dwordx4 v165, s[22:23]
	s_mov_b32 m0, s33
	s_mov_b32 s22, m0
	s_mov_b32 m0, s21
	s_nop 2
	global_load_lds_dwordx4 v162, s[42:43]
	s_mov_b32 m0, s22
	s_nop 0
	s_mov_b32 s22, m0
	s_mov_b32 m0, s47
	s_nop 2
	global_load_lds_dwordx4 v164, s[42:43]
	s_mov_b32 m0, s22
	s_waitcnt vmcnt(8)
	s_waitcnt lgkmcnt(0)
	s_setprio 1
	s_barrier
	v_mfma_f32_16x16x128_f8f6f4 v[92:95], v[16:23], v[172:179], v[92:95]
	v_mfma_f32_16x16x128_f8f6f4 v[88:91], v[24:31], v[172:179], v[88:91]
	v_mfma_f32_16x16x128_f8f6f4 v[76:79], v[16:23], v[180:187], v[76:79]
	v_mfma_f32_16x16x128_f8f6f4 v[72:75], v[24:31], v[180:187], v[72:75]
	v_mfma_f32_16x16x128_f8f6f4 v[60:63], v[16:23], v[188:195], v[60:63]
	v_mfma_f32_16x16x128_f8f6f4 v[56:59], v[24:31], v[188:195], v[56:59]
	v_mfma_f32_16x16x128_f8f6f4 v[44:47], v[16:23], v[196:203], v[44:47]
	v_mfma_f32_16x16x128_f8f6f4 v[40:43], v[24:31], v[196:203], v[40:43]
	v_mfma_f32_16x16x128_f8f6f4 v[84:87], v[0:7], v[172:179], v[84:87]
	v_mfma_f32_16x16x128_f8f6f4 v[80:83], v[8:15], v[172:179], v[80:83]
	v_mfma_f32_16x16x128_f8f6f4 v[68:71], v[0:7], v[180:187], v[68:71]
	v_mfma_f32_16x16x128_f8f6f4 v[64:67], v[8:15], v[180:187], v[64:67]
	v_mfma_f32_16x16x128_f8f6f4 v[52:55], v[0:7], v[188:195], v[52:55]
	v_mfma_f32_16x16x128_f8f6f4 v[48:51], v[8:15], v[188:195], v[48:51]
	v_mfma_f32_16x16x128_f8f6f4 v[36:39], v[0:7], v[196:203], v[36:39]
	v_mfma_f32_16x16x128_f8f6f4 v[32:35], v[8:15], v[196:203], v[32:35]
	s_setprio 0
	s_barrier
	v_add_u32_e32 v12, 0x18000, v169
	v_add_u32_e32 v28, 0x1c000, v169
	ds_read_b128 v[0:3], v12
	ds_read_b128 v[4:7], v12 offset:1024
	ds_read_b128 v[8:11], v12 offset:2048
	ds_read_b128 v[12:15], v12 offset:3072
	ds_read_b128 v[16:19], v28
	ds_read_b128 v[20:23], v28 offset:1024
	ds_read_b128 v[24:27], v28 offset:2048
	ds_read_b128 v[28:31], v28 offset:3072
	ds_read_b128 v[172:175], v170 offset:32768
	ds_read_b128 v[176:179], v170 offset:33792
	ds_read_b128 v[180:183], v170 offset:34816
	ds_read_b128 v[184:187], v170 offset:35840
	ds_read_b128 v[188:191], v170 offset:36864
	ds_read_b128 v[192:195], v170 offset:37888
	ds_read_b128 v[196:199], v170 offset:38912
	ds_read_b128 v[200:203], v170 offset:39936
	s_add_u32 s22, s42, 0x20000
	s_addc_u32 s23, s43, 0
	s_mov_b32 s33, m0
	s_mov_b32 m0, s48
	s_nop 2
	global_load_lds_dwordx4 v162, s[22:23]
	s_mov_b32 m0, s33
	s_nop 0
	s_mov_b32 s33, m0
	s_mov_b32 m0, s49
	s_nop 2
	global_load_lds_dwordx4 v164, s[22:23]
	s_mov_b32 m0, s33
	s_waitcnt vmcnt(8)
	s_waitcnt lgkmcnt(0)
	s_setprio 1
	s_barrier
	v_mfma_f32_16x16x128_f8f6f4 v[156:159], v[0:7], v[172:179], v[156:159]
	v_mfma_f32_16x16x128_f8f6f4 v[152:155], v[8:15], v[172:179], v[152:155]
	v_mfma_f32_16x16x128_f8f6f4 v[140:143], v[0:7], v[180:187], v[140:143]
	v_mfma_f32_16x16x128_f8f6f4 v[136:139], v[8:15], v[180:187], v[136:139]
	v_mfma_f32_16x16x128_f8f6f4 v[124:127], v[0:7], v[188:195], v[124:127]
	v_mfma_f32_16x16x128_f8f6f4 v[120:123], v[8:15], v[188:195], v[120:123]
	v_mfma_f32_16x16x128_f8f6f4 v[108:111], v[0:7], v[196:203], v[108:111]
	v_mfma_f32_16x16x128_f8f6f4 v[104:107], v[8:15], v[196:203], v[104:107]
	v_mfma_f32_16x16x128_f8f6f4 v[148:151], v[16:23], v[172:179], v[148:151]
	v_mfma_f32_16x16x128_f8f6f4 v[144:147], v[24:31], v[172:179], v[144:147]
	v_mfma_f32_16x16x128_f8f6f4 v[132:135], v[16:23], v[180:187], v[132:135]
	v_mfma_f32_16x16x128_f8f6f4 v[128:131], v[24:31], v[180:187], v[128:131]
	v_mfma_f32_16x16x128_f8f6f4 v[116:119], v[16:23], v[188:195], v[116:119]
	v_mfma_f32_16x16x128_f8f6f4 v[112:115], v[24:31], v[188:195], v[112:115]
	v_mfma_f32_16x16x128_f8f6f4 v[100:103], v[16:23], v[196:203], v[100:103]
	v_mfma_f32_16x16x128_f8f6f4 v[96:99], v[24:31], v[196:203], v[96:99]
	s_setprio 0
	s_barrier
	ds_read_b128 v[172:175], v170 offset:49152
	ds_read_b128 v[176:179], v170 offset:50176
	ds_read_b128 v[180:183], v170 offset:51200
	ds_read_b128 v[184:187], v170 offset:52224
	ds_read_b128 v[188:191], v170 offset:53248
	ds_read_b128 v[192:195], v170 offset:54272
	ds_read_b128 v[196:199], v170 offset:55296
	ds_read_b128 v[200:203], v170 offset:56320
	s_mov_b32 s22, m0
	s_mov_b32 m0, s58
	s_nop 2
	global_load_lds_dwordx4 v163, s[40:41]
	s_mov_b32 m0, s22
	s_nop 0
	s_mov_b32 s22, m0
	s_mov_b32 m0, s59
	s_nop 2
	global_load_lds_dwordx4 v165, s[40:41]
	s_mov_b32 m0, s22
	s_add_u32 s22, s36, 0x20080
	s_addc_u32 s23, s37, 0
	s_mov_b32 s33, m0
	s_mov_b32 m0, s62
	s_nop 2
	global_load_lds_dwordx4 v163, s[22:23]
	s_mov_b32 m0, s33
	s_nop 0
	s_mov_b32 s33, m0
	s_mov_b32 m0, s63
	s_nop 2
	global_load_lds_dwordx4 v165, s[22:23]
	s_mov_b32 m0, s33
	s_mov_b32 s22, m0
	s_mov_b32 m0, s60
	s_nop 2
	global_load_lds_dwordx4 v162, s[38:39]
	s_mov_b32 m0, s22
	s_nop 0
	s_mov_b32 s22, m0
	s_mov_b32 m0, s61
	s_nop 2
	global_load_lds_dwordx4 v164, s[38:39]
	s_mov_b32 m0, s22
	s_waitcnt vmcnt(8)
	s_waitcnt lgkmcnt(0)
	s_setprio 1
	s_barrier
	v_mfma_f32_16x16x128_f8f6f4 v[92:95], v[0:7], v[172:179], v[92:95]
	v_mfma_f32_16x16x128_f8f6f4 v[88:91], v[8:15], v[172:179], v[88:91]
	v_mfma_f32_16x16x128_f8f6f4 v[76:79], v[0:7], v[180:187], v[76:79]
	v_mfma_f32_16x16x128_f8f6f4 v[72:75], v[8:15], v[180:187], v[72:75]
	v_mfma_f32_16x16x128_f8f6f4 v[60:63], v[0:7], v[188:195], v[60:63]
	v_mfma_f32_16x16x128_f8f6f4 v[56:59], v[8:15], v[188:195], v[56:59]
	v_mfma_f32_16x16x128_f8f6f4 v[44:47], v[0:7], v[196:203], v[44:47]
	v_mfma_f32_16x16x128_f8f6f4 v[40:43], v[8:15], v[196:203], v[40:43]
	v_mfma_f32_16x16x128_f8f6f4 v[84:87], v[16:23], v[172:179], v[84:87]
	v_mfma_f32_16x16x128_f8f6f4 v[80:83], v[24:31], v[172:179], v[80:83]
	v_mfma_f32_16x16x128_f8f6f4 v[68:71], v[16:23], v[180:187], v[68:71]
	v_mfma_f32_16x16x128_f8f6f4 v[64:67], v[24:31], v[180:187], v[64:67]
	v_mfma_f32_16x16x128_f8f6f4 v[52:55], v[16:23], v[188:195], v[52:55]
	v_mfma_f32_16x16x128_f8f6f4 v[48:51], v[24:31], v[188:195], v[48:51]
	v_mfma_f32_16x16x128_f8f6f4 v[36:39], v[16:23], v[196:203], v[36:39]
	v_mfma_f32_16x16x128_f8f6f4 v[32:35], v[24:31], v[196:203], v[32:35]
	s_setprio 0
	s_barrier
	s_add_i32 s83, s83, 2
	s_add_u32 s81, s81, 0x100
	s_addc_u32 s82, s82, 0
	s_cmp_gt_u32 s83, 5
	s_cbranch_scc1 .LBB0_2130
	s_mov_b64 s[22:23], s[26:27]
	s_cmp_lg_u32 s83, -2
	s_cbranch_scc0 .LBB0_2121
	s_branch .LBB0_2128
